# removed compiler-inserted full VMEM drains in out-proj GEMM K loop and moe-up gather-index load; pipelined adaLN weight loads; EpiQKV table loads ahead of use
# speedup vs baseline: 1.0157x; 1.0157x over previous
.LBB0_57:
	s_add_u32 s40, s6, 0x6000
	s_addc_u32 s41, s7, 0
	s_add_u32 s42, s6, 0xc000
	s_addc_u32 s43, s7, 0
	s_add_u32 s44, s6, 0x12000
	s_addc_u32 s45, s7, 0
	v_lshl_add_u64 v[108:109], v[8:9], 0, s[6:7]
	v_lshl_add_u64 v[110:111], v[8:9], 0, s[40:41]
	v_lshl_add_u64 v[112:113], v[8:9], 0, s[42:43]
	v_lshl_add_u64 v[114:115], v[8:9], 0, s[44:45]
	s_add_u32 s6, s6, 0x18000
	s_addc_u32 s7, s7, 0
	global_load_dword v76, v[108:109], off
	global_load_dword v78, v[110:111], off
	global_load_dword v80, v[112:113], off
	global_load_dword v82, v[114:115], off
	s_add_u32 s40, s6, 0x6000
	s_addc_u32 s41, s7, 0
	s_add_u32 s42, s6, 0xc000
	s_addc_u32 s43, s7, 0
	s_add_u32 s44, s6, 0x12000
	s_addc_u32 s45, s7, 0
	v_lshl_add_u64 v[108:109], v[8:9], 0, s[6:7]
	v_lshl_add_u64 v[110:111], v[8:9], 0, s[40:41]
	v_lshl_add_u64 v[112:113], v[8:9], 0, s[42:43]
	v_lshl_add_u64 v[114:115], v[8:9], 0, s[44:45]
	s_add_u32 s6, s6, 0x18000
	s_addc_u32 s7, s7, 0
	global_load_dword v84, v[108:109], off
	global_load_dword v86, v[110:111], off
	global_load_dword v88, v[112:113], off
	global_load_dword v90, v[114:115], off
	s_add_u32 s40, s6, 0x6000
	s_addc_u32 s41, s7, 0
	s_add_u32 s42, s6, 0xc000
	s_addc_u32 s43, s7, 0
	s_add_u32 s44, s6, 0x12000
	s_addc_u32 s45, s7, 0
	v_lshl_add_u64 v[108:109], v[8:9], 0, s[6:7]
	v_lshl_add_u64 v[110:111], v[8:9], 0, s[40:41]
	v_lshl_add_u64 v[112:113], v[8:9], 0, s[42:43]
	v_lshl_add_u64 v[114:115], v[8:9], 0, s[44:45]
	s_add_u32 s6, s6, 0x18000
	s_addc_u32 s7, s7, 0
	global_load_dword v92, v[108:109], off
	global_load_dword v94, v[110:111], off
	global_load_dword v96, v[112:113], off
	global_load_dword v98, v[114:115], off
	s_mov_b32 s46, 7
.Lada_kloop:
	s_add_u32 s40, s6, 0x6000
	s_addc_u32 s41, s7, 0
	s_add_u32 s42, s6, 0xc000
	s_addc_u32 s43, s7, 0
	s_add_u32 s44, s6, 0x12000
	s_addc_u32 s45, s7, 0
	v_lshl_add_u64 v[108:109], v[8:9], 0, s[6:7]
	v_lshl_add_u64 v[110:111], v[8:9], 0, s[40:41]
	v_lshl_add_u64 v[112:113], v[8:9], 0, s[42:43]
	v_lshl_add_u64 v[114:115], v[8:9], 0, s[44:45]
	s_add_u32 s6, s6, 0x18000
	s_addc_u32 s7, s7, 0
	global_load_dword v100, v[108:109], off
	global_load_dword v102, v[110:111], off
	global_load_dword v104, v[112:113], off
	global_load_dword v106, v[114:115], off
	ds_read_b128 v[24:27], v21 offset:4096
	ds_read_b128 v[28:31], v21 offset:8192
	ds_read_b128 v[32:35], v21 offset:12288
	ds_read_b128 v[36:39], v21 offset:16384
	ds_read_b128 v[40:43], v21 offset:20480
	ds_read_b128 v[44:47], v21 offset:24576
	ds_read_b128 v[48:51], v21 offset:28672
	ds_read_b128 v[52:55], v21
	ds_read_b128 v[56:59], v21 offset:32768
	s_waitcnt lgkmcnt(0)
	v_mov_b32_e32 v69, v24
	v_mov_b32_e32 v70, v28
	v_mov_b32_e32 v71, v32
	v_mov_b32_e32 v68, v52
	v_mov_b32_e32 v72, v36
	v_mov_b32_e32 v73, v40
	v_mov_b32_e32 v74, v44
	v_mov_b32_e32 v75, v48
	v_mov_b32_e32 v24, v53
	v_mov_b32_e32 v32, v29
	v_mov_b32_e32 v40, v37
	v_mov_b32_e32 v48, v45
	v_mov_b32_e32 v28, v54
	v_mov_b32_e32 v29, v26
	v_mov_b32_e32 v36, v30
	v_mov_b32_e32 v37, v34
	v_mov_b32_e32 v44, v38
	v_mov_b32_e32 v45, v42
	v_mov_b32_e32 v52, v46
	v_mov_b32_e32 v53, v50
	v_mov_b32_e32 v26, v55
	v_mov_b32_e32 v34, v31
	v_mov_b32_e32 v42, v39
	v_mov_b32_e32 v50, v47
	v_add_u32_e32 v21, 16, v21
	s_waitcnt vmcnt(12)
	v_pk_fma_f32 v[10:11], v[76:77], v[68:69], v[10:11] op_sel_hi:[0,1,1]
	v_pk_fma_f32 v[12:13], v[76:77], v[70:71], v[12:13] op_sel_hi:[0,1,1]
	v_pk_fma_f32 v[14:15], v[76:77], v[72:73], v[14:15] op_sel_hi:[0,1,1]
	v_pk_fma_f32 v[16:17], v[76:77], v[74:75], v[16:17] op_sel_hi:[0,1,1]
	v_fmac_f32_e32 v22, v76, v56
	v_pk_fma_f32 v[10:11], v[78:79], v[24:25], v[10:11] op_sel_hi:[0,1,1]
	v_pk_fma_f32 v[12:13], v[78:79], v[32:33], v[12:13] op_sel_hi:[0,1,1]
	v_pk_fma_f32 v[14:15], v[78:79], v[40:41], v[14:15] op_sel_hi:[0,1,1]
	v_pk_fma_f32 v[16:17], v[78:79], v[48:49], v[16:17] op_sel_hi:[0,1,1]
	v_fmac_f32_e32 v22, v78, v57
	v_pk_fma_f32 v[10:11], v[80:81], v[28:29], v[10:11] op_sel_hi:[0,1,1]
	v_pk_fma_f32 v[12:13], v[80:81], v[36:37], v[12:13] op_sel_hi:[0,1,1]
	v_pk_fma_f32 v[14:15], v[80:81], v[44:45], v[14:15] op_sel_hi:[0,1,1]
	v_pk_fma_f32 v[16:17], v[80:81], v[52:53], v[16:17] op_sel_hi:[0,1,1]
	v_fmac_f32_e32 v22, v80, v58
	v_pk_fma_f32 v[10:11], v[82:83], v[26:27], v[10:11] op_sel_hi:[0,1,1]
	v_pk_fma_f32 v[12:13], v[82:83], v[34:35], v[12:13] op_sel_hi:[0,1,1]
	v_pk_fma_f32 v[14:15], v[82:83], v[42:43], v[14:15] op_sel_hi:[0,1,1]
	v_pk_fma_f32 v[16:17], v[82:83], v[50:51], v[16:17] op_sel_hi:[0,1,1]
	v_fmac_f32_e32 v22, v82, v59
	s_add_u32 s40, s6, 0x6000
	s_addc_u32 s41, s7, 0
	s_add_u32 s42, s6, 0xc000
	s_addc_u32 s43, s7, 0
	s_add_u32 s44, s6, 0x12000
	s_addc_u32 s45, s7, 0
	v_lshl_add_u64 v[108:109], v[8:9], 0, s[6:7]
	v_lshl_add_u64 v[110:111], v[8:9], 0, s[40:41]
	v_lshl_add_u64 v[112:113], v[8:9], 0, s[42:43]
	v_lshl_add_u64 v[114:115], v[8:9], 0, s[44:45]
	s_add_u32 s6, s6, 0x18000
	s_addc_u32 s7, s7, 0
	global_load_dword v76, v[108:109], off
	global_load_dword v78, v[110:111], off
	global_load_dword v80, v[112:113], off
	global_load_dword v82, v[114:115], off
	ds_read_b128 v[24:27], v21 offset:4096
	ds_read_b128 v[28:31], v21 offset:8192
	ds_read_b128 v[32:35], v21 offset:12288
	ds_read_b128 v[36:39], v21 offset:16384
	ds_read_b128 v[40:43], v21 offset:20480
	ds_read_b128 v[44:47], v21 offset:24576
	ds_read_b128 v[48:51], v21 offset:28672
	ds_read_b128 v[52:55], v21
	ds_read_b128 v[56:59], v21 offset:32768
	s_waitcnt lgkmcnt(0)
	v_mov_b32_e32 v69, v24
	v_mov_b32_e32 v70, v28
	v_mov_b32_e32 v71, v32
	v_mov_b32_e32 v68, v52
	v_mov_b32_e32 v72, v36
	v_mov_b32_e32 v73, v40
	v_mov_b32_e32 v74, v44
	v_mov_b32_e32 v75, v48
	v_mov_b32_e32 v24, v53
	v_mov_b32_e32 v32, v29
	v_mov_b32_e32 v40, v37
	v_mov_b32_e32 v48, v45
	v_mov_b32_e32 v28, v54
	v_mov_b32_e32 v29, v26
	v_mov_b32_e32 v36, v30
	v_mov_b32_e32 v37, v34
	v_mov_b32_e32 v44, v38
	v_mov_b32_e32 v45, v42
	v_mov_b32_e32 v52, v46
	v_mov_b32_e32 v53, v50
	v_mov_b32_e32 v26, v55
	v_mov_b32_e32 v34, v31
	v_mov_b32_e32 v42, v39
	v_mov_b32_e32 v50, v47
	v_add_u32_e32 v21, 16, v21
	s_waitcnt vmcnt(12)
	v_pk_fma_f32 v[10:11], v[84:85], v[68:69], v[10:11] op_sel_hi:[0,1,1]
	v_pk_fma_f32 v[12:13], v[84:85], v[70:71], v[12:13] op_sel_hi:[0,1,1]
	v_pk_fma_f32 v[14:15], v[84:85], v[72:73], v[14:15] op_sel_hi:[0,1,1]
	v_pk_fma_f32 v[16:17], v[84:85], v[74:75], v[16:17] op_sel_hi:[0,1,1]
	v_fmac_f32_e32 v22, v84, v56
	v_pk_fma_f32 v[10:11], v[86:87], v[24:25], v[10:11] op_sel_hi:[0,1,1]
	v_pk_fma_f32 v[12:13], v[86:87], v[32:33], v[12:13] op_sel_hi:[0,1,1]
	v_pk_fma_f32 v[14:15], v[86:87], v[40:41], v[14:15] op_sel_hi:[0,1,1]
	v_pk_fma_f32 v[16:17], v[86:87], v[48:49], v[16:17] op_sel_hi:[0,1,1]
	v_fmac_f32_e32 v22, v86, v57
	v_pk_fma_f32 v[10:11], v[88:89], v[28:29], v[10:11] op_sel_hi:[0,1,1]
	v_pk_fma_f32 v[12:13], v[88:89], v[36:37], v[12:13] op_sel_hi:[0,1,1]
	v_pk_fma_f32 v[14:15], v[88:89], v[44:45], v[14:15] op_sel_hi:[0,1,1]
	v_pk_fma_f32 v[16:17], v[88:89], v[52:53], v[16:17] op_sel_hi:[0,1,1]
	v_fmac_f32_e32 v22, v88, v58
	v_pk_fma_f32 v[10:11], v[90:91], v[26:27], v[10:11] op_sel_hi:[0,1,1]
	v_pk_fma_f32 v[12:13], v[90:91], v[34:35], v[12:13] op_sel_hi:[0,1,1]
	v_pk_fma_f32 v[14:15], v[90:91], v[42:43], v[14:15] op_sel_hi:[0,1,1]
	v_pk_fma_f32 v[16:17], v[90:91], v[50:51], v[16:17] op_sel_hi:[0,1,1]
	v_fmac_f32_e32 v22, v90, v59
	s_add_u32 s40, s6, 0x6000
	s_addc_u32 s41, s7, 0
	s_add_u32 s42, s6, 0xc000
	s_addc_u32 s43, s7, 0
	s_add_u32 s44, s6, 0x12000
	s_addc_u32 s45, s7, 0
	v_lshl_add_u64 v[108:109], v[8:9], 0, s[6:7]
	v_lshl_add_u64 v[110:111], v[8:9], 0, s[40:41]
	v_lshl_add_u64 v[112:113], v[8:9], 0, s[42:43]
	v_lshl_add_u64 v[114:115], v[8:9], 0, s[44:45]
	s_add_u32 s6, s6, 0x18000
	s_addc_u32 s7, s7, 0
	global_load_dword v84, v[108:109], off
	global_load_dword v86, v[110:111], off
	global_load_dword v88, v[112:113], off
	global_load_dword v90, v[114:115], off
	ds_read_b128 v[24:27], v21 offset:4096
	ds_read_b128 v[28:31], v21 offset:8192
	ds_read_b128 v[32:35], v21 offset:12288
	ds_read_b128 v[36:39], v21 offset:16384
	ds_read_b128 v[40:43], v21 offset:20480
	ds_read_b128 v[44:47], v21 offset:24576
	ds_read_b128 v[48:51], v21 offset:28672
	ds_read_b128 v[52:55], v21
	ds_read_b128 v[56:59], v21 offset:32768
	s_waitcnt lgkmcnt(0)
	v_mov_b32_e32 v69, v24
	v_mov_b32_e32 v70, v28
	v_mov_b32_e32 v71, v32
	v_mov_b32_e32 v68, v52
	v_mov_b32_e32 v72, v36
	v_mov_b32_e32 v73, v40
	v_mov_b32_e32 v74, v44
	v_mov_b32_e32 v75, v48
	v_mov_b32_e32 v24, v53
	v_mov_b32_e32 v32, v29
	v_mov_b32_e32 v40, v37
	v_mov_b32_e32 v48, v45
	v_mov_b32_e32 v28, v54
	v_mov_b32_e32 v29, v26
	v_mov_b32_e32 v36, v30
	v_mov_b32_e32 v37, v34
	v_mov_b32_e32 v44, v38
	v_mov_b32_e32 v45, v42
	v_mov_b32_e32 v52, v46
	v_mov_b32_e32 v53, v50
	v_mov_b32_e32 v26, v55
	v_mov_b32_e32 v34, v31
	v_mov_b32_e32 v42, v39
	v_mov_b32_e32 v50, v47
	v_add_u32_e32 v21, 16, v21
	s_waitcnt vmcnt(12)
	v_pk_fma_f32 v[10:11], v[92:93], v[68:69], v[10:11] op_sel_hi:[0,1,1]
	v_pk_fma_f32 v[12:13], v[92:93], v[70:71], v[12:13] op_sel_hi:[0,1,1]
	v_pk_fma_f32 v[14:15], v[92:93], v[72:73], v[14:15] op_sel_hi:[0,1,1]
	v_pk_fma_f32 v[16:17], v[92:93], v[74:75], v[16:17] op_sel_hi:[0,1,1]
	v_fmac_f32_e32 v22, v92, v56
	v_pk_fma_f32 v[10:11], v[94:95], v[24:25], v[10:11] op_sel_hi:[0,1,1]
	v_pk_fma_f32 v[12:13], v[94:95], v[32:33], v[12:13] op_sel_hi:[0,1,1]
	v_pk_fma_f32 v[14:15], v[94:95], v[40:41], v[14:15] op_sel_hi:[0,1,1]
	v_pk_fma_f32 v[16:17], v[94:95], v[48:49], v[16:17] op_sel_hi:[0,1,1]
	v_fmac_f32_e32 v22, v94, v57
	v_pk_fma_f32 v[10:11], v[96:97], v[28:29], v[10:11] op_sel_hi:[0,1,1]
	v_pk_fma_f32 v[12:13], v[96:97], v[36:37], v[12:13] op_sel_hi:[0,1,1]
	v_pk_fma_f32 v[14:15], v[96:97], v[44:45], v[14:15] op_sel_hi:[0,1,1]
	v_pk_fma_f32 v[16:17], v[96:97], v[52:53], v[16:17] op_sel_hi:[0,1,1]
	v_fmac_f32_e32 v22, v96, v58
	v_pk_fma_f32 v[10:11], v[98:99], v[26:27], v[10:11] op_sel_hi:[0,1,1]
	v_pk_fma_f32 v[12:13], v[98:99], v[34:35], v[12:13] op_sel_hi:[0,1,1]
	v_pk_fma_f32 v[14:15], v[98:99], v[42:43], v[14:15] op_sel_hi:[0,1,1]
	v_pk_fma_f32 v[16:17], v[98:99], v[50:51], v[16:17] op_sel_hi:[0,1,1]
	v_fmac_f32_e32 v22, v98, v59
	s_add_u32 s40, s6, 0x6000
	s_addc_u32 s41, s7, 0
	s_add_u32 s42, s6, 0xc000
	s_addc_u32 s43, s7, 0
	s_add_u32 s44, s6, 0x12000
	s_addc_u32 s45, s7, 0
	v_lshl_add_u64 v[108:109], v[8:9], 0, s[6:7]
	v_lshl_add_u64 v[110:111], v[8:9], 0, s[40:41]
	v_lshl_add_u64 v[112:113], v[8:9], 0, s[42:43]
	v_lshl_add_u64 v[114:115], v[8:9], 0, s[44:45]
	s_add_u32 s6, s6, 0x18000
	s_addc_u32 s7, s7, 0
	global_load_dword v92, v[108:109], off
	global_load_dword v94, v[110:111], off
	global_load_dword v96, v[112:113], off
	global_load_dword v98, v[114:115], off
	ds_read_b128 v[24:27], v21 offset:4096
	ds_read_b128 v[28:31], v21 offset:8192
	ds_read_b128 v[32:35], v21 offset:12288
	ds_read_b128 v[36:39], v21 offset:16384
	ds_read_b128 v[40:43], v21 offset:20480
	ds_read_b128 v[44:47], v21 offset:24576
	ds_read_b128 v[48:51], v21 offset:28672
	ds_read_b128 v[52:55], v21
	ds_read_b128 v[56:59], v21 offset:32768
	s_waitcnt lgkmcnt(0)
	v_mov_b32_e32 v69, v24
	v_mov_b32_e32 v70, v28
	v_mov_b32_e32 v71, v32
	v_mov_b32_e32 v68, v52
	v_mov_b32_e32 v72, v36
	v_mov_b32_e32 v73, v40
	v_mov_b32_e32 v74, v44
	v_mov_b32_e32 v75, v48
	v_mov_b32_e32 v24, v53
	v_mov_b32_e32 v32, v29
	v_mov_b32_e32 v40, v37
	v_mov_b32_e32 v48, v45
	v_mov_b32_e32 v28, v54
	v_mov_b32_e32 v29, v26
	v_mov_b32_e32 v36, v30
	v_mov_b32_e32 v37, v34
	v_mov_b32_e32 v44, v38
	v_mov_b32_e32 v45, v42
	v_mov_b32_e32 v52, v46
	v_mov_b32_e32 v53, v50
	v_mov_b32_e32 v26, v55
	v_mov_b32_e32 v34, v31
	v_mov_b32_e32 v42, v39
	v_mov_b32_e32 v50, v47
	v_add_u32_e32 v21, 16, v21
	s_waitcnt vmcnt(12)
	v_pk_fma_f32 v[10:11], v[100:101], v[68:69], v[10:11] op_sel_hi:[0,1,1]
	v_pk_fma_f32 v[12:13], v[100:101], v[70:71], v[12:13] op_sel_hi:[0,1,1]
	v_pk_fma_f32 v[14:15], v[100:101], v[72:73], v[14:15] op_sel_hi:[0,1,1]
	v_pk_fma_f32 v[16:17], v[100:101], v[74:75], v[16:17] op_sel_hi:[0,1,1]
	v_fmac_f32_e32 v22, v100, v56
	v_pk_fma_f32 v[10:11], v[102:103], v[24:25], v[10:11] op_sel_hi:[0,1,1]
	v_pk_fma_f32 v[12:13], v[102:103], v[32:33], v[12:13] op_sel_hi:[0,1,1]
	v_pk_fma_f32 v[14:15], v[102:103], v[40:41], v[14:15] op_sel_hi:[0,1,1]
	v_pk_fma_f32 v[16:17], v[102:103], v[48:49], v[16:17] op_sel_hi:[0,1,1]
	v_fmac_f32_e32 v22, v102, v57
	v_pk_fma_f32 v[10:11], v[104:105], v[28:29], v[10:11] op_sel_hi:[0,1,1]
	v_pk_fma_f32 v[12:13], v[104:105], v[36:37], v[12:13] op_sel_hi:[0,1,1]
	v_pk_fma_f32 v[14:15], v[104:105], v[44:45], v[14:15] op_sel_hi:[0,1,1]
	v_pk_fma_f32 v[16:17], v[104:105], v[52:53], v[16:17] op_sel_hi:[0,1,1]
	v_fmac_f32_e32 v22, v104, v58
	v_pk_fma_f32 v[10:11], v[106:107], v[26:27], v[10:11] op_sel_hi:[0,1,1]
	v_pk_fma_f32 v[12:13], v[106:107], v[34:35], v[12:13] op_sel_hi:[0,1,1]
	v_pk_fma_f32 v[14:15], v[106:107], v[42:43], v[14:15] op_sel_hi:[0,1,1]
	v_pk_fma_f32 v[16:17], v[106:107], v[50:51], v[16:17] op_sel_hi:[0,1,1]
	v_fmac_f32_e32 v22, v106, v59
	s_add_i32 s46, s46, -1
	s_cmp_lg_u32 s46, 0
	s_cbranch_scc1 .Lada_kloop
	s_add_u32 s40, s6, 0x6000
	s_addc_u32 s41, s7, 0
	s_add_u32 s42, s6, 0xc000
	s_addc_u32 s43, s7, 0
	s_add_u32 s44, s6, 0x12000
	s_addc_u32 s45, s7, 0
	v_lshl_add_u64 v[108:109], v[8:9], 0, s[6:7]
	v_lshl_add_u64 v[110:111], v[8:9], 0, s[40:41]
	v_lshl_add_u64 v[112:113], v[8:9], 0, s[42:43]
	v_lshl_add_u64 v[114:115], v[8:9], 0, s[44:45]
	s_add_u32 s6, s6, 0x18000
	s_addc_u32 s7, s7, 0
	global_load_dword v100, v[108:109], off
	global_load_dword v102, v[110:111], off
	global_load_dword v104, v[112:113], off
	global_load_dword v106, v[114:115], off
	ds_read_b128 v[24:27], v21 offset:4096
	ds_read_b128 v[28:31], v21 offset:8192
	ds_read_b128 v[32:35], v21 offset:12288
	ds_read_b128 v[36:39], v21 offset:16384
	ds_read_b128 v[40:43], v21 offset:20480
	ds_read_b128 v[44:47], v21 offset:24576
	ds_read_b128 v[48:51], v21 offset:28672
	ds_read_b128 v[52:55], v21
	ds_read_b128 v[56:59], v21 offset:32768
	s_waitcnt lgkmcnt(0)
	v_mov_b32_e32 v69, v24
	v_mov_b32_e32 v70, v28
	v_mov_b32_e32 v71, v32
	v_mov_b32_e32 v68, v52
	v_mov_b32_e32 v72, v36
	v_mov_b32_e32 v73, v40
	v_mov_b32_e32 v74, v44
	v_mov_b32_e32 v75, v48
	v_mov_b32_e32 v24, v53
	v_mov_b32_e32 v32, v29
	v_mov_b32_e32 v40, v37
	v_mov_b32_e32 v48, v45
	v_mov_b32_e32 v28, v54
	v_mov_b32_e32 v29, v26
	v_mov_b32_e32 v36, v30
	v_mov_b32_e32 v37, v34
	v_mov_b32_e32 v44, v38
	v_mov_b32_e32 v45, v42
	v_mov_b32_e32 v52, v46
	v_mov_b32_e32 v53, v50
	v_mov_b32_e32 v26, v55
	v_mov_b32_e32 v34, v31
	v_mov_b32_e32 v42, v39
	v_mov_b32_e32 v50, v47
	v_add_u32_e32 v21, 16, v21
	s_waitcnt vmcnt(12)
	v_pk_fma_f32 v[10:11], v[76:77], v[68:69], v[10:11] op_sel_hi:[0,1,1]
	v_pk_fma_f32 v[12:13], v[76:77], v[70:71], v[12:13] op_sel_hi:[0,1,1]
	v_pk_fma_f32 v[14:15], v[76:77], v[72:73], v[14:15] op_sel_hi:[0,1,1]
	v_pk_fma_f32 v[16:17], v[76:77], v[74:75], v[16:17] op_sel_hi:[0,1,1]
	v_fmac_f32_e32 v22, v76, v56
	v_pk_fma_f32 v[10:11], v[78:79], v[24:25], v[10:11] op_sel_hi:[0,1,1]
	v_pk_fma_f32 v[12:13], v[78:79], v[32:33], v[12:13] op_sel_hi:[0,1,1]
	v_pk_fma_f32 v[14:15], v[78:79], v[40:41], v[14:15] op_sel_hi:[0,1,1]
	v_pk_fma_f32 v[16:17], v[78:79], v[48:49], v[16:17] op_sel_hi:[0,1,1]
	v_fmac_f32_e32 v22, v78, v57
	v_pk_fma_f32 v[10:11], v[80:81], v[28:29], v[10:11] op_sel_hi:[0,1,1]
	v_pk_fma_f32 v[12:13], v[80:81], v[36:37], v[12:13] op_sel_hi:[0,1,1]
	v_pk_fma_f32 v[14:15], v[80:81], v[44:45], v[14:15] op_sel_hi:[0,1,1]
	v_pk_fma_f32 v[16:17], v[80:81], v[52:53], v[16:17] op_sel_hi:[0,1,1]
	v_fmac_f32_e32 v22, v80, v58
	v_pk_fma_f32 v[10:11], v[82:83], v[26:27], v[10:11] op_sel_hi:[0,1,1]
	v_pk_fma_f32 v[12:13], v[82:83], v[34:35], v[12:13] op_sel_hi:[0,1,1]
	v_pk_fma_f32 v[14:15], v[82:83], v[42:43], v[14:15] op_sel_hi:[0,1,1]
	v_pk_fma_f32 v[16:17], v[82:83], v[50:51], v[16:17] op_sel_hi:[0,1,1]
	v_fmac_f32_e32 v22, v82, v59
	ds_read_b128 v[24:27], v21 offset:4096
	ds_read_b128 v[28:31], v21 offset:8192
	ds_read_b128 v[32:35], v21 offset:12288
	ds_read_b128 v[36:39], v21 offset:16384
	ds_read_b128 v[40:43], v21 offset:20480
	ds_read_b128 v[44:47], v21 offset:24576
	ds_read_b128 v[48:51], v21 offset:28672
	ds_read_b128 v[52:55], v21
	ds_read_b128 v[56:59], v21 offset:32768
	s_waitcnt lgkmcnt(0)
	v_mov_b32_e32 v69, v24
	v_mov_b32_e32 v70, v28
	v_mov_b32_e32 v71, v32
	v_mov_b32_e32 v68, v52
	v_mov_b32_e32 v72, v36
	v_mov_b32_e32 v73, v40
	v_mov_b32_e32 v74, v44
	v_mov_b32_e32 v75, v48
	v_mov_b32_e32 v24, v53
	v_mov_b32_e32 v32, v29
	v_mov_b32_e32 v40, v37
	v_mov_b32_e32 v48, v45
	v_mov_b32_e32 v28, v54
	v_mov_b32_e32 v29, v26
	v_mov_b32_e32 v36, v30
	v_mov_b32_e32 v37, v34
	v_mov_b32_e32 v44, v38
	v_mov_b32_e32 v45, v42
	v_mov_b32_e32 v52, v46
	v_mov_b32_e32 v53, v50
	v_mov_b32_e32 v26, v55
	v_mov_b32_e32 v34, v31
	v_mov_b32_e32 v42, v39
	v_mov_b32_e32 v50, v47
	v_add_u32_e32 v21, 16, v21
	s_waitcnt vmcnt(8)
	v_pk_fma_f32 v[10:11], v[84:85], v[68:69], v[10:11] op_sel_hi:[0,1,1]
	v_pk_fma_f32 v[12:13], v[84:85], v[70:71], v[12:13] op_sel_hi:[0,1,1]
	v_pk_fma_f32 v[14:15], v[84:85], v[72:73], v[14:15] op_sel_hi:[0,1,1]
	v_pk_fma_f32 v[16:17], v[84:85], v[74:75], v[16:17] op_sel_hi:[0,1,1]
	v_fmac_f32_e32 v22, v84, v56
	v_pk_fma_f32 v[10:11], v[86:87], v[24:25], v[10:11] op_sel_hi:[0,1,1]
	v_pk_fma_f32 v[12:13], v[86:87], v[32:33], v[12:13] op_sel_hi:[0,1,1]
	v_pk_fma_f32 v[14:15], v[86:87], v[40:41], v[14:15] op_sel_hi:[0,1,1]
	v_pk_fma_f32 v[16:17], v[86:87], v[48:49], v[16:17] op_sel_hi:[0,1,1]
	v_fmac_f32_e32 v22, v86, v57
	v_pk_fma_f32 v[10:11], v[88:89], v[28:29], v[10:11] op_sel_hi:[0,1,1]
	v_pk_fma_f32 v[12:13], v[88:89], v[36:37], v[12:13] op_sel_hi:[0,1,1]
	v_pk_fma_f32 v[14:15], v[88:89], v[44:45], v[14:15] op_sel_hi:[0,1,1]
	v_pk_fma_f32 v[16:17], v[88:89], v[52:53], v[16:17] op_sel_hi:[0,1,1]
	v_fmac_f32_e32 v22, v88, v58
	v_pk_fma_f32 v[10:11], v[90:91], v[26:27], v[10:11] op_sel_hi:[0,1,1]
	v_pk_fma_f32 v[12:13], v[90:91], v[34:35], v[12:13] op_sel_hi:[0,1,1]
	v_pk_fma_f32 v[14:15], v[90:91], v[42:43], v[14:15] op_sel_hi:[0,1,1]
	v_pk_fma_f32 v[16:17], v[90:91], v[50:51], v[16:17] op_sel_hi:[0,1,1]
	v_fmac_f32_e32 v22, v90, v59
	ds_read_b128 v[24:27], v21 offset:4096
	ds_read_b128 v[28:31], v21 offset:8192
	ds_read_b128 v[32:35], v21 offset:12288
	ds_read_b128 v[36:39], v21 offset:16384
	ds_read_b128 v[40:43], v21 offset:20480
	ds_read_b128 v[44:47], v21 offset:24576
	ds_read_b128 v[48:51], v21 offset:28672
	ds_read_b128 v[52:55], v21
	ds_read_b128 v[56:59], v21 offset:32768
	s_waitcnt lgkmcnt(0)
	v_mov_b32_e32 v69, v24
	v_mov_b32_e32 v70, v28
	v_mov_b32_e32 v71, v32
	v_mov_b32_e32 v68, v52
	v_mov_b32_e32 v72, v36
	v_mov_b32_e32 v73, v40
	v_mov_b32_e32 v74, v44
	v_mov_b32_e32 v75, v48
	v_mov_b32_e32 v24, v53
	v_mov_b32_e32 v32, v29
	v_mov_b32_e32 v40, v37
	v_mov_b32_e32 v48, v45
	v_mov_b32_e32 v28, v54
	v_mov_b32_e32 v29, v26
	v_mov_b32_e32 v36, v30
	v_mov_b32_e32 v37, v34
	v_mov_b32_e32 v44, v38
	v_mov_b32_e32 v45, v42
	v_mov_b32_e32 v52, v46
	v_mov_b32_e32 v53, v50
	v_mov_b32_e32 v26, v55
	v_mov_b32_e32 v34, v31
	v_mov_b32_e32 v42, v39
	v_mov_b32_e32 v50, v47
	v_add_u32_e32 v21, 16, v21
	s_waitcnt vmcnt(4)
	v_pk_fma_f32 v[10:11], v[92:93], v[68:69], v[10:11] op_sel_hi:[0,1,1]
	v_pk_fma_f32 v[12:13], v[92:93], v[70:71], v[12:13] op_sel_hi:[0,1,1]
	v_pk_fma_f32 v[14:15], v[92:93], v[72:73], v[14:15] op_sel_hi:[0,1,1]
	v_pk_fma_f32 v[16:17], v[92:93], v[74:75], v[16:17] op_sel_hi:[0,1,1]
	v_fmac_f32_e32 v22, v92, v56
	v_pk_fma_f32 v[10:11], v[94:95], v[24:25], v[10:11] op_sel_hi:[0,1,1]
	v_pk_fma_f32 v[12:13], v[94:95], v[32:33], v[12:13] op_sel_hi:[0,1,1]
	v_pk_fma_f32 v[14:15], v[94:95], v[40:41], v[14:15] op_sel_hi:[0,1,1]
	v_pk_fma_f32 v[16:17], v[94:95], v[48:49], v[16:17] op_sel_hi:[0,1,1]
	v_fmac_f32_e32 v22, v94, v57
	v_pk_fma_f32 v[10:11], v[96:97], v[28:29], v[10:11] op_sel_hi:[0,1,1]
	v_pk_fma_f32 v[12:13], v[96:97], v[36:37], v[12:13] op_sel_hi:[0,1,1]
	v_pk_fma_f32 v[14:15], v[96:97], v[44:45], v[14:15] op_sel_hi:[0,1,1]
	v_pk_fma_f32 v[16:17], v[96:97], v[52:53], v[16:17] op_sel_hi:[0,1,1]
	v_fmac_f32_e32 v22, v96, v58
	v_pk_fma_f32 v[10:11], v[98:99], v[26:27], v[10:11] op_sel_hi:[0,1,1]
	v_pk_fma_f32 v[12:13], v[98:99], v[34:35], v[12:13] op_sel_hi:[0,1,1]
	v_pk_fma_f32 v[14:15], v[98:99], v[42:43], v[14:15] op_sel_hi:[0,1,1]
	v_pk_fma_f32 v[16:17], v[98:99], v[50:51], v[16:17] op_sel_hi:[0,1,1]
	v_fmac_f32_e32 v22, v98, v59
	ds_read_b128 v[24:27], v21 offset:4096
	ds_read_b128 v[28:31], v21 offset:8192
	ds_read_b128 v[32:35], v21 offset:12288
	ds_read_b128 v[36:39], v21 offset:16384
	ds_read_b128 v[40:43], v21 offset:20480
	ds_read_b128 v[44:47], v21 offset:24576
	ds_read_b128 v[48:51], v21 offset:28672
	ds_read_b128 v[52:55], v21
	ds_read_b128 v[56:59], v21 offset:32768
	s_waitcnt lgkmcnt(0)
	v_mov_b32_e32 v69, v24
	v_mov_b32_e32 v70, v28
	v_mov_b32_e32 v71, v32
	v_mov_b32_e32 v68, v52
	v_mov_b32_e32 v72, v36
	v_mov_b32_e32 v73, v40
	v_mov_b32_e32 v74, v44
	v_mov_b32_e32 v75, v48
	v_mov_b32_e32 v24, v53
	v_mov_b32_e32 v32, v29
	v_mov_b32_e32 v40, v37
	v_mov_b32_e32 v48, v45
	v_mov_b32_e32 v28, v54
	v_mov_b32_e32 v29, v26
	v_mov_b32_e32 v36, v30
	v_mov_b32_e32 v37, v34
	v_mov_b32_e32 v44, v38
	v_mov_b32_e32 v45, v42
	v_mov_b32_e32 v52, v46
	v_mov_b32_e32 v53, v50
	v_mov_b32_e32 v26, v55
	v_mov_b32_e32 v34, v31
	v_mov_b32_e32 v42, v39
	v_mov_b32_e32 v50, v47
	v_add_u32_e32 v21, 16, v21
	s_waitcnt vmcnt(0)
	v_pk_fma_f32 v[10:11], v[100:101], v[68:69], v[10:11] op_sel_hi:[0,1,1]
	v_pk_fma_f32 v[12:13], v[100:101], v[70:71], v[12:13] op_sel_hi:[0,1,1]
	v_pk_fma_f32 v[14:15], v[100:101], v[72:73], v[14:15] op_sel_hi:[0,1,1]
	v_pk_fma_f32 v[16:17], v[100:101], v[74:75], v[16:17] op_sel_hi:[0,1,1]
	v_fmac_f32_e32 v22, v100, v56
	v_pk_fma_f32 v[10:11], v[102:103], v[24:25], v[10:11] op_sel_hi:[0,1,1]
	v_pk_fma_f32 v[12:13], v[102:103], v[32:33], v[12:13] op_sel_hi:[0,1,1]
	v_pk_fma_f32 v[14:15], v[102:103], v[40:41], v[14:15] op_sel_hi:[0,1,1]
	v_pk_fma_f32 v[16:17], v[102:103], v[48:49], v[16:17] op_sel_hi:[0,1,1]
	v_fmac_f32_e32 v22, v102, v57
	v_pk_fma_f32 v[10:11], v[104:105], v[28:29], v[10:11] op_sel_hi:[0,1,1]
	v_pk_fma_f32 v[12:13], v[104:105], v[36:37], v[12:13] op_sel_hi:[0,1,1]
	v_pk_fma_f32 v[14:15], v[104:105], v[44:45], v[14:15] op_sel_hi:[0,1,1]
	v_pk_fma_f32 v[16:17], v[104:105], v[52:53], v[16:17] op_sel_hi:[0,1,1]
	v_fmac_f32_e32 v22, v104, v58
	v_pk_fma_f32 v[10:11], v[106:107], v[26:27], v[10:11] op_sel_hi:[0,1,1]
	v_pk_fma_f32 v[12:13], v[106:107], v[34:35], v[12:13] op_sel_hi:[0,1,1]
	v_pk_fma_f32 v[14:15], v[106:107], v[42:43], v[14:15] op_sel_hi:[0,1,1]
	v_pk_fma_f32 v[16:17], v[106:107], v[50:51], v[16:17] op_sel_hi:[0,1,1]
	v_fmac_f32_e32 v22, v106, v59
	ds_write2st64_b32 v20, v10, v11 offset0:144 offset1:145
	ds_write2st64_b32 v20, v12, v13 offset0:146 offset1:147
	ds_write2st64_b32 v20, v14, v15 offset0:148 offset1:149
	ds_write2st64_b32 v20, v16, v17 offset0:150 offset1:151
	ds_write_b32 v20, v22 offset:38912
	s_waitcnt lgkmcnt(0)
	s_barrier
	s_and_saveexec_b64 s[6:7], s[0:1]
	s_cbranch_execz .LBB0_55
	v_and_b32_e32 v10, 0x3ff, v6
	s_ashr_i32 s16, s9, 4
	s_mul_i32 s9, s8, 0x1800
	v_lshl_or_b32 v10, s8, 10, v10
	v_add_u32_e32 v8, s9, v6
	v_readlane_b32 s40, v253, 34
	v_ashrrev_i32_e32 v11, 31, v10
	v_ashrrev_i32_e32 v9, 31, v8
	v_readlane_b32 s50, v253, 44
	v_readlane_b32 s51, v253, 45
	v_readlane_b32 s52, v253, 46
	v_readlane_b32 s53, v253, 47
	v_readlane_b32 s54, v253, 48
	v_readlane_b32 s55, v253, 49
	v_lshlrev_b64 v[12:13], 2, v[10:11]
	s_mul_i32 s17, s8, 9
	v_lshl_add_u64 v[8:9], v[8:9], 2, s[50:51]
	v_lshl_add_u64 v[10:11], s[54:55], 0, v[12:13]
	v_lshl_add_u64 v[12:13], s[52:53], 0, v[12:13]
	v_lshl_add_u64 v[6:7], v[6:7], 2, s[4:5]
	s_mov_b64 s[8:9], 0
	v_mov_b32_e32 v14, v2
	v_readlane_b32 s41, v253, 35
	v_readlane_b32 s42, v253, 36
	v_readlane_b32 s43, v253, 37
	v_readlane_b32 s44, v253, 38
	v_readlane_b32 s45, v253, 39
	v_readlane_b32 s46, v253, 40
	v_readlane_b32 s47, v253, 41
	v_readlane_b32 s48, v253, 42
	v_readlane_b32 s49, v253, 43
	s_branch .LBB0_62

.LBB0_308:
	v_mov_b32_e32 v0, 0
	s_mov_b32 s17, -2
	s_mov_b64 s[2:3], 0
	v_mov_b32_e32 v1, v0
	v_mov_b64_e32 v[2:3], v[0:1]
	v_mov_b64_e32 v[4:5], v[0:1]
	v_mov_b64_e32 v[6:7], v[0:1]
	v_mov_b64_e32 v[8:9], v[0:1]
	v_mov_b64_e32 v[10:11], v[0:1]
	v_mov_b64_e32 v[12:13], v[0:1]
	v_mov_b64_e32 v[14:15], v[0:1]
	v_mov_b64_e32 v[16:17], v[0:1]
	v_mov_b64_e32 v[18:19], v[0:1]
	v_mov_b64_e32 v[20:21], v[0:1]
	v_mov_b64_e32 v[22:23], v[0:1]
	v_mov_b64_e32 v[24:25], v[0:1]
	v_mov_b64_e32 v[26:27], v[0:1]
	s_waitcnt lgkmcnt(0)
	v_mov_b64_e32 v[28:29], v[0:1]
	v_mov_b64_e32 v[30:31], v[0:1]
	v_mov_b64_e32 v[32:33], v[0:1]
	v_mov_b64_e32 v[34:35], v[0:1]
	v_mov_b64_e32 v[36:37], v[0:1]
	v_mov_b64_e32 v[38:39], v[0:1]
	v_mov_b64_e32 v[40:41], v[0:1]
	v_mov_b64_e32 v[42:43], v[0:1]
	v_mov_b64_e32 v[44:45], v[0:1]
	v_mov_b64_e32 v[46:47], v[0:1]
	v_mov_b64_e32 v[48:49], v[0:1]
	v_mov_b64_e32 v[50:51], v[0:1]
	v_mov_b64_e32 v[52:53], v[0:1]
	v_mov_b64_e32 v[54:55], v[0:1]
	v_mov_b64_e32 v[56:57], v[0:1]
	v_mov_b64_e32 v[58:59], v[0:1]
	v_mov_b64_e32 v[60:61], v[0:1]
	v_mov_b64_e32 v[62:63], v[0:1]
	v_mov_b64_e32 v[66:67], v[0:1]
	v_mov_b64_e32 v[68:69], v[0:1]
	v_mov_b64_e32 v[70:71], v[0:1]
	v_mov_b64_e32 v[72:73], v[0:1]
	v_mov_b64_e32 v[74:75], v[0:1]
	v_mov_b64_e32 v[76:77], v[0:1]
	v_mov_b64_e32 v[78:79], v[0:1]
	v_mov_b64_e32 v[80:81], v[0:1]
	v_mov_b64_e32 v[82:83], v[0:1]
	v_mov_b64_e32 v[84:85], v[0:1]
	v_mov_b64_e32 v[86:87], v[0:1]
	v_mov_b64_e32 v[88:89], v[0:1]
	v_mov_b64_e32 v[90:91], v[0:1]
	v_mov_b64_e32 v[92:93], v[0:1]
	v_mov_b64_e32 v[94:95], v[0:1]
	v_mov_b64_e32 v[96:97], v[0:1]
	v_mov_b64_e32 v[98:99], v[0:1]
	v_mov_b64_e32 v[100:101], v[0:1]
	v_mov_b64_e32 v[102:103], v[0:1]
	v_mov_b64_e32 v[104:105], v[0:1]
	v_mov_b64_e32 v[106:107], v[0:1]
	v_mov_b64_e32 v[108:109], v[0:1]
	v_mov_b64_e32 v[110:111], v[0:1]
	v_mov_b64_e32 v[112:113], v[0:1]
	v_mov_b64_e32 v[116:117], v[0:1]
	v_mov_b64_e32 v[118:119], v[0:1]
	v_mov_b64_e32 v[120:121], v[0:1]
	v_mov_b64_e32 v[122:123], v[0:1]
	v_mov_b64_e32 v[124:125], v[0:1]
	v_mov_b64_e32 v[126:127], v[0:1]
	v_mov_b64_e32 v[128:129], v[0:1]
	v_mov_b64_e32 v[130:131], v[0:1]

.LBB0_626:
	v_mov_b32_e32 v0, 0
	s_mov_b32 s13, -2
	s_mov_b64 s[2:3], 0
	v_mov_b32_e32 v1, v0
	v_mov_b64_e32 v[2:3], v[0:1]
	v_mov_b64_e32 v[4:5], v[0:1]
	v_mov_b64_e32 v[6:7], v[0:1]
	v_mov_b64_e32 v[8:9], v[0:1]
	v_mov_b64_e32 v[10:11], v[0:1]
	v_mov_b64_e32 v[12:13], v[0:1]
	v_mov_b64_e32 v[14:15], v[0:1]
	v_mov_b64_e32 v[16:17], v[0:1]
	v_mov_b64_e32 v[18:19], v[0:1]
	v_mov_b64_e32 v[20:21], v[0:1]
	v_mov_b64_e32 v[22:23], v[0:1]
	v_mov_b64_e32 v[24:25], v[0:1]
	v_mov_b64_e32 v[26:27], v[0:1]
	s_waitcnt lgkmcnt(0)
	v_mov_b64_e32 v[28:29], v[0:1]
	v_mov_b64_e32 v[30:31], v[0:1]
	v_mov_b64_e32 v[32:33], v[0:1]
	v_mov_b64_e32 v[34:35], v[0:1]
	v_mov_b64_e32 v[36:37], v[0:1]
	v_mov_b64_e32 v[38:39], v[0:1]
	v_mov_b64_e32 v[40:41], v[0:1]
	v_mov_b64_e32 v[42:43], v[0:1]
	v_mov_b64_e32 v[44:45], v[0:1]
	v_mov_b64_e32 v[46:47], v[0:1]
	v_mov_b64_e32 v[48:49], v[0:1]
	v_mov_b64_e32 v[50:51], v[0:1]
	v_mov_b64_e32 v[52:53], v[0:1]
	v_mov_b64_e32 v[54:55], v[0:1]
	v_mov_b64_e32 v[56:57], v[0:1]
	v_mov_b64_e32 v[58:59], v[0:1]
	v_mov_b64_e32 v[60:61], v[0:1]
	v_mov_b64_e32 v[62:63], v[0:1]
	v_mov_b64_e32 v[66:67], v[0:1]
	v_mov_b64_e32 v[68:69], v[0:1]
	v_mov_b64_e32 v[70:71], v[0:1]
	v_mov_b64_e32 v[72:73], v[0:1]
	v_mov_b64_e32 v[74:75], v[0:1]
	v_mov_b64_e32 v[76:77], v[0:1]
	v_mov_b64_e32 v[78:79], v[0:1]
	v_mov_b64_e32 v[80:81], v[0:1]
	v_mov_b64_e32 v[82:83], v[0:1]
	v_mov_b64_e32 v[84:85], v[0:1]
	v_mov_b64_e32 v[86:87], v[0:1]
	v_mov_b64_e32 v[88:89], v[0:1]
	v_mov_b64_e32 v[90:91], v[0:1]
	v_mov_b64_e32 v[92:93], v[0:1]
	v_mov_b64_e32 v[94:95], v[0:1]
	v_mov_b64_e32 v[96:97], v[0:1]
	v_mov_b64_e32 v[98:99], v[0:1]
	v_mov_b64_e32 v[100:101], v[0:1]
	v_mov_b64_e32 v[102:103], v[0:1]
	v_mov_b64_e32 v[104:105], v[0:1]
	v_mov_b64_e32 v[106:107], v[0:1]
	v_mov_b64_e32 v[108:109], v[0:1]
	v_mov_b64_e32 v[110:111], v[0:1]
	v_mov_b64_e32 v[112:113], v[0:1]
	v_mov_b64_e32 v[116:117], v[0:1]
	v_mov_b64_e32 v[118:119], v[0:1]
	v_mov_b64_e32 v[120:121], v[0:1]
	v_mov_b64_e32 v[122:123], v[0:1]
	v_mov_b64_e32 v[124:125], v[0:1]
	v_mov_b64_e32 v[126:127], v[0:1]
	v_mov_b64_e32 v[128:129], v[0:1]
	v_mov_b64_e32 v[130:131], v[0:1]

.LBB0_630:
	s_mul_hi_i32 s13, s20, 0x78787879
	s_lshr_b32 s15, s13, 31
	s_ashr_i32 s13, s13, 3
	s_add_i32 s13, s13, s15
	s_lshl_b32 s2, s22, 2
	s_mul_i32 s13, s13, 17
	s_or_b32 s3, s2, s21
	s_sub_i32 s13, s20, s13
	s_add_i32 s2, s2, -12
	s_cmp_lt_u32 s2, 8
	s_cselect_b64 s[22:23], -1, 0
	s_cmp_lt_i32 s3, 8
	s_cselect_b64 s[24:25], -1, 0
	s_and_b64 s[26:27], s[24:25], exec
	s_cselect_b32 s2, 0, 64
	s_or_b64 vcc, s[24:25], s[22:23]
	s_and_b32 s15, s3, -2
	s_cmp_eq_u32 s15, 10
	s_cselect_b64 s[22:23], -1, 0
	s_cmp_gt_i32 s3, 27
	s_cselect_b64 s[24:25], -1, 0
	s_or_b64 s[22:23], s[24:25], s[22:23]
	s_cmp_lt_i32 s13, 16
	s_cselect_b64 s[24:25], -1, 0
	s_cmp_lt_i32 s3, 20
	s_movk_i32 s15, 0xc0
	s_cselect_b32 s15, 0x80, s15
	s_cmp_lt_i32 s3, 10
	s_cselect_b64 s[26:27], -1, 0
	s_and_b64 s[36:37], s[26:27], exec
	v_mbcnt_lo_u32_b32 v114, -1, 0
	v_mbcnt_hi_u32_b32 v114, -1, v114
	s_cselect_b32 s2, s2, s15
	v_and_b32_e32 v145, 15, v114
	v_ashrrev_i32_e32 v114, 4, v114
	s_and_b64 s[24:25], s[26:27], s[24:25]
	s_lshl_b32 s2, s2, 2
	v_lshlrev_b32_e32 v138, 3, v114
	s_add_u32 s26, s8, s2
	s_addc_u32 s27, s9, 0
	v_ashrrev_i32_e32 v139, 31, v138
	s_lshl_b32 s2, s13, 2
	v_cmp_gt_u32_e64 s[36:37], 2, v114
	v_cndmask_b32_e64 v114, 0, 1, s[24:25]
	v_cndmask_b32_e32 v146, 1.0, v236, vcc
	v_lshl_add_u64 v[136:137], v[138:139], 2, s[26:27]
	s_add_i32 s2, s2, s46
	v_and_b32_e32 v139, 8, v138
	s_and_b64 vcc, exec, s[22:23]
	v_cmp_ne_u32_e64 s[38:39], 1, v114
	s_lshl_b32 s13, s20, 8
	s_add_i32 s13, s13, s29
	v_or_b32_e32 v114, s13, v145
	v_lshl_add_u32 v147, s3, 6, v138
	v_mul_u32_u24_e32 v114, 0x1200, v114
	v_lshl_add_u32 v114, v147, 1, v114
	s_mov_b32 s26, s4
	s_mov_b32 s27, s5
	s_and_b64 vcc, exec, s[22:23]
	s_cbranch_vccnz .Lqkv_epi_v
	global_load_dwordx4 v[148:151], v[136:137], off
	global_load_dwordx4 v[152:155], v[136:137], off offset:16
	global_load_dwordx4 v[156:159], v[136:137], off offset:128
	global_load_dwordx4 v[160:163], v[136:137], off offset:144
	s_and_b64 vcc, exec, s[24:25]
	s_cbranch_vccz .Lqkv_epi_norope
	v_lshlrev_b32_e32 v147, 2, v139
	v_lshl_add_u32 v136, v145, 6, v147
	v_mov_b32_e32 v138, v147
	v_add_u32_e32 v139, 0x1000, v147
	v_add_u32_e32 v137, 0x1000, v136
	s_lshl_b32 s15, s2, 6
	s_add_u32 s40, s6, s15
	s_addc_u32 s41, s7, 0
	global_load_dwordx4 v[164:167], v138, s[40:41]
	global_load_dwordx4 v[168:171], v138, s[40:41] offset:16
	global_load_dwordx4 v[172:175], v139, s[40:41]
	global_load_dwordx4 v[176:179], v139, s[40:41] offset:16
	global_load_dwordx4 v[180:183], v136, s[6:7]
	global_load_dwordx4 v[184:187], v136, s[6:7] offset:16
	global_load_dwordx4 v[202:205], v137, s[6:7]
	global_load_dwordx4 v[206:209], v137, s[6:7] offset:16
	global_load_dwordx4 v[210:213], v136, s[6:7] offset:1024
	global_load_dwordx4 v[214:217], v136, s[6:7] offset:1040
	global_load_dwordx4 v[218:221], v137, s[6:7] offset:1024
	global_load_dwordx4 v[222:225], v137, s[6:7] offset:1040
	v_pk_mul_f32 v[132:133], v[116:117], v[116:117]
	v_pk_mul_f32 v[134:135], v[124:125], v[124:125]
	v_pk_fma_f32 v[132:133], v[118:119], v[118:119], v[132:133]
	v_pk_fma_f32 v[134:135], v[126:127], v[126:127], v[134:135]
	v_pk_fma_f32 v[132:133], v[120:121], v[120:121], v[132:133]
	v_pk_fma_f32 v[134:135], v[128:129], v[128:129], v[134:135]
	v_pk_fma_f32 v[132:133], v[122:123], v[122:123], v[132:133]
	v_pk_fma_f32 v[134:135], v[130:131], v[130:131], v[134:135]
	v_pk_add_f32 v[132:133], v[132:133], v[134:135]
	s_nop 0
	v_add_f32_e32 v194, v132, v133
	ds_swizzle_b32 v195, v194 offset:swizzle(SWAP,16)
	s_waitcnt lgkmcnt(0)
	v_add_f32_e32 v194, v194, v195
	v_mov_b32_e32 v195, v194
	s_nop 1
	v_permlane32_swap_b32_e32 v194, v195
	v_add_f32_e32 v194, v194, v195
	v_fmamk_f32 v194, v194, 0x3c800000, v192
	v_rsq_f32_e32 v194, v194
	s_nop 0
	v_mul_f32_e32 v196, v146, v194
	v_pk_mul_f32 v[116:117], v[116:117], v[196:197] op_sel_hi:[1,0]
	v_pk_mul_f32 v[118:119], v[118:119], v[196:197] op_sel_hi:[1,0]
	v_pk_mul_f32 v[120:121], v[120:121], v[196:197] op_sel_hi:[1,0]
	v_pk_mul_f32 v[122:123], v[122:123], v[196:197] op_sel_hi:[1,0]
	v_pk_mul_f32 v[124:125], v[124:125], v[196:197] op_sel_hi:[1,0]
	v_pk_mul_f32 v[126:127], v[126:127], v[196:197] op_sel_hi:[1,0]
	v_pk_mul_f32 v[128:129], v[128:129], v[196:197] op_sel_hi:[1,0]
	v_pk_mul_f32 v[130:131], v[130:131], v[196:197] op_sel_hi:[1,0]
	s_waitcnt vmcnt(12)
	v_pk_mul_f32 v[116:117], v[148:149], v[116:117]
	v_pk_mul_f32 v[118:119], v[150:151], v[118:119]
	v_pk_mul_f32 v[120:121], v[152:153], v[120:121]
	v_pk_mul_f32 v[122:123], v[154:155], v[122:123]
	v_pk_mul_f32 v[124:125], v[156:157], v[124:125]
	v_pk_mul_f32 v[126:127], v[158:159], v[126:127]
	v_pk_mul_f32 v[128:129], v[160:161], v[128:129]
	v_pk_mul_f32 v[130:131], v[162:163], v[130:131]
	s_waitcnt vmcnt(8)
	v_pk_mul_f32 v[226:227], v[116:117], v[172:173]
	v_pk_mul_f32 v[228:229], v[118:119], v[174:175]
	v_pk_mul_f32 v[230:231], v[120:121], v[176:177]
	v_pk_mul_f32 v[232:233], v[122:123], v[178:179]
	v_mov_b64_e32 v[244:245], v[226:227]
	v_mov_b64_e32 v[246:247], v[228:229]
	v_mov_b64_e32 v[248:249], v[230:231]
	v_mov_b64_e32 v[250:251], v[232:233]
	v_permlane32_swap_b32_e32 v226, v244
	v_permlane32_swap_b32_e32 v227, v245
	v_permlane32_swap_b32_e32 v228, v246
	v_permlane32_swap_b32_e32 v229, v247
	v_permlane32_swap_b32_e32 v230, v248
	v_permlane32_swap_b32_e32 v231, v249
	v_permlane32_swap_b32_e32 v232, v250
	v_permlane32_swap_b32_e32 v233, v251
	v_cndmask_b32_e64 v244, v226, -v244, s[36:37]
	v_cndmask_b32_e64 v245, v227, -v245, s[36:37]
	v_cndmask_b32_e64 v246, v228, -v246, s[36:37]
	v_cndmask_b32_e64 v247, v229, -v247, s[36:37]
	v_cndmask_b32_e64 v248, v230, -v248, s[36:37]
	v_cndmask_b32_e64 v249, v231, -v249, s[36:37]
	v_cndmask_b32_e64 v250, v232, -v250, s[36:37]
	v_cndmask_b32_e64 v251, v233, -v251, s[36:37]
	v_pk_fma_f32 v[116:117], v[116:117], v[164:165], v[244:245]
	v_pk_fma_f32 v[118:119], v[118:119], v[166:167], v[246:247]
	v_pk_fma_f32 v[120:121], v[120:121], v[168:169], v[248:249]
	v_pk_fma_f32 v[122:123], v[122:123], v[170:171], v[250:251]
	s_waitcnt vmcnt(4)
	v_pk_mul_f32 v[226:227], v[124:125], v[202:203]
	v_pk_mul_f32 v[228:229], v[126:127], v[204:205]
	v_pk_mul_f32 v[230:231], v[128:129], v[206:207]
	v_pk_mul_f32 v[232:233], v[130:131], v[208:209]
	v_mov_b64_e32 v[244:245], v[226:227]
	v_mov_b64_e32 v[246:247], v[228:229]
	v_mov_b64_e32 v[248:249], v[230:231]
	v_mov_b64_e32 v[250:251], v[232:233]
	v_permlane32_swap_b32_e32 v226, v244
	v_permlane32_swap_b32_e32 v227, v245
	v_permlane32_swap_b32_e32 v228, v246
	v_permlane32_swap_b32_e32 v229, v247
	v_permlane32_swap_b32_e32 v230, v248
	v_permlane32_swap_b32_e32 v231, v249
	v_permlane32_swap_b32_e32 v232, v250
	v_permlane32_swap_b32_e32 v233, v251
	v_cndmask_b32_e64 v244, v226, -v244, s[36:37]
	v_cndmask_b32_e64 v245, v227, -v245, s[36:37]
	v_cndmask_b32_e64 v246, v228, -v246, s[36:37]
	v_cndmask_b32_e64 v247, v229, -v247, s[36:37]
	v_cndmask_b32_e64 v248, v230, -v248, s[36:37]
	v_cndmask_b32_e64 v249, v231, -v249, s[36:37]
	v_cndmask_b32_e64 v250, v232, -v250, s[36:37]
	v_cndmask_b32_e64 v251, v233, -v251, s[36:37]
	v_pk_fma_f32 v[124:125], v[124:125], v[180:181], v[244:245]
	v_pk_fma_f32 v[126:127], v[126:127], v[182:183], v[246:247]
	v_pk_fma_f32 v[128:129], v[128:129], v[184:185], v[248:249]
	v_pk_fma_f32 v[130:131], v[130:131], v[186:187], v[250:251]
	global_load_dwordx4 v[180:183], v136, s[6:7] offset:2048
	global_load_dwordx4 v[184:187], v136, s[6:7] offset:2064
	global_load_dwordx4 v[202:205], v137, s[6:7] offset:2048
	global_load_dwordx4 v[206:209], v137, s[6:7] offset:2064
	v_cvt_pk_bf16_f32 v116, v116, v117
	v_cvt_pk_bf16_f32 v117, v118, v119
	v_cvt_pk_bf16_f32 v118, v120, v121
	v_cvt_pk_bf16_f32 v119, v122, v123
	global_store_dwordx4 v114, v[116:119], s[26:27]
	v_cvt_pk_bf16_f32 v124, v124, v125
	v_cvt_pk_bf16_f32 v125, v126, v127
	v_cvt_pk_bf16_f32 v126, v128, v129
	v_cvt_pk_bf16_f32 v127, v130, v131
	global_store_dwordx4 v114, v[124:127], s[26:27] offset:64
	s_add_u32 s26, s26, 0x12000
	s_addc_u32 s27, s27, 0
	v_pk_mul_f32 v[132:133], v[98:99], v[98:99]
	v_pk_mul_f32 v[134:135], v[106:107], v[106:107]
	v_pk_fma_f32 v[132:133], v[100:101], v[100:101], v[132:133]
	v_pk_fma_f32 v[134:135], v[108:109], v[108:109], v[134:135]
	v_pk_fma_f32 v[132:133], v[102:103], v[102:103], v[132:133]
	v_pk_fma_f32 v[134:135], v[110:111], v[110:111], v[134:135]
	v_pk_fma_f32 v[132:133], v[104:105], v[104:105], v[132:133]
	v_pk_fma_f32 v[134:135], v[112:113], v[112:113], v[134:135]
	v_pk_add_f32 v[132:133], v[132:133], v[134:135]
	s_nop 0
	v_add_f32_e32 v194, v132, v133
	ds_swizzle_b32 v195, v194 offset:swizzle(SWAP,16)
	s_waitcnt lgkmcnt(0)
	v_add_f32_e32 v194, v194, v195
	v_mov_b32_e32 v195, v194
	s_nop 1
	v_permlane32_swap_b32_e32 v194, v195
	v_add_f32_e32 v194, v194, v195
	v_fmamk_f32 v194, v194, 0x3c800000, v192
	v_rsq_f32_e32 v194, v194
	s_nop 0
	v_mul_f32_e32 v196, v146, v194
	v_pk_mul_f32 v[98:99], v[98:99], v[196:197] op_sel_hi:[1,0]
	v_pk_mul_f32 v[100:101], v[100:101], v[196:197] op_sel_hi:[1,0]
	v_pk_mul_f32 v[102:103], v[102:103], v[196:197] op_sel_hi:[1,0]
	v_pk_mul_f32 v[104:105], v[104:105], v[196:197] op_sel_hi:[1,0]
	v_pk_mul_f32 v[106:107], v[106:107], v[196:197] op_sel_hi:[1,0]
	v_pk_mul_f32 v[108:109], v[108:109], v[196:197] op_sel_hi:[1,0]
	v_pk_mul_f32 v[110:111], v[110:111], v[196:197] op_sel_hi:[1,0]
	v_pk_mul_f32 v[112:113], v[112:113], v[196:197] op_sel_hi:[1,0]
	v_pk_mul_f32 v[98:99], v[148:149], v[98:99]
	v_pk_mul_f32 v[100:101], v[150:151], v[100:101]
	v_pk_mul_f32 v[102:103], v[152:153], v[102:103]
	v_pk_mul_f32 v[104:105], v[154:155], v[104:105]
	v_pk_mul_f32 v[106:107], v[156:157], v[106:107]
	v_pk_mul_f32 v[108:109], v[158:159], v[108:109]
	v_pk_mul_f32 v[110:111], v[160:161], v[110:111]
	v_pk_mul_f32 v[112:113], v[162:163], v[112:113]
	v_pk_mul_f32 v[226:227], v[98:99], v[172:173]
	v_pk_mul_f32 v[228:229], v[100:101], v[174:175]
	v_pk_mul_f32 v[230:231], v[102:103], v[176:177]
	v_pk_mul_f32 v[232:233], v[104:105], v[178:179]
	v_mov_b64_e32 v[244:245], v[226:227]
	v_mov_b64_e32 v[246:247], v[228:229]
	v_mov_b64_e32 v[248:249], v[230:231]
	v_mov_b64_e32 v[250:251], v[232:233]
	v_permlane32_swap_b32_e32 v226, v244
	v_permlane32_swap_b32_e32 v227, v245
	v_permlane32_swap_b32_e32 v228, v246
	v_permlane32_swap_b32_e32 v229, v247
	v_permlane32_swap_b32_e32 v230, v248
	v_permlane32_swap_b32_e32 v231, v249
	v_permlane32_swap_b32_e32 v232, v250
	v_permlane32_swap_b32_e32 v233, v251
	v_cndmask_b32_e64 v244, v226, -v244, s[36:37]
	v_cndmask_b32_e64 v245, v227, -v245, s[36:37]
	v_cndmask_b32_e64 v246, v228, -v246, s[36:37]
	v_cndmask_b32_e64 v247, v229, -v247, s[36:37]
	v_cndmask_b32_e64 v248, v230, -v248, s[36:37]
	v_cndmask_b32_e64 v249, v231, -v249, s[36:37]
	v_cndmask_b32_e64 v250, v232, -v250, s[36:37]
	v_cndmask_b32_e64 v251, v233, -v251, s[36:37]
	v_pk_fma_f32 v[98:99], v[98:99], v[164:165], v[244:245]
	v_pk_fma_f32 v[100:101], v[100:101], v[166:167], v[246:247]
	v_pk_fma_f32 v[102:103], v[102:103], v[168:169], v[248:249]
	v_pk_fma_f32 v[104:105], v[104:105], v[170:171], v[250:251]
	s_waitcnt vmcnt(6)
	v_pk_mul_f32 v[226:227], v[106:107], v[218:219]
	v_pk_mul_f32 v[228:229], v[108:109], v[220:221]
	v_pk_mul_f32 v[230:231], v[110:111], v[222:223]
	v_pk_mul_f32 v[232:233], v[112:113], v[224:225]
	v_mov_b64_e32 v[244:245], v[226:227]
	v_mov_b64_e32 v[246:247], v[228:229]
	v_mov_b64_e32 v[248:249], v[230:231]
	v_mov_b64_e32 v[250:251], v[232:233]
	v_permlane32_swap_b32_e32 v226, v244
	v_permlane32_swap_b32_e32 v227, v245
	v_permlane32_swap_b32_e32 v228, v246
	v_permlane32_swap_b32_e32 v229, v247
	v_permlane32_swap_b32_e32 v230, v248
	v_permlane32_swap_b32_e32 v231, v249
	v_permlane32_swap_b32_e32 v232, v250
	v_permlane32_swap_b32_e32 v233, v251
	v_cndmask_b32_e64 v244, v226, -v244, s[36:37]
	v_cndmask_b32_e64 v245, v227, -v245, s[36:37]
	v_cndmask_b32_e64 v246, v228, -v246, s[36:37]
	v_cndmask_b32_e64 v247, v229, -v247, s[36:37]
	v_cndmask_b32_e64 v248, v230, -v248, s[36:37]
	v_cndmask_b32_e64 v249, v231, -v249, s[36:37]
	v_cndmask_b32_e64 v250, v232, -v250, s[36:37]
	v_cndmask_b32_e64 v251, v233, -v251, s[36:37]
	v_pk_fma_f32 v[106:107], v[106:107], v[210:211], v[244:245]
	v_pk_fma_f32 v[108:109], v[108:109], v[212:213], v[246:247]
	v_pk_fma_f32 v[110:111], v[110:111], v[214:215], v[248:249]
	v_pk_fma_f32 v[112:113], v[112:113], v[216:217], v[250:251]
	global_load_dwordx4 v[210:213], v136, s[6:7] offset:3072
	global_load_dwordx4 v[214:217], v136, s[6:7] offset:3088
	global_load_dwordx4 v[218:221], v137, s[6:7] offset:3072
	global_load_dwordx4 v[222:225], v137, s[6:7] offset:3088
	v_cvt_pk_bf16_f32 v98, v98, v99
	v_cvt_pk_bf16_f32 v99, v100, v101
	v_cvt_pk_bf16_f32 v100, v102, v103
	v_cvt_pk_bf16_f32 v101, v104, v105
	global_store_dwordx4 v114, v[98:101], s[26:27]
	v_cvt_pk_bf16_f32 v106, v106, v107
	v_cvt_pk_bf16_f32 v107, v108, v109
	v_cvt_pk_bf16_f32 v108, v110, v111
	v_cvt_pk_bf16_f32 v109, v112, v113
	global_store_dwordx4 v114, v[106:109], s[26:27] offset:64
	s_add_u32 s26, s26, 0x12000
	s_addc_u32 s27, s27, 0
	v_pk_mul_f32 v[132:133], v[82:83], v[82:83]
	v_pk_mul_f32 v[134:135], v[90:91], v[90:91]
	v_pk_fma_f32 v[132:133], v[84:85], v[84:85], v[132:133]
	v_pk_fma_f32 v[134:135], v[92:93], v[92:93], v[134:135]
	v_pk_fma_f32 v[132:133], v[86:87], v[86:87], v[132:133]
	v_pk_fma_f32 v[134:135], v[94:95], v[94:95], v[134:135]
	v_pk_fma_f32 v[132:133], v[88:89], v[88:89], v[132:133]
	v_pk_fma_f32 v[134:135], v[96:97], v[96:97], v[134:135]
	v_pk_add_f32 v[132:133], v[132:133], v[134:135]
	s_nop 0
	v_add_f32_e32 v194, v132, v133
	ds_swizzle_b32 v195, v194 offset:swizzle(SWAP,16)
	s_waitcnt lgkmcnt(0)
	v_add_f32_e32 v194, v194, v195
	v_mov_b32_e32 v195, v194
	s_nop 1
	v_permlane32_swap_b32_e32 v194, v195
	v_add_f32_e32 v194, v194, v195
	v_fmamk_f32 v194, v194, 0x3c800000, v192
	v_rsq_f32_e32 v194, v194
	s_nop 0
	v_mul_f32_e32 v196, v146, v194
	v_pk_mul_f32 v[82:83], v[82:83], v[196:197] op_sel_hi:[1,0]
	v_pk_mul_f32 v[84:85], v[84:85], v[196:197] op_sel_hi:[1,0]
	v_pk_mul_f32 v[86:87], v[86:87], v[196:197] op_sel_hi:[1,0]
	v_pk_mul_f32 v[88:89], v[88:89], v[196:197] op_sel_hi:[1,0]
	v_pk_mul_f32 v[90:91], v[90:91], v[196:197] op_sel_hi:[1,0]
	v_pk_mul_f32 v[92:93], v[92:93], v[196:197] op_sel_hi:[1,0]
	v_pk_mul_f32 v[94:95], v[94:95], v[196:197] op_sel_hi:[1,0]
	v_pk_mul_f32 v[96:97], v[96:97], v[196:197] op_sel_hi:[1,0]
	v_pk_mul_f32 v[82:83], v[148:149], v[82:83]
	v_pk_mul_f32 v[84:85], v[150:151], v[84:85]
	v_pk_mul_f32 v[86:87], v[152:153], v[86:87]
	v_pk_mul_f32 v[88:89], v[154:155], v[88:89]
	v_pk_mul_f32 v[90:91], v[156:157], v[90:91]
	v_pk_mul_f32 v[92:93], v[158:159], v[92:93]
	v_pk_mul_f32 v[94:95], v[160:161], v[94:95]
	v_pk_mul_f32 v[96:97], v[162:163], v[96:97]
	v_pk_mul_f32 v[226:227], v[82:83], v[172:173]
	v_pk_mul_f32 v[228:229], v[84:85], v[174:175]
	v_pk_mul_f32 v[230:231], v[86:87], v[176:177]
	v_pk_mul_f32 v[232:233], v[88:89], v[178:179]
	v_mov_b64_e32 v[244:245], v[226:227]
	v_mov_b64_e32 v[246:247], v[228:229]
	v_mov_b64_e32 v[248:249], v[230:231]
	v_mov_b64_e32 v[250:251], v[232:233]
	v_permlane32_swap_b32_e32 v226, v244
	v_permlane32_swap_b32_e32 v227, v245
	v_permlane32_swap_b32_e32 v228, v246
	v_permlane32_swap_b32_e32 v229, v247
	v_permlane32_swap_b32_e32 v230, v248
	v_permlane32_swap_b32_e32 v231, v249
	v_permlane32_swap_b32_e32 v232, v250
	v_permlane32_swap_b32_e32 v233, v251
	v_cndmask_b32_e64 v244, v226, -v244, s[36:37]
	v_cndmask_b32_e64 v245, v227, -v245, s[36:37]
	v_cndmask_b32_e64 v246, v228, -v246, s[36:37]
	v_cndmask_b32_e64 v247, v229, -v247, s[36:37]
	v_cndmask_b32_e64 v248, v230, -v248, s[36:37]
	v_cndmask_b32_e64 v249, v231, -v249, s[36:37]
	v_cndmask_b32_e64 v250, v232, -v250, s[36:37]
	v_cndmask_b32_e64 v251, v233, -v251, s[36:37]
	v_pk_fma_f32 v[82:83], v[82:83], v[164:165], v[244:245]
	v_pk_fma_f32 v[84:85], v[84:85], v[166:167], v[246:247]
	v_pk_fma_f32 v[86:87], v[86:87], v[168:169], v[248:249]
	v_pk_fma_f32 v[88:89], v[88:89], v[170:171], v[250:251]
	s_waitcnt vmcnt(8)
	v_pk_mul_f32 v[226:227], v[90:91], v[202:203]
	v_pk_mul_f32 v[228:229], v[92:93], v[204:205]
	v_pk_mul_f32 v[230:231], v[94:95], v[206:207]
	v_pk_mul_f32 v[232:233], v[96:97], v[208:209]
	v_mov_b64_e32 v[244:245], v[226:227]
	v_mov_b64_e32 v[246:247], v[228:229]
	v_mov_b64_e32 v[248:249], v[230:231]
	v_mov_b64_e32 v[250:251], v[232:233]
	v_permlane32_swap_b32_e32 v226, v244
	v_permlane32_swap_b32_e32 v227, v245
	v_permlane32_swap_b32_e32 v228, v246
	v_permlane32_swap_b32_e32 v229, v247
	v_permlane32_swap_b32_e32 v230, v248
	v_permlane32_swap_b32_e32 v231, v249
	v_permlane32_swap_b32_e32 v232, v250
	v_permlane32_swap_b32_e32 v233, v251
	v_cndmask_b32_e64 v244, v226, -v244, s[36:37]
	v_cndmask_b32_e64 v245, v227, -v245, s[36:37]
	v_cndmask_b32_e64 v246, v228, -v246, s[36:37]
	v_cndmask_b32_e64 v247, v229, -v247, s[36:37]
	v_cndmask_b32_e64 v248, v230, -v248, s[36:37]
	v_cndmask_b32_e64 v249, v231, -v249, s[36:37]
	v_cndmask_b32_e64 v250, v232, -v250, s[36:37]
	v_cndmask_b32_e64 v251, v233, -v251, s[36:37]
	v_pk_fma_f32 v[90:91], v[90:91], v[180:181], v[244:245]
	v_pk_fma_f32 v[92:93], v[92:93], v[182:183], v[246:247]
	v_pk_fma_f32 v[94:95], v[94:95], v[184:185], v[248:249]
	v_pk_fma_f32 v[96:97], v[96:97], v[186:187], v[250:251]
	global_load_dwordx4 v[180:183], v136, s[6:7]
	global_load_dwordx4 v[184:187], v136, s[6:7] offset:16
	global_load_dwordx4 v[202:205], v137, s[6:7]
	global_load_dwordx4 v[206:209], v137, s[6:7] offset:16
	v_cvt_pk_bf16_f32 v82, v82, v83
	v_cvt_pk_bf16_f32 v83, v84, v85
	v_cvt_pk_bf16_f32 v84, v86, v87
	v_cvt_pk_bf16_f32 v85, v88, v89
	global_store_dwordx4 v114, v[82:85], s[26:27]
	v_cvt_pk_bf16_f32 v90, v90, v91
	v_cvt_pk_bf16_f32 v91, v92, v93
	v_cvt_pk_bf16_f32 v92, v94, v95
	v_cvt_pk_bf16_f32 v93, v96, v97
	global_store_dwordx4 v114, v[90:93], s[26:27] offset:64
	s_add_u32 s26, s26, 0x12000
	s_addc_u32 s27, s27, 0
	v_pk_mul_f32 v[132:133], v[66:67], v[66:67]
	v_pk_mul_f32 v[134:135], v[74:75], v[74:75]
	v_pk_fma_f32 v[132:133], v[68:69], v[68:69], v[132:133]
	v_pk_fma_f32 v[134:135], v[76:77], v[76:77], v[134:135]
	v_pk_fma_f32 v[132:133], v[70:71], v[70:71], v[132:133]
	v_pk_fma_f32 v[134:135], v[78:79], v[78:79], v[134:135]
	v_pk_fma_f32 v[132:133], v[72:73], v[72:73], v[132:133]
	v_pk_fma_f32 v[134:135], v[80:81], v[80:81], v[134:135]
	v_pk_add_f32 v[132:133], v[132:133], v[134:135]
	s_nop 0
	v_add_f32_e32 v194, v132, v133
	ds_swizzle_b32 v195, v194 offset:swizzle(SWAP,16)
	s_waitcnt lgkmcnt(0)
	v_add_f32_e32 v194, v194, v195
	v_mov_b32_e32 v195, v194
	s_nop 1
	v_permlane32_swap_b32_e32 v194, v195
	v_add_f32_e32 v194, v194, v195
	v_fmamk_f32 v194, v194, 0x3c800000, v192
	v_rsq_f32_e32 v194, v194
	s_nop 0
	v_mul_f32_e32 v196, v146, v194
	v_pk_mul_f32 v[66:67], v[66:67], v[196:197] op_sel_hi:[1,0]
	v_pk_mul_f32 v[68:69], v[68:69], v[196:197] op_sel_hi:[1,0]
	v_pk_mul_f32 v[70:71], v[70:71], v[196:197] op_sel_hi:[1,0]
	v_pk_mul_f32 v[72:73], v[72:73], v[196:197] op_sel_hi:[1,0]
	v_pk_mul_f32 v[74:75], v[74:75], v[196:197] op_sel_hi:[1,0]
	v_pk_mul_f32 v[76:77], v[76:77], v[196:197] op_sel_hi:[1,0]
	v_pk_mul_f32 v[78:79], v[78:79], v[196:197] op_sel_hi:[1,0]
	v_pk_mul_f32 v[80:81], v[80:81], v[196:197] op_sel_hi:[1,0]
	v_pk_mul_f32 v[66:67], v[148:149], v[66:67]
	v_pk_mul_f32 v[68:69], v[150:151], v[68:69]
	v_pk_mul_f32 v[70:71], v[152:153], v[70:71]
	v_pk_mul_f32 v[72:73], v[154:155], v[72:73]
	v_pk_mul_f32 v[74:75], v[156:157], v[74:75]
	v_pk_mul_f32 v[76:77], v[158:159], v[76:77]
	v_pk_mul_f32 v[78:79], v[160:161], v[78:79]
	v_pk_mul_f32 v[80:81], v[162:163], v[80:81]
	v_pk_mul_f32 v[226:227], v[66:67], v[172:173]
	v_pk_mul_f32 v[228:229], v[68:69], v[174:175]
	v_pk_mul_f32 v[230:231], v[70:71], v[176:177]
	v_pk_mul_f32 v[232:233], v[72:73], v[178:179]
	v_mov_b64_e32 v[244:245], v[226:227]
	v_mov_b64_e32 v[246:247], v[228:229]
	v_mov_b64_e32 v[248:249], v[230:231]
	v_mov_b64_e32 v[250:251], v[232:233]
	v_permlane32_swap_b32_e32 v226, v244
	v_permlane32_swap_b32_e32 v227, v245
	v_permlane32_swap_b32_e32 v228, v246
	v_permlane32_swap_b32_e32 v229, v247
	v_permlane32_swap_b32_e32 v230, v248
	v_permlane32_swap_b32_e32 v231, v249
	v_permlane32_swap_b32_e32 v232, v250
	v_permlane32_swap_b32_e32 v233, v251
	v_cndmask_b32_e64 v244, v226, -v244, s[36:37]
	v_cndmask_b32_e64 v245, v227, -v245, s[36:37]
	v_cndmask_b32_e64 v246, v228, -v246, s[36:37]
	v_cndmask_b32_e64 v247, v229, -v247, s[36:37]
	v_cndmask_b32_e64 v248, v230, -v248, s[36:37]
	v_cndmask_b32_e64 v249, v231, -v249, s[36:37]
	v_cndmask_b32_e64 v250, v232, -v250, s[36:37]
	v_cndmask_b32_e64 v251, v233, -v251, s[36:37]
	v_pk_fma_f32 v[66:67], v[66:67], v[164:165], v[244:245]
	v_pk_fma_f32 v[68:69], v[68:69], v[166:167], v[246:247]
	v_pk_fma_f32 v[70:71], v[70:71], v[168:169], v[248:249]
	v_pk_fma_f32 v[72:73], v[72:73], v[170:171], v[250:251]
	s_add_u32 s40, s40, 0x80
	s_addc_u32 s41, s41, 0
	global_load_dwordx4 v[164:167], v138, s[40:41]
	global_load_dwordx4 v[168:171], v138, s[40:41] offset:16
	global_load_dwordx4 v[172:175], v139, s[40:41]
	global_load_dwordx4 v[176:179], v139, s[40:41] offset:16
	s_waitcnt vmcnt(12)
	v_pk_mul_f32 v[226:227], v[74:75], v[218:219]
	v_pk_mul_f32 v[228:229], v[76:77], v[220:221]
	v_pk_mul_f32 v[230:231], v[78:79], v[222:223]
	v_pk_mul_f32 v[232:233], v[80:81], v[224:225]
	v_mov_b64_e32 v[244:245], v[226:227]
	v_mov_b64_e32 v[246:247], v[228:229]
	v_mov_b64_e32 v[248:249], v[230:231]
	v_mov_b64_e32 v[250:251], v[232:233]
	v_permlane32_swap_b32_e32 v226, v244
	v_permlane32_swap_b32_e32 v227, v245
	v_permlane32_swap_b32_e32 v228, v246
	v_permlane32_swap_b32_e32 v229, v247
	v_permlane32_swap_b32_e32 v230, v248
	v_permlane32_swap_b32_e32 v231, v249
	v_permlane32_swap_b32_e32 v232, v250
	v_permlane32_swap_b32_e32 v233, v251
	v_cndmask_b32_e64 v244, v226, -v244, s[36:37]
	v_cndmask_b32_e64 v245, v227, -v245, s[36:37]
	v_cndmask_b32_e64 v246, v228, -v246, s[36:37]
	v_cndmask_b32_e64 v247, v229, -v247, s[36:37]
	v_cndmask_b32_e64 v248, v230, -v248, s[36:37]
	v_cndmask_b32_e64 v249, v231, -v249, s[36:37]
	v_cndmask_b32_e64 v250, v232, -v250, s[36:37]
	v_cndmask_b32_e64 v251, v233, -v251, s[36:37]
	v_pk_fma_f32 v[74:75], v[74:75], v[210:211], v[244:245]
	v_pk_fma_f32 v[76:77], v[76:77], v[212:213], v[246:247]
	v_pk_fma_f32 v[78:79], v[78:79], v[214:215], v[248:249]
	v_pk_fma_f32 v[80:81], v[80:81], v[216:217], v[250:251]
	global_load_dwordx4 v[210:213], v136, s[6:7] offset:1024
	global_load_dwordx4 v[214:217], v136, s[6:7] offset:1040
	global_load_dwordx4 v[218:221], v137, s[6:7] offset:1024
	global_load_dwordx4 v[222:225], v137, s[6:7] offset:1040
	v_cvt_pk_bf16_f32 v66, v66, v67
	v_cvt_pk_bf16_f32 v67, v68, v69
	v_cvt_pk_bf16_f32 v68, v70, v71
	v_cvt_pk_bf16_f32 v69, v72, v73
	global_store_dwordx4 v114, v[66:69], s[26:27]
	v_cvt_pk_bf16_f32 v74, v74, v75
	v_cvt_pk_bf16_f32 v75, v76, v77
	v_cvt_pk_bf16_f32 v76, v78, v79
	v_cvt_pk_bf16_f32 v77, v80, v81
	global_store_dwordx4 v114, v[74:77], s[26:27] offset:64
	s_add_u32 s26, s26, 0x5a000
	s_addc_u32 s27, s27, 0
	v_pk_mul_f32 v[132:133], v[48:49], v[48:49]
	v_pk_mul_f32 v[134:135], v[56:57], v[56:57]
	v_pk_fma_f32 v[132:133], v[50:51], v[50:51], v[132:133]
	v_pk_fma_f32 v[134:135], v[58:59], v[58:59], v[134:135]
	v_pk_fma_f32 v[132:133], v[52:53], v[52:53], v[132:133]
	v_pk_fma_f32 v[134:135], v[60:61], v[60:61], v[134:135]
	v_pk_fma_f32 v[132:133], v[54:55], v[54:55], v[132:133]
	v_pk_fma_f32 v[134:135], v[62:63], v[62:63], v[134:135]
	v_pk_add_f32 v[132:133], v[132:133], v[134:135]
	s_nop 0
	v_add_f32_e32 v194, v132, v133
	ds_swizzle_b32 v195, v194 offset:swizzle(SWAP,16)
	s_waitcnt lgkmcnt(0)
	v_add_f32_e32 v194, v194, v195
	v_mov_b32_e32 v195, v194
	s_nop 1
	v_permlane32_swap_b32_e32 v194, v195
	v_add_f32_e32 v194, v194, v195
	v_fmamk_f32 v194, v194, 0x3c800000, v192
	v_rsq_f32_e32 v194, v194
	s_nop 0
	v_mul_f32_e32 v196, v146, v194
	v_pk_mul_f32 v[48:49], v[48:49], v[196:197] op_sel_hi:[1,0]
	v_pk_mul_f32 v[50:51], v[50:51], v[196:197] op_sel_hi:[1,0]
	v_pk_mul_f32 v[52:53], v[52:53], v[196:197] op_sel_hi:[1,0]
	v_pk_mul_f32 v[54:55], v[54:55], v[196:197] op_sel_hi:[1,0]
	v_pk_mul_f32 v[56:57], v[56:57], v[196:197] op_sel_hi:[1,0]
	v_pk_mul_f32 v[58:59], v[58:59], v[196:197] op_sel_hi:[1,0]
	v_pk_mul_f32 v[60:61], v[60:61], v[196:197] op_sel_hi:[1,0]
	v_pk_mul_f32 v[62:63], v[62:63], v[196:197] op_sel_hi:[1,0]
	v_pk_mul_f32 v[48:49], v[148:149], v[48:49]
	v_pk_mul_f32 v[50:51], v[150:151], v[50:51]
	v_pk_mul_f32 v[52:53], v[152:153], v[52:53]
	v_pk_mul_f32 v[54:55], v[154:155], v[54:55]
	v_pk_mul_f32 v[56:57], v[156:157], v[56:57]
	v_pk_mul_f32 v[58:59], v[158:159], v[58:59]
	v_pk_mul_f32 v[60:61], v[160:161], v[60:61]
	v_pk_mul_f32 v[62:63], v[162:163], v[62:63]
	s_waitcnt vmcnt(6)
	v_pk_mul_f32 v[226:227], v[48:49], v[172:173]
	v_pk_mul_f32 v[228:229], v[50:51], v[174:175]
	v_pk_mul_f32 v[230:231], v[52:53], v[176:177]
	v_pk_mul_f32 v[232:233], v[54:55], v[178:179]
	v_mov_b64_e32 v[244:245], v[226:227]
	v_mov_b64_e32 v[246:247], v[228:229]
	v_mov_b64_e32 v[248:249], v[230:231]
	v_mov_b64_e32 v[250:251], v[232:233]
	v_permlane32_swap_b32_e32 v226, v244
	v_permlane32_swap_b32_e32 v227, v245
	v_permlane32_swap_b32_e32 v228, v246
	v_permlane32_swap_b32_e32 v229, v247
	v_permlane32_swap_b32_e32 v230, v248
	v_permlane32_swap_b32_e32 v231, v249
	v_permlane32_swap_b32_e32 v232, v250
	v_permlane32_swap_b32_e32 v233, v251
	v_cndmask_b32_e64 v244, v226, -v244, s[36:37]
	v_cndmask_b32_e64 v245, v227, -v245, s[36:37]
	v_cndmask_b32_e64 v246, v228, -v246, s[36:37]
	v_cndmask_b32_e64 v247, v229, -v247, s[36:37]
	v_cndmask_b32_e64 v248, v230, -v248, s[36:37]
	v_cndmask_b32_e64 v249, v231, -v249, s[36:37]
	v_cndmask_b32_e64 v250, v232, -v250, s[36:37]
	v_cndmask_b32_e64 v251, v233, -v251, s[36:37]
	v_pk_fma_f32 v[48:49], v[48:49], v[164:165], v[244:245]
	v_pk_fma_f32 v[50:51], v[50:51], v[166:167], v[246:247]
	v_pk_fma_f32 v[52:53], v[52:53], v[168:169], v[248:249]
	v_pk_fma_f32 v[54:55], v[54:55], v[170:171], v[250:251]
	v_pk_mul_f32 v[226:227], v[56:57], v[202:203]
	v_pk_mul_f32 v[228:229], v[58:59], v[204:205]
	v_pk_mul_f32 v[230:231], v[60:61], v[206:207]
	v_pk_mul_f32 v[232:233], v[62:63], v[208:209]
	v_mov_b64_e32 v[244:245], v[226:227]
	v_mov_b64_e32 v[246:247], v[228:229]
	v_mov_b64_e32 v[248:249], v[230:231]
	v_mov_b64_e32 v[250:251], v[232:233]
	v_permlane32_swap_b32_e32 v226, v244
	v_permlane32_swap_b32_e32 v227, v245
	v_permlane32_swap_b32_e32 v228, v246
	v_permlane32_swap_b32_e32 v229, v247
	v_permlane32_swap_b32_e32 v230, v248
	v_permlane32_swap_b32_e32 v231, v249
	v_permlane32_swap_b32_e32 v232, v250
	v_permlane32_swap_b32_e32 v233, v251
	v_cndmask_b32_e64 v244, v226, -v244, s[36:37]
	v_cndmask_b32_e64 v245, v227, -v245, s[36:37]
	v_cndmask_b32_e64 v246, v228, -v246, s[36:37]
	v_cndmask_b32_e64 v247, v229, -v247, s[36:37]
	v_cndmask_b32_e64 v248, v230, -v248, s[36:37]
	v_cndmask_b32_e64 v249, v231, -v249, s[36:37]
	v_cndmask_b32_e64 v250, v232, -v250, s[36:37]
	v_cndmask_b32_e64 v251, v233, -v251, s[36:37]
	v_pk_fma_f32 v[56:57], v[56:57], v[180:181], v[244:245]
	v_pk_fma_f32 v[58:59], v[58:59], v[182:183], v[246:247]
	v_pk_fma_f32 v[60:61], v[60:61], v[184:185], v[248:249]
	v_pk_fma_f32 v[62:63], v[62:63], v[186:187], v[250:251]
	global_load_dwordx4 v[180:183], v136, s[6:7] offset:2048
	global_load_dwordx4 v[184:187], v136, s[6:7] offset:2064
	global_load_dwordx4 v[202:205], v137, s[6:7] offset:2048
	global_load_dwordx4 v[206:209], v137, s[6:7] offset:2064
	v_cvt_pk_bf16_f32 v48, v48, v49
	v_cvt_pk_bf16_f32 v49, v50, v51
	v_cvt_pk_bf16_f32 v50, v52, v53
	v_cvt_pk_bf16_f32 v51, v54, v55
	global_store_dwordx4 v114, v[48:51], s[26:27]
	v_cvt_pk_bf16_f32 v56, v56, v57
	v_cvt_pk_bf16_f32 v57, v58, v59
	v_cvt_pk_bf16_f32 v58, v60, v61
	v_cvt_pk_bf16_f32 v59, v62, v63
	global_store_dwordx4 v114, v[56:59], s[26:27] offset:64
	s_add_u32 s26, s26, 0x12000
	s_addc_u32 s27, s27, 0
	v_pk_mul_f32 v[132:133], v[32:33], v[32:33]
	v_pk_mul_f32 v[134:135], v[40:41], v[40:41]
	v_pk_fma_f32 v[132:133], v[34:35], v[34:35], v[132:133]
	v_pk_fma_f32 v[134:135], v[42:43], v[42:43], v[134:135]
	v_pk_fma_f32 v[132:133], v[36:37], v[36:37], v[132:133]
	v_pk_fma_f32 v[134:135], v[44:45], v[44:45], v[134:135]
	v_pk_fma_f32 v[132:133], v[38:39], v[38:39], v[132:133]
	v_pk_fma_f32 v[134:135], v[46:47], v[46:47], v[134:135]
	v_pk_add_f32 v[132:133], v[132:133], v[134:135]
	s_nop 0
	v_add_f32_e32 v194, v132, v133
	ds_swizzle_b32 v195, v194 offset:swizzle(SWAP,16)
	s_waitcnt lgkmcnt(0)
	v_add_f32_e32 v194, v194, v195
	v_mov_b32_e32 v195, v194
	s_nop 1
	v_permlane32_swap_b32_e32 v194, v195
	v_add_f32_e32 v194, v194, v195
	v_fmamk_f32 v194, v194, 0x3c800000, v192
	v_rsq_f32_e32 v194, v194
	s_nop 0
	v_mul_f32_e32 v196, v146, v194
	v_pk_mul_f32 v[32:33], v[32:33], v[196:197] op_sel_hi:[1,0]
	v_pk_mul_f32 v[34:35], v[34:35], v[196:197] op_sel_hi:[1,0]
	v_pk_mul_f32 v[36:37], v[36:37], v[196:197] op_sel_hi:[1,0]
	v_pk_mul_f32 v[38:39], v[38:39], v[196:197] op_sel_hi:[1,0]
	v_pk_mul_f32 v[40:41], v[40:41], v[196:197] op_sel_hi:[1,0]
	v_pk_mul_f32 v[42:43], v[42:43], v[196:197] op_sel_hi:[1,0]
	v_pk_mul_f32 v[44:45], v[44:45], v[196:197] op_sel_hi:[1,0]
	v_pk_mul_f32 v[46:47], v[46:47], v[196:197] op_sel_hi:[1,0]
	v_pk_mul_f32 v[32:33], v[148:149], v[32:33]
	v_pk_mul_f32 v[34:35], v[150:151], v[34:35]
	v_pk_mul_f32 v[36:37], v[152:153], v[36:37]
	v_pk_mul_f32 v[38:39], v[154:155], v[38:39]
	v_pk_mul_f32 v[40:41], v[156:157], v[40:41]
	v_pk_mul_f32 v[42:43], v[158:159], v[42:43]
	v_pk_mul_f32 v[44:45], v[160:161], v[44:45]
	v_pk_mul_f32 v[46:47], v[162:163], v[46:47]
	v_pk_mul_f32 v[226:227], v[32:33], v[172:173]
	v_pk_mul_f32 v[228:229], v[34:35], v[174:175]
	v_pk_mul_f32 v[230:231], v[36:37], v[176:177]
	v_pk_mul_f32 v[232:233], v[38:39], v[178:179]
	v_mov_b64_e32 v[244:245], v[226:227]
	v_mov_b64_e32 v[246:247], v[228:229]
	v_mov_b64_e32 v[248:249], v[230:231]
	v_mov_b64_e32 v[250:251], v[232:233]
	v_permlane32_swap_b32_e32 v226, v244
	v_permlane32_swap_b32_e32 v227, v245
	v_permlane32_swap_b32_e32 v228, v246
	v_permlane32_swap_b32_e32 v229, v247
	v_permlane32_swap_b32_e32 v230, v248
	v_permlane32_swap_b32_e32 v231, v249
	v_permlane32_swap_b32_e32 v232, v250
	v_permlane32_swap_b32_e32 v233, v251
	v_cndmask_b32_e64 v244, v226, -v244, s[36:37]
	v_cndmask_b32_e64 v245, v227, -v245, s[36:37]
	v_cndmask_b32_e64 v246, v228, -v246, s[36:37]
	v_cndmask_b32_e64 v247, v229, -v247, s[36:37]
	v_cndmask_b32_e64 v248, v230, -v248, s[36:37]
	v_cndmask_b32_e64 v249, v231, -v249, s[36:37]
	v_cndmask_b32_e64 v250, v232, -v250, s[36:37]
	v_cndmask_b32_e64 v251, v233, -v251, s[36:37]
	v_pk_fma_f32 v[32:33], v[32:33], v[164:165], v[244:245]
	v_pk_fma_f32 v[34:35], v[34:35], v[166:167], v[246:247]
	v_pk_fma_f32 v[36:37], v[36:37], v[168:169], v[248:249]
	v_pk_fma_f32 v[38:39], v[38:39], v[170:171], v[250:251]
	s_waitcnt vmcnt(8)
	v_pk_mul_f32 v[226:227], v[40:41], v[218:219]
	v_pk_mul_f32 v[228:229], v[42:43], v[220:221]
	v_pk_mul_f32 v[230:231], v[44:45], v[222:223]
	v_pk_mul_f32 v[232:233], v[46:47], v[224:225]
	v_mov_b64_e32 v[244:245], v[226:227]
	v_mov_b64_e32 v[246:247], v[228:229]
	v_mov_b64_e32 v[248:249], v[230:231]
	v_mov_b64_e32 v[250:251], v[232:233]
	v_permlane32_swap_b32_e32 v226, v244
	v_permlane32_swap_b32_e32 v227, v245
	v_permlane32_swap_b32_e32 v228, v246
	v_permlane32_swap_b32_e32 v229, v247
	v_permlane32_swap_b32_e32 v230, v248
	v_permlane32_swap_b32_e32 v231, v249
	v_permlane32_swap_b32_e32 v232, v250
	v_permlane32_swap_b32_e32 v233, v251
	v_cndmask_b32_e64 v244, v226, -v244, s[36:37]
	v_cndmask_b32_e64 v245, v227, -v245, s[36:37]
	v_cndmask_b32_e64 v246, v228, -v246, s[36:37]
	v_cndmask_b32_e64 v247, v229, -v247, s[36:37]
	v_cndmask_b32_e64 v248, v230, -v248, s[36:37]
	v_cndmask_b32_e64 v249, v231, -v249, s[36:37]
	v_cndmask_b32_e64 v250, v232, -v250, s[36:37]
	v_cndmask_b32_e64 v251, v233, -v251, s[36:37]
	v_pk_fma_f32 v[40:41], v[40:41], v[210:211], v[244:245]
	v_pk_fma_f32 v[42:43], v[42:43], v[212:213], v[246:247]
	v_pk_fma_f32 v[44:45], v[44:45], v[214:215], v[248:249]
	v_pk_fma_f32 v[46:47], v[46:47], v[216:217], v[250:251]
	global_load_dwordx4 v[210:213], v136, s[6:7] offset:3072
	global_load_dwordx4 v[214:217], v136, s[6:7] offset:3088
	global_load_dwordx4 v[218:221], v137, s[6:7] offset:3072
	global_load_dwordx4 v[222:225], v137, s[6:7] offset:3088
	v_cvt_pk_bf16_f32 v32, v32, v33
	v_cvt_pk_bf16_f32 v33, v34, v35
	v_cvt_pk_bf16_f32 v34, v36, v37
	v_cvt_pk_bf16_f32 v35, v38, v39
	global_store_dwordx4 v114, v[32:35], s[26:27]
	v_cvt_pk_bf16_f32 v40, v40, v41
	v_cvt_pk_bf16_f32 v41, v42, v43
	v_cvt_pk_bf16_f32 v42, v44, v45
	v_cvt_pk_bf16_f32 v43, v46, v47
	global_store_dwordx4 v114, v[40:43], s[26:27] offset:64
	s_add_u32 s26, s26, 0x12000
	s_addc_u32 s27, s27, 0
	v_pk_mul_f32 v[132:133], v[16:17], v[16:17]
	v_pk_mul_f32 v[134:135], v[24:25], v[24:25]
	v_pk_fma_f32 v[132:133], v[18:19], v[18:19], v[132:133]
	v_pk_fma_f32 v[134:135], v[26:27], v[26:27], v[134:135]
	v_pk_fma_f32 v[132:133], v[20:21], v[20:21], v[132:133]
	v_pk_fma_f32 v[134:135], v[28:29], v[28:29], v[134:135]
	v_pk_fma_f32 v[132:133], v[22:23], v[22:23], v[132:133]
	v_pk_fma_f32 v[134:135], v[30:31], v[30:31], v[134:135]
	v_pk_add_f32 v[132:133], v[132:133], v[134:135]
	s_nop 0
	v_add_f32_e32 v194, v132, v133
	ds_swizzle_b32 v195, v194 offset:swizzle(SWAP,16)
	s_waitcnt lgkmcnt(0)
	v_add_f32_e32 v194, v194, v195
	v_mov_b32_e32 v195, v194
	s_nop 1
	v_permlane32_swap_b32_e32 v194, v195
	v_add_f32_e32 v194, v194, v195
	v_fmamk_f32 v194, v194, 0x3c800000, v192
	v_rsq_f32_e32 v194, v194
	s_nop 0
	v_mul_f32_e32 v196, v146, v194
	v_pk_mul_f32 v[16:17], v[16:17], v[196:197] op_sel_hi:[1,0]
	v_pk_mul_f32 v[18:19], v[18:19], v[196:197] op_sel_hi:[1,0]
	v_pk_mul_f32 v[20:21], v[20:21], v[196:197] op_sel_hi:[1,0]
	v_pk_mul_f32 v[22:23], v[22:23], v[196:197] op_sel_hi:[1,0]
	v_pk_mul_f32 v[24:25], v[24:25], v[196:197] op_sel_hi:[1,0]
	v_pk_mul_f32 v[26:27], v[26:27], v[196:197] op_sel_hi:[1,0]
	v_pk_mul_f32 v[28:29], v[28:29], v[196:197] op_sel_hi:[1,0]
	v_pk_mul_f32 v[30:31], v[30:31], v[196:197] op_sel_hi:[1,0]
	v_pk_mul_f32 v[16:17], v[148:149], v[16:17]
	v_pk_mul_f32 v[18:19], v[150:151], v[18:19]
	v_pk_mul_f32 v[20:21], v[152:153], v[20:21]
	v_pk_mul_f32 v[22:23], v[154:155], v[22:23]
	v_pk_mul_f32 v[24:25], v[156:157], v[24:25]
	v_pk_mul_f32 v[26:27], v[158:159], v[26:27]
	v_pk_mul_f32 v[28:29], v[160:161], v[28:29]
	v_pk_mul_f32 v[30:31], v[162:163], v[30:31]
	v_pk_mul_f32 v[226:227], v[16:17], v[172:173]
	v_pk_mul_f32 v[228:229], v[18:19], v[174:175]
	v_pk_mul_f32 v[230:231], v[20:21], v[176:177]
	v_pk_mul_f32 v[232:233], v[22:23], v[178:179]
	v_mov_b64_e32 v[244:245], v[226:227]
	v_mov_b64_e32 v[246:247], v[228:229]
	v_mov_b64_e32 v[248:249], v[230:231]
	v_mov_b64_e32 v[250:251], v[232:233]
	v_permlane32_swap_b32_e32 v226, v244
	v_permlane32_swap_b32_e32 v227, v245
	v_permlane32_swap_b32_e32 v228, v246
	v_permlane32_swap_b32_e32 v229, v247
	v_permlane32_swap_b32_e32 v230, v248
	v_permlane32_swap_b32_e32 v231, v249
	v_permlane32_swap_b32_e32 v232, v250
	v_permlane32_swap_b32_e32 v233, v251
	v_cndmask_b32_e64 v244, v226, -v244, s[36:37]
	v_cndmask_b32_e64 v245, v227, -v245, s[36:37]
	v_cndmask_b32_e64 v246, v228, -v246, s[36:37]
	v_cndmask_b32_e64 v247, v229, -v247, s[36:37]
	v_cndmask_b32_e64 v248, v230, -v248, s[36:37]
	v_cndmask_b32_e64 v249, v231, -v249, s[36:37]
	v_cndmask_b32_e64 v250, v232, -v250, s[36:37]
	v_cndmask_b32_e64 v251, v233, -v251, s[36:37]
	v_pk_fma_f32 v[16:17], v[16:17], v[164:165], v[244:245]
	v_pk_fma_f32 v[18:19], v[18:19], v[166:167], v[246:247]
	v_pk_fma_f32 v[20:21], v[20:21], v[168:169], v[248:249]
	v_pk_fma_f32 v[22:23], v[22:23], v[170:171], v[250:251]
	s_waitcnt vmcnt(8)
	v_pk_mul_f32 v[226:227], v[24:25], v[202:203]
	v_pk_mul_f32 v[228:229], v[26:27], v[204:205]
	v_pk_mul_f32 v[230:231], v[28:29], v[206:207]
	v_pk_mul_f32 v[232:233], v[30:31], v[208:209]
	v_mov_b64_e32 v[244:245], v[226:227]
	v_mov_b64_e32 v[246:247], v[228:229]
	v_mov_b64_e32 v[248:249], v[230:231]
	v_mov_b64_e32 v[250:251], v[232:233]
	v_permlane32_swap_b32_e32 v226, v244
	v_permlane32_swap_b32_e32 v227, v245
	v_permlane32_swap_b32_e32 v228, v246
	v_permlane32_swap_b32_e32 v229, v247
	v_permlane32_swap_b32_e32 v230, v248
	v_permlane32_swap_b32_e32 v231, v249
	v_permlane32_swap_b32_e32 v232, v250
	v_permlane32_swap_b32_e32 v233, v251
	v_cndmask_b32_e64 v244, v226, -v244, s[36:37]
	v_cndmask_b32_e64 v245, v227, -v245, s[36:37]
	v_cndmask_b32_e64 v246, v228, -v246, s[36:37]
	v_cndmask_b32_e64 v247, v229, -v247, s[36:37]
	v_cndmask_b32_e64 v248, v230, -v248, s[36:37]
	v_cndmask_b32_e64 v249, v231, -v249, s[36:37]
	v_cndmask_b32_e64 v250, v232, -v250, s[36:37]
	v_cndmask_b32_e64 v251, v233, -v251, s[36:37]
	v_pk_fma_f32 v[24:25], v[24:25], v[180:181], v[244:245]
	v_pk_fma_f32 v[26:27], v[26:27], v[182:183], v[246:247]
	v_pk_fma_f32 v[28:29], v[28:29], v[184:185], v[248:249]
	v_pk_fma_f32 v[30:31], v[30:31], v[186:187], v[250:251]
	v_cvt_pk_bf16_f32 v16, v16, v17
	v_cvt_pk_bf16_f32 v17, v18, v19
	v_cvt_pk_bf16_f32 v18, v20, v21
	v_cvt_pk_bf16_f32 v19, v22, v23
	global_store_dwordx4 v114, v[16:19], s[26:27]
	v_cvt_pk_bf16_f32 v24, v24, v25
	v_cvt_pk_bf16_f32 v25, v26, v27
	v_cvt_pk_bf16_f32 v26, v28, v29
	v_cvt_pk_bf16_f32 v27, v30, v31
	global_store_dwordx4 v114, v[24:27], s[26:27] offset:64
	s_add_u32 s26, s26, 0x12000
	s_addc_u32 s27, s27, 0
	v_pk_mul_f32 v[132:133], v[0:1], v[0:1]
	v_pk_mul_f32 v[134:135], v[8:9], v[8:9]
	v_pk_fma_f32 v[132:133], v[2:3], v[2:3], v[132:133]
	v_pk_fma_f32 v[134:135], v[10:11], v[10:11], v[134:135]
	v_pk_fma_f32 v[132:133], v[4:5], v[4:5], v[132:133]
	v_pk_fma_f32 v[134:135], v[12:13], v[12:13], v[134:135]
	v_pk_fma_f32 v[132:133], v[6:7], v[6:7], v[132:133]
	v_pk_fma_f32 v[134:135], v[14:15], v[14:15], v[134:135]
	v_pk_add_f32 v[132:133], v[132:133], v[134:135]
	s_nop 0
	v_add_f32_e32 v194, v132, v133
	ds_swizzle_b32 v195, v194 offset:swizzle(SWAP,16)
	s_waitcnt lgkmcnt(0)
	v_add_f32_e32 v194, v194, v195
	v_mov_b32_e32 v195, v194
	s_nop 1
	v_permlane32_swap_b32_e32 v194, v195
	v_add_f32_e32 v194, v194, v195
	v_fmamk_f32 v194, v194, 0x3c800000, v192
	v_rsq_f32_e32 v194, v194
	s_nop 0
	v_mul_f32_e32 v196, v146, v194
	v_pk_mul_f32 v[0:1], v[0:1], v[196:197] op_sel_hi:[1,0]
	v_pk_mul_f32 v[2:3], v[2:3], v[196:197] op_sel_hi:[1,0]
	v_pk_mul_f32 v[4:5], v[4:5], v[196:197] op_sel_hi:[1,0]
	v_pk_mul_f32 v[6:7], v[6:7], v[196:197] op_sel_hi:[1,0]
	v_pk_mul_f32 v[8:9], v[8:9], v[196:197] op_sel_hi:[1,0]
	v_pk_mul_f32 v[10:11], v[10:11], v[196:197] op_sel_hi:[1,0]
	v_pk_mul_f32 v[12:13], v[12:13], v[196:197] op_sel_hi:[1,0]
	v_pk_mul_f32 v[14:15], v[14:15], v[196:197] op_sel_hi:[1,0]
	v_pk_mul_f32 v[0:1], v[148:149], v[0:1]
	v_pk_mul_f32 v[2:3], v[150:151], v[2:3]
	v_pk_mul_f32 v[4:5], v[152:153], v[4:5]
	v_pk_mul_f32 v[6:7], v[154:155], v[6:7]
	v_pk_mul_f32 v[8:9], v[156:157], v[8:9]
	v_pk_mul_f32 v[10:11], v[158:159], v[10:11]
	v_pk_mul_f32 v[12:13], v[160:161], v[12:13]
	v_pk_mul_f32 v[14:15], v[162:163], v[14:15]
	v_pk_mul_f32 v[226:227], v[0:1], v[172:173]
	v_pk_mul_f32 v[228:229], v[2:3], v[174:175]
	v_pk_mul_f32 v[230:231], v[4:5], v[176:177]
	v_pk_mul_f32 v[232:233], v[6:7], v[178:179]
	v_mov_b64_e32 v[244:245], v[226:227]
	v_mov_b64_e32 v[246:247], v[228:229]
	v_mov_b64_e32 v[248:249], v[230:231]
	v_mov_b64_e32 v[250:251], v[232:233]
	v_permlane32_swap_b32_e32 v226, v244
	v_permlane32_swap_b32_e32 v227, v245
	v_permlane32_swap_b32_e32 v228, v246
	v_permlane32_swap_b32_e32 v229, v247
	v_permlane32_swap_b32_e32 v230, v248
	v_permlane32_swap_b32_e32 v231, v249
	v_permlane32_swap_b32_e32 v232, v250
	v_permlane32_swap_b32_e32 v233, v251
	v_cndmask_b32_e64 v244, v226, -v244, s[36:37]
	v_cndmask_b32_e64 v245, v227, -v245, s[36:37]
	v_cndmask_b32_e64 v246, v228, -v246, s[36:37]
	v_cndmask_b32_e64 v247, v229, -v247, s[36:37]
	v_cndmask_b32_e64 v248, v230, -v248, s[36:37]
	v_cndmask_b32_e64 v249, v231, -v249, s[36:37]
	v_cndmask_b32_e64 v250, v232, -v250, s[36:37]
	v_cndmask_b32_e64 v251, v233, -v251, s[36:37]
	v_pk_fma_f32 v[0:1], v[0:1], v[164:165], v[244:245]
	v_pk_fma_f32 v[2:3], v[2:3], v[166:167], v[246:247]
	v_pk_fma_f32 v[4:5], v[4:5], v[168:169], v[248:249]
	v_pk_fma_f32 v[6:7], v[6:7], v[170:171], v[250:251]
	s_waitcnt vmcnt(4)
	v_pk_mul_f32 v[226:227], v[8:9], v[218:219]
	v_pk_mul_f32 v[228:229], v[10:11], v[220:221]
	v_pk_mul_f32 v[230:231], v[12:13], v[222:223]
	v_pk_mul_f32 v[232:233], v[14:15], v[224:225]
	v_mov_b64_e32 v[244:245], v[226:227]
	v_mov_b64_e32 v[246:247], v[228:229]
	v_mov_b64_e32 v[248:249], v[230:231]
	v_mov_b64_e32 v[250:251], v[232:233]
	v_permlane32_swap_b32_e32 v226, v244
	v_permlane32_swap_b32_e32 v227, v245
	v_permlane32_swap_b32_e32 v228, v246
	v_permlane32_swap_b32_e32 v229, v247
	v_permlane32_swap_b32_e32 v230, v248
	v_permlane32_swap_b32_e32 v231, v249
	v_permlane32_swap_b32_e32 v232, v250
	v_permlane32_swap_b32_e32 v233, v251
	v_cndmask_b32_e64 v244, v226, -v244, s[36:37]
	v_cndmask_b32_e64 v245, v227, -v245, s[36:37]
	v_cndmask_b32_e64 v246, v228, -v246, s[36:37]
	v_cndmask_b32_e64 v247, v229, -v247, s[36:37]
	v_cndmask_b32_e64 v248, v230, -v248, s[36:37]
	v_cndmask_b32_e64 v249, v231, -v249, s[36:37]
	v_cndmask_b32_e64 v250, v232, -v250, s[36:37]
	v_cndmask_b32_e64 v251, v233, -v251, s[36:37]
	v_pk_fma_f32 v[8:9], v[8:9], v[210:211], v[244:245]
	v_pk_fma_f32 v[10:11], v[10:11], v[212:213], v[246:247]
	v_pk_fma_f32 v[12:13], v[12:13], v[214:215], v[248:249]
	v_pk_fma_f32 v[14:15], v[14:15], v[216:217], v[250:251]
	v_cvt_pk_bf16_f32 v0, v0, v1
	v_cvt_pk_bf16_f32 v1, v2, v3
	v_cvt_pk_bf16_f32 v2, v4, v5
	v_cvt_pk_bf16_f32 v3, v6, v7
	global_store_dwordx4 v114, v[0:3], s[26:27]
	v_cvt_pk_bf16_f32 v8, v8, v9
	v_cvt_pk_bf16_f32 v9, v10, v11
	v_cvt_pk_bf16_f32 v10, v12, v13
	v_cvt_pk_bf16_f32 v11, v14, v15
	global_store_dwordx4 v114, v[8:11], s[26:27] offset:64
	s_branch .Lqkv_epi_done
.Lqkv_epi_norope:
	v_pk_mul_f32 v[132:133], v[116:117], v[116:117]
	v_pk_mul_f32 v[134:135], v[124:125], v[124:125]
	v_pk_fma_f32 v[132:133], v[118:119], v[118:119], v[132:133]
	v_pk_fma_f32 v[134:135], v[126:127], v[126:127], v[134:135]
	v_pk_fma_f32 v[132:133], v[120:121], v[120:121], v[132:133]
	v_pk_fma_f32 v[134:135], v[128:129], v[128:129], v[134:135]
	v_pk_fma_f32 v[132:133], v[122:123], v[122:123], v[132:133]
	v_pk_fma_f32 v[134:135], v[130:131], v[130:131], v[134:135]
	v_pk_add_f32 v[132:133], v[132:133], v[134:135]
	s_nop 0
	v_add_f32_e32 v194, v132, v133
	ds_swizzle_b32 v195, v194 offset:swizzle(SWAP,16)
	s_waitcnt lgkmcnt(0)
	v_add_f32_e32 v194, v194, v195
	v_mov_b32_e32 v195, v194
	s_nop 1
	v_permlane32_swap_b32_e32 v194, v195
	v_add_f32_e32 v194, v194, v195
	v_fmamk_f32 v194, v194, 0x3c800000, v192
	v_rsq_f32_e32 v194, v194
	s_nop 0
	v_mul_f32_e32 v196, v146, v194
	v_pk_mul_f32 v[116:117], v[116:117], v[196:197] op_sel_hi:[1,0]
	v_pk_mul_f32 v[118:119], v[118:119], v[196:197] op_sel_hi:[1,0]
	v_pk_mul_f32 v[120:121], v[120:121], v[196:197] op_sel_hi:[1,0]
	v_pk_mul_f32 v[122:123], v[122:123], v[196:197] op_sel_hi:[1,0]
	v_pk_mul_f32 v[124:125], v[124:125], v[196:197] op_sel_hi:[1,0]
	v_pk_mul_f32 v[126:127], v[126:127], v[196:197] op_sel_hi:[1,0]
	v_pk_mul_f32 v[128:129], v[128:129], v[196:197] op_sel_hi:[1,0]
	v_pk_mul_f32 v[130:131], v[130:131], v[196:197] op_sel_hi:[1,0]
	s_waitcnt vmcnt(0)
	v_pk_mul_f32 v[116:117], v[148:149], v[116:117]
	v_pk_mul_f32 v[118:119], v[150:151], v[118:119]
	v_pk_mul_f32 v[120:121], v[152:153], v[120:121]
	v_pk_mul_f32 v[122:123], v[154:155], v[122:123]
	v_pk_mul_f32 v[124:125], v[156:157], v[124:125]
	v_pk_mul_f32 v[126:127], v[158:159], v[126:127]
	v_pk_mul_f32 v[128:129], v[160:161], v[128:129]
	v_pk_mul_f32 v[130:131], v[162:163], v[130:131]
	v_cvt_pk_bf16_f32 v116, v116, v117
	v_cvt_pk_bf16_f32 v117, v118, v119
	v_cvt_pk_bf16_f32 v118, v120, v121
	v_cvt_pk_bf16_f32 v119, v122, v123
	global_store_dwordx4 v114, v[116:119], s[26:27]
	v_cvt_pk_bf16_f32 v124, v124, v125
	v_cvt_pk_bf16_f32 v125, v126, v127
	v_cvt_pk_bf16_f32 v126, v128, v129
	v_cvt_pk_bf16_f32 v127, v130, v131
	global_store_dwordx4 v114, v[124:127], s[26:27] offset:64
	s_add_u32 s26, s26, 0x12000
	s_addc_u32 s27, s27, 0
	v_pk_mul_f32 v[132:133], v[98:99], v[98:99]
	v_pk_mul_f32 v[134:135], v[106:107], v[106:107]
	v_pk_fma_f32 v[132:133], v[100:101], v[100:101], v[132:133]
	v_pk_fma_f32 v[134:135], v[108:109], v[108:109], v[134:135]
	v_pk_fma_f32 v[132:133], v[102:103], v[102:103], v[132:133]
	v_pk_fma_f32 v[134:135], v[110:111], v[110:111], v[134:135]
	v_pk_fma_f32 v[132:133], v[104:105], v[104:105], v[132:133]
	v_pk_fma_f32 v[134:135], v[112:113], v[112:113], v[134:135]
	v_pk_add_f32 v[132:133], v[132:133], v[134:135]
	s_nop 0
	v_add_f32_e32 v194, v132, v133
	ds_swizzle_b32 v195, v194 offset:swizzle(SWAP,16)
	s_waitcnt lgkmcnt(0)
	v_add_f32_e32 v194, v194, v195
	v_mov_b32_e32 v195, v194
	s_nop 1
	v_permlane32_swap_b32_e32 v194, v195
	v_add_f32_e32 v194, v194, v195
	v_fmamk_f32 v194, v194, 0x3c800000, v192
	v_rsq_f32_e32 v194, v194
	s_nop 0
	v_mul_f32_e32 v196, v146, v194
	v_pk_mul_f32 v[98:99], v[98:99], v[196:197] op_sel_hi:[1,0]
	v_pk_mul_f32 v[100:101], v[100:101], v[196:197] op_sel_hi:[1,0]
	v_pk_mul_f32 v[102:103], v[102:103], v[196:197] op_sel_hi:[1,0]
	v_pk_mul_f32 v[104:105], v[104:105], v[196:197] op_sel_hi:[1,0]
	v_pk_mul_f32 v[106:107], v[106:107], v[196:197] op_sel_hi:[1,0]
	v_pk_mul_f32 v[108:109], v[108:109], v[196:197] op_sel_hi:[1,0]
	v_pk_mul_f32 v[110:111], v[110:111], v[196:197] op_sel_hi:[1,0]
	v_pk_mul_f32 v[112:113], v[112:113], v[196:197] op_sel_hi:[1,0]
	v_pk_mul_f32 v[98:99], v[148:149], v[98:99]
	v_pk_mul_f32 v[100:101], v[150:151], v[100:101]
	v_pk_mul_f32 v[102:103], v[152:153], v[102:103]
	v_pk_mul_f32 v[104:105], v[154:155], v[104:105]
	v_pk_mul_f32 v[106:107], v[156:157], v[106:107]
	v_pk_mul_f32 v[108:109], v[158:159], v[108:109]
	v_pk_mul_f32 v[110:111], v[160:161], v[110:111]
	v_pk_mul_f32 v[112:113], v[162:163], v[112:113]
	v_cvt_pk_bf16_f32 v98, v98, v99
	v_cvt_pk_bf16_f32 v99, v100, v101
	v_cvt_pk_bf16_f32 v100, v102, v103
	v_cvt_pk_bf16_f32 v101, v104, v105
	global_store_dwordx4 v114, v[98:101], s[26:27]
	v_cvt_pk_bf16_f32 v106, v106, v107
	v_cvt_pk_bf16_f32 v107, v108, v109
	v_cvt_pk_bf16_f32 v108, v110, v111
	v_cvt_pk_bf16_f32 v109, v112, v113
	global_store_dwordx4 v114, v[106:109], s[26:27] offset:64
	s_add_u32 s26, s26, 0x12000
	s_addc_u32 s27, s27, 0
	v_pk_mul_f32 v[132:133], v[82:83], v[82:83]
	v_pk_mul_f32 v[134:135], v[90:91], v[90:91]
	v_pk_fma_f32 v[132:133], v[84:85], v[84:85], v[132:133]
	v_pk_fma_f32 v[134:135], v[92:93], v[92:93], v[134:135]
	v_pk_fma_f32 v[132:133], v[86:87], v[86:87], v[132:133]
	v_pk_fma_f32 v[134:135], v[94:95], v[94:95], v[134:135]
	v_pk_fma_f32 v[132:133], v[88:89], v[88:89], v[132:133]
	v_pk_fma_f32 v[134:135], v[96:97], v[96:97], v[134:135]
	v_pk_add_f32 v[132:133], v[132:133], v[134:135]
	s_nop 0
	v_add_f32_e32 v194, v132, v133
	ds_swizzle_b32 v195, v194 offset:swizzle(SWAP,16)
	s_waitcnt lgkmcnt(0)
	v_add_f32_e32 v194, v194, v195
	v_mov_b32_e32 v195, v194
	s_nop 1
	v_permlane32_swap_b32_e32 v194, v195
	v_add_f32_e32 v194, v194, v195
	v_fmamk_f32 v194, v194, 0x3c800000, v192
	v_rsq_f32_e32 v194, v194
	s_nop 0
	v_mul_f32_e32 v196, v146, v194
	v_pk_mul_f32 v[82:83], v[82:83], v[196:197] op_sel_hi:[1,0]
	v_pk_mul_f32 v[84:85], v[84:85], v[196:197] op_sel_hi:[1,0]
	v_pk_mul_f32 v[86:87], v[86:87], v[196:197] op_sel_hi:[1,0]
	v_pk_mul_f32 v[88:89], v[88:89], v[196:197] op_sel_hi:[1,0]
	v_pk_mul_f32 v[90:91], v[90:91], v[196:197] op_sel_hi:[1,0]
	v_pk_mul_f32 v[92:93], v[92:93], v[196:197] op_sel_hi:[1,0]
	v_pk_mul_f32 v[94:95], v[94:95], v[196:197] op_sel_hi:[1,0]
	v_pk_mul_f32 v[96:97], v[96:97], v[196:197] op_sel_hi:[1,0]
	v_pk_mul_f32 v[82:83], v[148:149], v[82:83]
	v_pk_mul_f32 v[84:85], v[150:151], v[84:85]
	v_pk_mul_f32 v[86:87], v[152:153], v[86:87]
	v_pk_mul_f32 v[88:89], v[154:155], v[88:89]
	v_pk_mul_f32 v[90:91], v[156:157], v[90:91]
	v_pk_mul_f32 v[92:93], v[158:159], v[92:93]
	v_pk_mul_f32 v[94:95], v[160:161], v[94:95]
	v_pk_mul_f32 v[96:97], v[162:163], v[96:97]
	v_cvt_pk_bf16_f32 v82, v82, v83
	v_cvt_pk_bf16_f32 v83, v84, v85
	v_cvt_pk_bf16_f32 v84, v86, v87
	v_cvt_pk_bf16_f32 v85, v88, v89
	global_store_dwordx4 v114, v[82:85], s[26:27]
	v_cvt_pk_bf16_f32 v90, v90, v91
	v_cvt_pk_bf16_f32 v91, v92, v93
	v_cvt_pk_bf16_f32 v92, v94, v95
	v_cvt_pk_bf16_f32 v93, v96, v97
	global_store_dwordx4 v114, v[90:93], s[26:27] offset:64
	s_add_u32 s26, s26, 0x12000
	s_addc_u32 s27, s27, 0
	v_pk_mul_f32 v[132:133], v[66:67], v[66:67]
	v_pk_mul_f32 v[134:135], v[74:75], v[74:75]
	v_pk_fma_f32 v[132:133], v[68:69], v[68:69], v[132:133]
	v_pk_fma_f32 v[134:135], v[76:77], v[76:77], v[134:135]
	v_pk_fma_f32 v[132:133], v[70:71], v[70:71], v[132:133]
	v_pk_fma_f32 v[134:135], v[78:79], v[78:79], v[134:135]
	v_pk_fma_f32 v[132:133], v[72:73], v[72:73], v[132:133]
	v_pk_fma_f32 v[134:135], v[80:81], v[80:81], v[134:135]
	v_pk_add_f32 v[132:133], v[132:133], v[134:135]
	s_nop 0
	v_add_f32_e32 v194, v132, v133
	ds_swizzle_b32 v195, v194 offset:swizzle(SWAP,16)
	s_waitcnt lgkmcnt(0)
	v_add_f32_e32 v194, v194, v195
	v_mov_b32_e32 v195, v194
	s_nop 1
	v_permlane32_swap_b32_e32 v194, v195
	v_add_f32_e32 v194, v194, v195
	v_fmamk_f32 v194, v194, 0x3c800000, v192
	v_rsq_f32_e32 v194, v194
	s_nop 0
	v_mul_f32_e32 v196, v146, v194
	v_pk_mul_f32 v[66:67], v[66:67], v[196:197] op_sel_hi:[1,0]
	v_pk_mul_f32 v[68:69], v[68:69], v[196:197] op_sel_hi:[1,0]
	v_pk_mul_f32 v[70:71], v[70:71], v[196:197] op_sel_hi:[1,0]
	v_pk_mul_f32 v[72:73], v[72:73], v[196:197] op_sel_hi:[1,0]
	v_pk_mul_f32 v[74:75], v[74:75], v[196:197] op_sel_hi:[1,0]
	v_pk_mul_f32 v[76:77], v[76:77], v[196:197] op_sel_hi:[1,0]
	v_pk_mul_f32 v[78:79], v[78:79], v[196:197] op_sel_hi:[1,0]
	v_pk_mul_f32 v[80:81], v[80:81], v[196:197] op_sel_hi:[1,0]
	v_pk_mul_f32 v[66:67], v[148:149], v[66:67]
	v_pk_mul_f32 v[68:69], v[150:151], v[68:69]
	v_pk_mul_f32 v[70:71], v[152:153], v[70:71]
	v_pk_mul_f32 v[72:73], v[154:155], v[72:73]
	v_pk_mul_f32 v[74:75], v[156:157], v[74:75]
	v_pk_mul_f32 v[76:77], v[158:159], v[76:77]
	v_pk_mul_f32 v[78:79], v[160:161], v[78:79]
	v_pk_mul_f32 v[80:81], v[162:163], v[80:81]
	v_cvt_pk_bf16_f32 v66, v66, v67
	v_cvt_pk_bf16_f32 v67, v68, v69
	v_cvt_pk_bf16_f32 v68, v70, v71
	v_cvt_pk_bf16_f32 v69, v72, v73
	global_store_dwordx4 v114, v[66:69], s[26:27]
	v_cvt_pk_bf16_f32 v74, v74, v75
	v_cvt_pk_bf16_f32 v75, v76, v77
	v_cvt_pk_bf16_f32 v76, v78, v79
	v_cvt_pk_bf16_f32 v77, v80, v81
	global_store_dwordx4 v114, v[74:77], s[26:27] offset:64
	s_add_u32 s26, s26, 0x5a000
	s_addc_u32 s27, s27, 0
	v_pk_mul_f32 v[132:133], v[48:49], v[48:49]
	v_pk_mul_f32 v[134:135], v[56:57], v[56:57]
	v_pk_fma_f32 v[132:133], v[50:51], v[50:51], v[132:133]
	v_pk_fma_f32 v[134:135], v[58:59], v[58:59], v[134:135]
	v_pk_fma_f32 v[132:133], v[52:53], v[52:53], v[132:133]
	v_pk_fma_f32 v[134:135], v[60:61], v[60:61], v[134:135]
	v_pk_fma_f32 v[132:133], v[54:55], v[54:55], v[132:133]
	v_pk_fma_f32 v[134:135], v[62:63], v[62:63], v[134:135]
	v_pk_add_f32 v[132:133], v[132:133], v[134:135]
	s_nop 0
	v_add_f32_e32 v194, v132, v133
	ds_swizzle_b32 v195, v194 offset:swizzle(SWAP,16)
	s_waitcnt lgkmcnt(0)
	v_add_f32_e32 v194, v194, v195
	v_mov_b32_e32 v195, v194
	s_nop 1
	v_permlane32_swap_b32_e32 v194, v195
	v_add_f32_e32 v194, v194, v195
	v_fmamk_f32 v194, v194, 0x3c800000, v192
	v_rsq_f32_e32 v194, v194
	s_nop 0
	v_mul_f32_e32 v196, v146, v194
	v_pk_mul_f32 v[48:49], v[48:49], v[196:197] op_sel_hi:[1,0]
	v_pk_mul_f32 v[50:51], v[50:51], v[196:197] op_sel_hi:[1,0]
	v_pk_mul_f32 v[52:53], v[52:53], v[196:197] op_sel_hi:[1,0]
	v_pk_mul_f32 v[54:55], v[54:55], v[196:197] op_sel_hi:[1,0]
	v_pk_mul_f32 v[56:57], v[56:57], v[196:197] op_sel_hi:[1,0]
	v_pk_mul_f32 v[58:59], v[58:59], v[196:197] op_sel_hi:[1,0]
	v_pk_mul_f32 v[60:61], v[60:61], v[196:197] op_sel_hi:[1,0]
	v_pk_mul_f32 v[62:63], v[62:63], v[196:197] op_sel_hi:[1,0]
	v_pk_mul_f32 v[48:49], v[148:149], v[48:49]
	v_pk_mul_f32 v[50:51], v[150:151], v[50:51]
	v_pk_mul_f32 v[52:53], v[152:153], v[52:53]
	v_pk_mul_f32 v[54:55], v[154:155], v[54:55]
	v_pk_mul_f32 v[56:57], v[156:157], v[56:57]
	v_pk_mul_f32 v[58:59], v[158:159], v[58:59]
	v_pk_mul_f32 v[60:61], v[160:161], v[60:61]
	v_pk_mul_f32 v[62:63], v[162:163], v[62:63]
	v_cvt_pk_bf16_f32 v48, v48, v49
	v_cvt_pk_bf16_f32 v49, v50, v51
	v_cvt_pk_bf16_f32 v50, v52, v53
	v_cvt_pk_bf16_f32 v51, v54, v55
	global_store_dwordx4 v114, v[48:51], s[26:27]
	v_cvt_pk_bf16_f32 v56, v56, v57
	v_cvt_pk_bf16_f32 v57, v58, v59
	v_cvt_pk_bf16_f32 v58, v60, v61
	v_cvt_pk_bf16_f32 v59, v62, v63
	global_store_dwordx4 v114, v[56:59], s[26:27] offset:64
	s_add_u32 s26, s26, 0x12000
	s_addc_u32 s27, s27, 0
	v_pk_mul_f32 v[132:133], v[32:33], v[32:33]
	v_pk_mul_f32 v[134:135], v[40:41], v[40:41]
	v_pk_fma_f32 v[132:133], v[34:35], v[34:35], v[132:133]
	v_pk_fma_f32 v[134:135], v[42:43], v[42:43], v[134:135]
	v_pk_fma_f32 v[132:133], v[36:37], v[36:37], v[132:133]
	v_pk_fma_f32 v[134:135], v[44:45], v[44:45], v[134:135]
	v_pk_fma_f32 v[132:133], v[38:39], v[38:39], v[132:133]
	v_pk_fma_f32 v[134:135], v[46:47], v[46:47], v[134:135]
	v_pk_add_f32 v[132:133], v[132:133], v[134:135]
	s_nop 0
	v_add_f32_e32 v194, v132, v133
	ds_swizzle_b32 v195, v194 offset:swizzle(SWAP,16)
	s_waitcnt lgkmcnt(0)
	v_add_f32_e32 v194, v194, v195
	v_mov_b32_e32 v195, v194
	s_nop 1
	v_permlane32_swap_b32_e32 v194, v195
	v_add_f32_e32 v194, v194, v195
	v_fmamk_f32 v194, v194, 0x3c800000, v192
	v_rsq_f32_e32 v194, v194
	s_nop 0
	v_mul_f32_e32 v196, v146, v194
	v_pk_mul_f32 v[32:33], v[32:33], v[196:197] op_sel_hi:[1,0]
	v_pk_mul_f32 v[34:35], v[34:35], v[196:197] op_sel_hi:[1,0]
	v_pk_mul_f32 v[36:37], v[36:37], v[196:197] op_sel_hi:[1,0]
	v_pk_mul_f32 v[38:39], v[38:39], v[196:197] op_sel_hi:[1,0]
	v_pk_mul_f32 v[40:41], v[40:41], v[196:197] op_sel_hi:[1,0]
	v_pk_mul_f32 v[42:43], v[42:43], v[196:197] op_sel_hi:[1,0]
	v_pk_mul_f32 v[44:45], v[44:45], v[196:197] op_sel_hi:[1,0]
	v_pk_mul_f32 v[46:47], v[46:47], v[196:197] op_sel_hi:[1,0]
	v_pk_mul_f32 v[32:33], v[148:149], v[32:33]
	v_pk_mul_f32 v[34:35], v[150:151], v[34:35]
	v_pk_mul_f32 v[36:37], v[152:153], v[36:37]
	v_pk_mul_f32 v[38:39], v[154:155], v[38:39]
	v_pk_mul_f32 v[40:41], v[156:157], v[40:41]
	v_pk_mul_f32 v[42:43], v[158:159], v[42:43]
	v_pk_mul_f32 v[44:45], v[160:161], v[44:45]
	v_pk_mul_f32 v[46:47], v[162:163], v[46:47]
	v_cvt_pk_bf16_f32 v32, v32, v33
	v_cvt_pk_bf16_f32 v33, v34, v35
	v_cvt_pk_bf16_f32 v34, v36, v37
	v_cvt_pk_bf16_f32 v35, v38, v39
	global_store_dwordx4 v114, v[32:35], s[26:27]
	v_cvt_pk_bf16_f32 v40, v40, v41
	v_cvt_pk_bf16_f32 v41, v42, v43
	v_cvt_pk_bf16_f32 v42, v44, v45
	v_cvt_pk_bf16_f32 v43, v46, v47
	global_store_dwordx4 v114, v[40:43], s[26:27] offset:64
	s_add_u32 s26, s26, 0x12000
	s_addc_u32 s27, s27, 0
	v_pk_mul_f32 v[132:133], v[16:17], v[16:17]
	v_pk_mul_f32 v[134:135], v[24:25], v[24:25]
	v_pk_fma_f32 v[132:133], v[18:19], v[18:19], v[132:133]
	v_pk_fma_f32 v[134:135], v[26:27], v[26:27], v[134:135]
	v_pk_fma_f32 v[132:133], v[20:21], v[20:21], v[132:133]
	v_pk_fma_f32 v[134:135], v[28:29], v[28:29], v[134:135]
	v_pk_fma_f32 v[132:133], v[22:23], v[22:23], v[132:133]
	v_pk_fma_f32 v[134:135], v[30:31], v[30:31], v[134:135]
	v_pk_add_f32 v[132:133], v[132:133], v[134:135]
	s_nop 0
	v_add_f32_e32 v194, v132, v133
	ds_swizzle_b32 v195, v194 offset:swizzle(SWAP,16)
	s_waitcnt lgkmcnt(0)
	v_add_f32_e32 v194, v194, v195
	v_mov_b32_e32 v195, v194
	s_nop 1
	v_permlane32_swap_b32_e32 v194, v195
	v_add_f32_e32 v194, v194, v195
	v_fmamk_f32 v194, v194, 0x3c800000, v192
	v_rsq_f32_e32 v194, v194
	s_nop 0
	v_mul_f32_e32 v196, v146, v194
	v_pk_mul_f32 v[16:17], v[16:17], v[196:197] op_sel_hi:[1,0]
	v_pk_mul_f32 v[18:19], v[18:19], v[196:197] op_sel_hi:[1,0]
	v_pk_mul_f32 v[20:21], v[20:21], v[196:197] op_sel_hi:[1,0]
	v_pk_mul_f32 v[22:23], v[22:23], v[196:197] op_sel_hi:[1,0]
	v_pk_mul_f32 v[24:25], v[24:25], v[196:197] op_sel_hi:[1,0]
	v_pk_mul_f32 v[26:27], v[26:27], v[196:197] op_sel_hi:[1,0]
	v_pk_mul_f32 v[28:29], v[28:29], v[196:197] op_sel_hi:[1,0]
	v_pk_mul_f32 v[30:31], v[30:31], v[196:197] op_sel_hi:[1,0]
	v_pk_mul_f32 v[16:17], v[148:149], v[16:17]
	v_pk_mul_f32 v[18:19], v[150:151], v[18:19]
	v_pk_mul_f32 v[20:21], v[152:153], v[20:21]
	v_pk_mul_f32 v[22:23], v[154:155], v[22:23]
	v_pk_mul_f32 v[24:25], v[156:157], v[24:25]
	v_pk_mul_f32 v[26:27], v[158:159], v[26:27]
	v_pk_mul_f32 v[28:29], v[160:161], v[28:29]
	v_pk_mul_f32 v[30:31], v[162:163], v[30:31]
	v_cvt_pk_bf16_f32 v16, v16, v17
	v_cvt_pk_bf16_f32 v17, v18, v19
	v_cvt_pk_bf16_f32 v18, v20, v21
	v_cvt_pk_bf16_f32 v19, v22, v23
	global_store_dwordx4 v114, v[16:19], s[26:27]
	v_cvt_pk_bf16_f32 v24, v24, v25
	v_cvt_pk_bf16_f32 v25, v26, v27
	v_cvt_pk_bf16_f32 v26, v28, v29
	v_cvt_pk_bf16_f32 v27, v30, v31
	global_store_dwordx4 v114, v[24:27], s[26:27] offset:64
	s_add_u32 s26, s26, 0x12000
	s_addc_u32 s27, s27, 0
	v_pk_mul_f32 v[132:133], v[0:1], v[0:1]
	v_pk_mul_f32 v[134:135], v[8:9], v[8:9]
	v_pk_fma_f32 v[132:133], v[2:3], v[2:3], v[132:133]
	v_pk_fma_f32 v[134:135], v[10:11], v[10:11], v[134:135]
	v_pk_fma_f32 v[132:133], v[4:5], v[4:5], v[132:133]
	v_pk_fma_f32 v[134:135], v[12:13], v[12:13], v[134:135]
	v_pk_fma_f32 v[132:133], v[6:7], v[6:7], v[132:133]
	v_pk_fma_f32 v[134:135], v[14:15], v[14:15], v[134:135]
	v_pk_add_f32 v[132:133], v[132:133], v[134:135]
	s_nop 0
	v_add_f32_e32 v194, v132, v133
	ds_swizzle_b32 v195, v194 offset:swizzle(SWAP,16)
	s_waitcnt lgkmcnt(0)
	v_add_f32_e32 v194, v194, v195
	v_mov_b32_e32 v195, v194
	s_nop 1
	v_permlane32_swap_b32_e32 v194, v195
	v_add_f32_e32 v194, v194, v195
	v_fmamk_f32 v194, v194, 0x3c800000, v192
	v_rsq_f32_e32 v194, v194
	s_nop 0
	v_mul_f32_e32 v196, v146, v194
	v_pk_mul_f32 v[0:1], v[0:1], v[196:197] op_sel_hi:[1,0]
	v_pk_mul_f32 v[2:3], v[2:3], v[196:197] op_sel_hi:[1,0]
	v_pk_mul_f32 v[4:5], v[4:5], v[196:197] op_sel_hi:[1,0]
	v_pk_mul_f32 v[6:7], v[6:7], v[196:197] op_sel_hi:[1,0]
	v_pk_mul_f32 v[8:9], v[8:9], v[196:197] op_sel_hi:[1,0]
	v_pk_mul_f32 v[10:11], v[10:11], v[196:197] op_sel_hi:[1,0]
	v_pk_mul_f32 v[12:13], v[12:13], v[196:197] op_sel_hi:[1,0]
	v_pk_mul_f32 v[14:15], v[14:15], v[196:197] op_sel_hi:[1,0]
	v_pk_mul_f32 v[0:1], v[148:149], v[0:1]
	v_pk_mul_f32 v[2:3], v[150:151], v[2:3]
	v_pk_mul_f32 v[4:5], v[152:153], v[4:5]
	v_pk_mul_f32 v[6:7], v[154:155], v[6:7]
	v_pk_mul_f32 v[8:9], v[156:157], v[8:9]
	v_pk_mul_f32 v[10:11], v[158:159], v[10:11]
	v_pk_mul_f32 v[12:13], v[160:161], v[12:13]
	v_pk_mul_f32 v[14:15], v[162:163], v[14:15]
	v_cvt_pk_bf16_f32 v0, v0, v1
	v_cvt_pk_bf16_f32 v1, v2, v3
	v_cvt_pk_bf16_f32 v2, v4, v5
	v_cvt_pk_bf16_f32 v3, v6, v7
	global_store_dwordx4 v114, v[0:3], s[26:27]
	v_cvt_pk_bf16_f32 v8, v8, v9
	v_cvt_pk_bf16_f32 v9, v10, v11
	v_cvt_pk_bf16_f32 v10, v12, v13
	v_cvt_pk_bf16_f32 v11, v14, v15
	global_store_dwordx4 v114, v[8:11], s[26:27] offset:64
	s_branch .Lqkv_epi_done
.Lqkv_epi_v:
	v_cvt_pk_bf16_f32 v116, v116, v117
	v_cvt_pk_bf16_f32 v117, v118, v119
	v_cvt_pk_bf16_f32 v118, v120, v121
	v_cvt_pk_bf16_f32 v119, v122, v123
	global_store_dwordx4 v114, v[116:119], s[26:27]
	v_cvt_pk_bf16_f32 v124, v124, v125
	v_cvt_pk_bf16_f32 v125, v126, v127
	v_cvt_pk_bf16_f32 v126, v128, v129
	v_cvt_pk_bf16_f32 v127, v130, v131
	global_store_dwordx4 v114, v[124:127], s[26:27] offset:64
	s_add_u32 s26, s26, 0x12000
	s_addc_u32 s27, s27, 0
	v_cvt_pk_bf16_f32 v98, v98, v99
	v_cvt_pk_bf16_f32 v99, v100, v101
	v_cvt_pk_bf16_f32 v100, v102, v103
	v_cvt_pk_bf16_f32 v101, v104, v105
	global_store_dwordx4 v114, v[98:101], s[26:27]
	v_cvt_pk_bf16_f32 v106, v106, v107
	v_cvt_pk_bf16_f32 v107, v108, v109
	v_cvt_pk_bf16_f32 v108, v110, v111
	v_cvt_pk_bf16_f32 v109, v112, v113
	global_store_dwordx4 v114, v[106:109], s[26:27] offset:64
	s_add_u32 s26, s26, 0x12000
	s_addc_u32 s27, s27, 0
	v_cvt_pk_bf16_f32 v82, v82, v83
	v_cvt_pk_bf16_f32 v83, v84, v85
	v_cvt_pk_bf16_f32 v84, v86, v87
	v_cvt_pk_bf16_f32 v85, v88, v89
	global_store_dwordx4 v114, v[82:85], s[26:27]
	v_cvt_pk_bf16_f32 v90, v90, v91
	v_cvt_pk_bf16_f32 v91, v92, v93
	v_cvt_pk_bf16_f32 v92, v94, v95
	v_cvt_pk_bf16_f32 v93, v96, v97
	global_store_dwordx4 v114, v[90:93], s[26:27] offset:64
	s_add_u32 s26, s26, 0x12000
	s_addc_u32 s27, s27, 0
	v_cvt_pk_bf16_f32 v66, v66, v67
	v_cvt_pk_bf16_f32 v67, v68, v69
	v_cvt_pk_bf16_f32 v68, v70, v71
	v_cvt_pk_bf16_f32 v69, v72, v73
	global_store_dwordx4 v114, v[66:69], s[26:27]
	v_cvt_pk_bf16_f32 v74, v74, v75
	v_cvt_pk_bf16_f32 v75, v76, v77
	v_cvt_pk_bf16_f32 v76, v78, v79
	v_cvt_pk_bf16_f32 v77, v80, v81
	global_store_dwordx4 v114, v[74:77], s[26:27] offset:64
	s_add_u32 s26, s26, 0x5a000
	s_addc_u32 s27, s27, 0
	v_cvt_pk_bf16_f32 v48, v48, v49
	v_cvt_pk_bf16_f32 v49, v50, v51
	v_cvt_pk_bf16_f32 v50, v52, v53
	v_cvt_pk_bf16_f32 v51, v54, v55
	global_store_dwordx4 v114, v[48:51], s[26:27]
	v_cvt_pk_bf16_f32 v56, v56, v57
	v_cvt_pk_bf16_f32 v57, v58, v59
	v_cvt_pk_bf16_f32 v58, v60, v61
	v_cvt_pk_bf16_f32 v59, v62, v63
	global_store_dwordx4 v114, v[56:59], s[26:27] offset:64
	s_add_u32 s26, s26, 0x12000
	s_addc_u32 s27, s27, 0
	v_cvt_pk_bf16_f32 v32, v32, v33
	v_cvt_pk_bf16_f32 v33, v34, v35
	v_cvt_pk_bf16_f32 v34, v36, v37
	v_cvt_pk_bf16_f32 v35, v38, v39
	global_store_dwordx4 v114, v[32:35], s[26:27]
	v_cvt_pk_bf16_f32 v40, v40, v41
	v_cvt_pk_bf16_f32 v41, v42, v43
	v_cvt_pk_bf16_f32 v42, v44, v45
	v_cvt_pk_bf16_f32 v43, v46, v47
	global_store_dwordx4 v114, v[40:43], s[26:27] offset:64
	s_add_u32 s26, s26, 0x12000
	s_addc_u32 s27, s27, 0
	v_cvt_pk_bf16_f32 v16, v16, v17
	v_cvt_pk_bf16_f32 v17, v18, v19
	v_cvt_pk_bf16_f32 v18, v20, v21
	v_cvt_pk_bf16_f32 v19, v22, v23
	global_store_dwordx4 v114, v[16:19], s[26:27]
	v_cvt_pk_bf16_f32 v24, v24, v25
	v_cvt_pk_bf16_f32 v25, v26, v27
	v_cvt_pk_bf16_f32 v26, v28, v29
	v_cvt_pk_bf16_f32 v27, v30, v31
	global_store_dwordx4 v114, v[24:27], s[26:27] offset:64
	s_add_u32 s26, s26, 0x12000
	s_addc_u32 s27, s27, 0
	v_cvt_pk_bf16_f32 v0, v0, v1
	v_cvt_pk_bf16_f32 v1, v2, v3
	v_cvt_pk_bf16_f32 v2, v4, v5
	v_cvt_pk_bf16_f32 v3, v6, v7
	global_store_dwordx4 v114, v[0:3], s[26:27]
	v_cvt_pk_bf16_f32 v8, v8, v9
	v_cvt_pk_bf16_f32 v9, v10, v11
	v_cvt_pk_bf16_f32 v10, v12, v13
	v_cvt_pk_bf16_f32 v11, v14, v15
	global_store_dwordx4 v114, v[8:11], s[26:27] offset:64
.Lqkv_epi_done:
	s_andn2_b64 vcc, exec, s[34:35]
	s_mov_b64 s[2:3], -1
	s_cbranch_vccnz .LBB0_623
	s_andn2_b64 vcc, exec, s[0:1]
	s_cbranch_vccnz .LBB0_622
	s_barrier
	s_branch .LBB0_622

.LBB0_728:
	v_lshl_add_u64 v[50:51], s[4:5], 1, v[202:203]
	s_mov_b32 s13, m0
	s_mov_b32 m0, s34
	s_nop 0
	global_load_lds_dwordx4 v[50:51], off
	s_mov_b32 m0, s13
	v_lshl_add_u64 v[48:49], s[20:21], 1, v[204:205]
	s_mov_b32 s13, m0
	s_mov_b32 m0, s35
	s_nop 0
	global_load_lds_dwordx4 v[48:49], off
	s_mov_b32 m0, s13
	s_cmp_lg_u32 0, -1
	s_mov_b64 s[24:25], 0x48000
	s_cselect_b32 s13, 0, 0
	v_lshl_add_u64 v[0:1], v[50:51], 0, s[24:25]
	s_add_i32 s13, s13, s12
	s_add_i32 s14, s13, 0x2000
	s_mov_b32 s15, m0
	s_mov_b32 m0, s14
	s_nop 0
	global_load_lds_dwordx4 v[0:1], off
	s_mov_b32 m0, s15
	v_lshl_add_u64 v[0:1], s[22:23], 1, v[206:207]
	s_nop 0
	global_load_dwordx4 v[140:143], v[0:1], off
	global_load_dwordx4 v[132:135], v[0:1], off offset:32
	global_load_dwordx4 v[120:123], v[0:1], off offset:64
	global_load_dwordx4 v[116:119], v[0:1], off offset:96
	v_mov_b32_e32 v15, 0
	s_mov_b64 s[14:15], 0x90000
	v_mov_b32_e32 v14, v15
	v_mov_b32_e32 v0, v15
	v_mov_b32_e32 v1, v15
	v_mov_b32_e32 v2, v15
	v_mov_b32_e32 v3, v15
	v_mov_b32_e32 v4, v15
	v_mov_b32_e32 v5, v15
	v_mov_b32_e32 v6, v15
	v_mov_b32_e32 v7, v15
	v_mov_b32_e32 v8, v15
	v_mov_b32_e32 v9, v15
	v_mov_b32_e32 v10, v15
	v_mov_b32_e32 v11, v15
	v_mov_b32_e32 v12, v15
	v_mov_b32_e32 v13, v15
	s_waitcnt lgkmcnt(0)
	v_mov_b64_e32 v[30:31], v[14:15]
	v_mov_b64_e32 v[28:29], v[12:13]
	v_mov_b64_e32 v[26:27], v[10:11]
	v_mov_b64_e32 v[24:25], v[8:9]
	v_mov_b64_e32 v[22:23], v[6:7]
	v_mov_b64_e32 v[20:21], v[4:5]
	v_mov_b64_e32 v[18:19], v[2:3]
	v_mov_b64_e32 v[16:17], v[0:1]
	v_lshl_add_u64 v[32:33], v[50:51], 0, s[14:15]
	s_add_i32 s14, s13, 0x4000
	s_mov_b32 s15, m0
	s_mov_b32 m0, s14
	s_nop 0
	global_load_lds_dwordx4 v[32:33], off
	s_mov_b32 m0, s15
	s_waitcnt vmcnt(3) lgkmcnt(0)
	s_barrier
	ds_read_b128 v[0:3], v65
	ds_read_b128 v[4:7], v65 offset:512
	s_mov_b64 s[14:15], 0xd8000
	s_add_i32 s13, s13, 0x8000
	s_andn2_b64 vcc, exec, s[2:3]
	s_mov_b64 s[2:3], -1
	s_waitcnt vmcnt(0) lgkmcnt(0)
	v_mfma_f32_32x32x16_bf16 v[32:47], v[0:3], v[140:143], v[16:31]
	v_mfma_f32_32x32x16_bf16 v[16:31], v[4:7], v[140:143], v[16:31]
	ds_read_b128 v[0:3], v65 offset:2048
	ds_read_b128 v[4:7], v65 offset:2560
	s_waitcnt lgkmcnt(1)
	v_mfma_f32_32x32x16_bf16 v[32:47], v[0:3], v[132:135], v[32:47]
	s_waitcnt lgkmcnt(0)
	v_mfma_f32_32x32x16_bf16 v[16:31], v[4:7], v[132:135], v[16:31]
	ds_read_b128 v[0:3], v65 offset:4096
	ds_read_b128 v[4:7], v65 offset:4608
	s_waitcnt lgkmcnt(1)
	v_mfma_f32_32x32x16_bf16 v[32:47], v[0:3], v[120:123], v[32:47]
	s_waitcnt lgkmcnt(0)
	v_mfma_f32_32x32x16_bf16 v[16:31], v[4:7], v[120:123], v[16:31]
	ds_read_b128 v[0:3], v65 offset:6144
	ds_read_b128 v[4:7], v65 offset:6656
	s_waitcnt lgkmcnt(1)
	v_mfma_f32_32x32x16_bf16 v[32:47], v[0:3], v[116:119], v[32:47]
	s_waitcnt lgkmcnt(0)
	v_mfma_f32_32x32x16_bf16 v[16:31], v[4:7], v[116:119], v[16:31]
	s_nop 15
	s_nop 7
	s_nop 0
	v_max3_f32 v0, v32, v33, v16
	v_max3_f32 v1, v34, v35, v17
	s_nop 0
	v_max3_f32 v0, v0, v18, v19
	v_max3_f32 v1, v1, v38, v39
	s_nop 0
	v_max3_f32 v0, v0, v36, v37
	v_max3_f32 v1, v1, v22, v23
	s_nop 0
	v_max3_f32 v0, v0, v20, v21
	v_max3_f32 v1, v1, v42, v43
	s_nop 0
	v_max3_f32 v0, v0, v40, v41
	v_max3_f32 v1, v1, v26, v27
	s_nop 0
	v_max3_f32 v0, v0, v24, v25
	v_max3_f32 v1, v1, v46, v47
	s_nop 0
	v_max3_f32 v0, v0, v44, v45
	v_max3_f32 v1, v1, v30, v31
	s_nop 0
	v_max3_f32 v0, v0, v28, v29
	s_nop 0
	v_max_f32_e32 v0, v0, v1
	s_nop 0
	v_mov_b32_e32 v1, v0
	s_nop 1
	v_permlane32_swap_b32_e32 v0, v1
	v_max_f32_e32 v0, v0, v1
	s_nop 0
	v_add_f32_e32 v234, v115, v0
	v_sub_f32_e32 v1, v32, v0
	v_sub_f32_e32 v2, v16, v0
	v_sub_f32_e32 v3, v33, v0
	v_sub_f32_e32 v4, v17, v0
	v_sub_f32_e32 v5, v34, v0
	s_nop 0
	v_xor_b32_e32 v66, 0x80000000, v234
	v_mov_b32_e32 v67, v66
	v_mov_b32_e32 v68, v66
	v_mov_b32_e32 v69, v66
	v_mov_b32_e32 v70, v66
	v_mov_b32_e32 v71, v66
	v_mov_b32_e32 v72, v66
	v_mov_b32_e32 v73, v66
	v_mov_b32_e32 v74, v66
	v_mov_b32_e32 v75, v66
	v_mov_b32_e32 v76, v66
	v_mov_b32_e32 v77, v66
	v_mov_b32_e32 v78, v66
	v_mov_b32_e32 v79, v66
	v_mov_b32_e32 v80, v66
	v_mov_b32_e32 v81, v66
	v_sub_f32_e32 v6, v18, v0
	v_sub_f32_e32 v7, v35, v0
	v_sub_f32_e32 v8, v19, v0
	v_sub_f32_e32 v9, v36, v0
	v_sub_f32_e32 v10, v20, v0
	v_sub_f32_e32 v11, v37, v0
	v_sub_f32_e32 v12, v21, v0
	v_sub_f32_e32 v13, v38, v0
	v_sub_f32_e32 v14, v22, v0
	v_sub_f32_e32 v16, v39, v0
	v_sub_f32_e32 v17, v23, v0
	v_sub_f32_e32 v18, v40, v0
	v_sub_f32_e32 v19, v24, v0
	v_sub_f32_e32 v20, v41, v0
	v_sub_f32_e32 v21, v25, v0
	v_sub_f32_e32 v22, v42, v0
	v_sub_f32_e32 v23, v26, v0
	v_sub_f32_e32 v24, v43, v0
	v_sub_f32_e32 v25, v27, v0
	v_sub_f32_e32 v26, v44, v0
	v_sub_f32_e32 v27, v28, v0
	v_sub_f32_e32 v28, v45, v0
	v_sub_f32_e32 v29, v29, v0
	v_sub_f32_e32 v32, v46, v0
	v_sub_f32_e32 v30, v30, v0
	v_sub_f32_e32 v33, v47, v0
	v_sub_f32_e32 v0, v31, v0
	s_waitcnt vmcnt(0) lgkmcnt(0)
	s_barrier
	v_exp_f32_e32 v98, v1
	v_exp_f32_e32 v97, v0
	v_lshl_add_u64 v[0:1], v[50:51], 0, s[14:15]
	s_mov_b32 s14, m0
	s_mov_b32 m0, s34
	s_nop 0
	global_load_lds_dwordx4 v[0:1], off
	s_mov_b32 m0, s14
	v_lshl_add_u64 v[0:1], v[48:49], 0, s[24:25]
	s_mov_b32 s14, m0
	s_mov_b32 m0, s13
	s_nop 0
	global_load_lds_dwordx4 v[0:1], off
	s_mov_b32 m0, s14
	ds_read_b128 v[176:179], v65 offset:8192
	ds_read_b128 v[172:175], v65 offset:8704
	ds_read_b128 v[168:171], v65 offset:10240
	ds_read_b128 v[164:167], v65 offset:10752
	ds_read_b128 v[160:163], v65 offset:12288
	ds_read_b128 v[156:159], v65 offset:12800
	ds_read_b128 v[152:155], v65 offset:14336
	ds_read_b128 v[148:151], v65 offset:14848
	v_exp_f32_e32 v99, v3
	v_exp_f32_e32 v100, v5
	v_exp_f32_e32 v101, v7
	v_exp_f32_e32 v102, v9
	v_exp_f32_e32 v103, v11
	v_exp_f32_e32 v104, v13
	v_exp_f32_e32 v105, v16
	v_exp_f32_e32 v106, v18
	v_exp_f32_e32 v107, v20
	v_exp_f32_e32 v108, v22
	v_exp_f32_e32 v109, v24
	v_exp_f32_e32 v110, v26
	v_exp_f32_e32 v111, v28
	v_exp_f32_e32 v112, v32
	v_exp_f32_e32 v113, v33
	v_exp_f32_e32 v82, v2
	v_exp_f32_e32 v83, v4
	v_exp_f32_e32 v84, v6
	v_exp_f32_e32 v85, v8
	v_exp_f32_e32 v86, v10
	v_exp_f32_e32 v87, v12
	v_exp_f32_e32 v88, v14
	v_exp_f32_e32 v89, v17
	v_exp_f32_e32 v90, v19
	v_exp_f32_e32 v91, v21
	v_exp_f32_e32 v92, v23
	v_exp_f32_e32 v93, v25
	v_exp_f32_e32 v94, v27
	v_exp_f32_e32 v95, v29
	v_exp_f32_e32 v96, v30
	s_waitcnt vmcnt(2) lgkmcnt(0)
	s_barrier
	s_cbranch_vccnz .LBB0_730
	v_mov_b32_e32 v30, v15
	v_mov_b32_e32 v31, v15
	v_mov_b32_e32 v0, v15
	v_mov_b32_e32 v1, v15
	v_mov_b32_e32 v2, v15
	v_mov_b32_e32 v3, v15
	v_mov_b32_e32 v4, v15
	v_mov_b32_e32 v5, v15
	v_mov_b32_e32 v6, v15
	v_mov_b32_e32 v7, v15
	v_mov_b32_e32 v8, v15
	v_mov_b32_e32 v9, v15
	v_mov_b32_e32 v10, v15
	v_mov_b32_e32 v11, v15
	v_mov_b32_e32 v12, v15
	v_mov_b32_e32 v13, v15
	v_mov_b32_e32 v14, v15
	v_mov_b32_e32 v16, v15
	v_mov_b32_e32 v17, v15
	v_mov_b32_e32 v18, v15
	v_mov_b32_e32 v19, v15
	v_mov_b32_e32 v20, v15
	v_mov_b32_e32 v21, v15
	v_mov_b32_e32 v22, v15
	v_mov_b32_e32 v23, v15
	v_mov_b32_e32 v24, v15
	v_mov_b32_e32 v25, v15
	v_mov_b32_e32 v26, v15
	v_mov_b32_e32 v27, v15
	v_mov_b32_e32 v28, v15
	v_mov_b32_e32 v29, v15
	v_mov_b64_e32 v[62:63], v[30:31]
	s_mov_b64 s[2:3], 0
	v_mov_b64_e32 v[60:61], v[28:29]
	v_mov_b64_e32 v[58:59], v[26:27]
	v_mov_b64_e32 v[56:57], v[24:25]
	v_mov_b64_e32 v[54:55], v[22:23]
	v_mov_b64_e32 v[52:53], v[20:21]
	v_mov_b64_e32 v[50:51], v[18:19]
	v_mov_b64_e32 v[48:49], v[16:17]
	v_mov_b64_e32 v[46:47], v[14:15]
	v_mov_b64_e32 v[44:45], v[12:13]
	v_mov_b64_e32 v[42:43], v[10:11]
	v_mov_b64_e32 v[40:41], v[8:9]
	v_mov_b64_e32 v[38:39], v[6:7]
	v_mov_b64_e32 v[36:37], v[4:5]
	v_mov_b64_e32 v[34:35], v[2:3]
	v_mov_b64_e32 v[32:33], v[0:1]

.LBB0_1110:
	v_mov_b32_e32 v0, 0
	s_mov_b32 s15, -2
	s_mov_b64 s[2:3], 0
	v_mov_b32_e32 v1, v0
	v_mov_b32_e32 v2, v0
	v_mov_b32_e32 v3, v0
	v_mov_b32_e32 v4, v0
	v_mov_b32_e32 v5, v0
	v_mov_b32_e32 v6, v0
	v_mov_b32_e32 v7, v0
	v_mov_b32_e32 v8, v0
	v_mov_b32_e32 v9, v0
	v_mov_b32_e32 v10, v0
	v_mov_b32_e32 v11, v0
	v_mov_b32_e32 v12, v0
	v_mov_b32_e32 v13, v0
	v_mov_b32_e32 v14, v0
	v_mov_b32_e32 v15, v0
	v_mov_b32_e32 v16, v0
	v_mov_b32_e32 v17, v0
	v_mov_b32_e32 v18, v0
	v_mov_b32_e32 v19, v0
	v_mov_b32_e32 v20, v0
	v_mov_b32_e32 v21, v0
	v_mov_b32_e32 v22, v0
	v_mov_b32_e32 v23, v0
	v_mov_b32_e32 v24, v0
	v_mov_b32_e32 v25, v0
	v_mov_b32_e32 v26, v0
	v_mov_b32_e32 v27, v0
	s_waitcnt lgkmcnt(0)
	v_mov_b32_e32 v28, v0
	v_mov_b32_e32 v29, v0
	v_mov_b32_e32 v30, v0
	v_mov_b32_e32 v31, v0
	v_mov_b32_e32 v32, v0
	v_mov_b32_e32 v33, v0
	v_mov_b32_e32 v34, v0
	v_mov_b32_e32 v35, v0
	v_mov_b32_e32 v36, v0
	v_mov_b32_e32 v37, v0
	v_mov_b32_e32 v38, v0
	v_mov_b32_e32 v39, v0
	v_mov_b32_e32 v40, v0
	v_mov_b32_e32 v41, v0
	v_mov_b32_e32 v42, v0
	v_mov_b32_e32 v43, v0
	v_mov_b32_e32 v44, v0
	v_mov_b32_e32 v45, v0
	v_mov_b32_e32 v46, v0
	v_mov_b32_e32 v47, v0
	v_mov_b32_e32 v48, v0
	v_mov_b32_e32 v49, v0
	v_mov_b32_e32 v50, v0
	v_mov_b32_e32 v51, v0
	v_mov_b32_e32 v52, v0
	v_mov_b32_e32 v53, v0
	v_mov_b32_e32 v54, v0
	v_mov_b32_e32 v55, v0
	v_mov_b32_e32 v56, v0
	v_mov_b32_e32 v57, v0
	v_mov_b32_e32 v58, v0
	v_mov_b32_e32 v59, v0
	v_mov_b32_e32 v60, v0
	v_mov_b32_e32 v61, v0
	v_mov_b32_e32 v62, v0
	v_mov_b32_e32 v63, v0
	v_mov_b32_e32 v66, v0
	v_mov_b32_e32 v67, v0
	v_mov_b32_e32 v68, v0
	v_mov_b32_e32 v69, v0
	v_mov_b32_e32 v70, v0
	v_mov_b32_e32 v71, v0
	v_mov_b32_e32 v72, v0
	v_mov_b32_e32 v73, v0
	v_mov_b32_e32 v74, v0
	v_mov_b32_e32 v75, v0
	v_mov_b32_e32 v76, v0
	v_mov_b32_e32 v77, v0
	v_mov_b32_e32 v78, v0
	v_mov_b32_e32 v79, v0
	v_mov_b32_e32 v80, v0
	v_mov_b32_e32 v81, v0
	v_mov_b32_e32 v82, v0
	v_mov_b32_e32 v83, v0
	v_mov_b32_e32 v84, v0
	v_mov_b32_e32 v85, v0
	v_mov_b32_e32 v86, v0
	v_mov_b32_e32 v87, v0
	v_mov_b32_e32 v88, v0
	v_mov_b32_e32 v89, v0
	v_mov_b32_e32 v90, v0
	v_mov_b32_e32 v91, v0
	v_mov_b32_e32 v92, v0
	v_mov_b32_e32 v93, v0
	v_mov_b32_e32 v94, v0
	v_mov_b32_e32 v95, v0
	v_mov_b32_e32 v96, v0
	v_mov_b32_e32 v97, v0
	v_mov_b32_e32 v98, v0
	v_mov_b32_e32 v99, v0
	v_mov_b32_e32 v100, v0
	v_mov_b32_e32 v101, v0
	v_mov_b32_e32 v102, v0
	v_mov_b32_e32 v103, v0
	v_mov_b32_e32 v104, v0
	v_mov_b32_e32 v105, v0
	v_mov_b32_e32 v106, v0
	v_mov_b32_e32 v107, v0
	v_mov_b32_e32 v108, v0
	v_mov_b32_e32 v109, v0
	v_mov_b32_e32 v110, v0
	v_mov_b32_e32 v111, v0
	v_mov_b32_e32 v112, v0
	v_mov_b32_e32 v113, v0
	v_mov_b32_e32 v116, v0
	v_mov_b32_e32 v117, v0
	v_mov_b32_e32 v118, v0
	v_mov_b32_e32 v119, v0
	v_mov_b32_e32 v120, v0
	v_mov_b32_e32 v121, v0
	v_mov_b32_e32 v122, v0
	v_mov_b32_e32 v123, v0
	v_mov_b32_e32 v124, v0
	v_mov_b32_e32 v125, v0
	v_mov_b32_e32 v126, v0
	v_mov_b32_e32 v127, v0
	v_mov_b32_e32 v128, v0
	v_mov_b32_e32 v129, v0
	v_mov_b32_e32 v130, v0
	v_mov_b32_e32 v131, v0
.LBB0_1111:
	s_add_u32 s66, s26, s2
	s_addc_u32 s67, s27, s3
	s_nop 0
	v_add_u32_e32 v132, 0x10000, v204
	v_add_u32_e32 v134, 0x14000, v204
	s_add_u32 s20, s66, 0x100
	ds_read_b128 v[136:139], v132
	ds_read_b128 v[140:143], v132 offset:1024
	ds_read_b128 v[144:147], v132 offset:2048
	ds_read_b128 v[148:151], v132 offset:3072
	ds_read_b128 v[152:155], v134
	ds_read_b128 v[156:159], v134 offset:1024
	ds_read_b128 v[160:163], v134 offset:2048
	ds_read_b128 v[164:167], v134 offset:3072
	s_addc_u32 s21, s67, 0
	s_add_u32 s18, s66, 0x180
	s_addc_u32 s19, s67, 0
	s_add_u32 s17, s24, s2
	s_addc_u32 s33, s25, s3
	s_add_u32 s34, s17, 0x100
	s_addc_u32 s35, s33, 0
	ds_read_b128 v[168:171], v205
	ds_read_b128 v[172:175], v205 offset:1024
	ds_read_b128 v[176:179], v205 offset:2048
	ds_read_b128 v[180:183], v205 offset:3072
	ds_read_b128 v[184:187], v205 offset:4096
	ds_read_b128 v[188:191], v205 offset:5120
	ds_read_b128 v[194:197], v205 offset:6144
	ds_read_b128 v[198:201], v205 offset:7168
	s_add_u32 s64, s66, 0x40080
	s_addc_u32 s65, s67, 0
	s_nop 4
	s_mov_b32 s68, m0
	s_mov_b32 m0, s62
	s_nop 0
	global_load_lds_dwordx4 v65, s[64:65]
	s_mov_b32 m0, s68
	s_nop 0
	s_nop 4
	s_mov_b32 s68, m0
	s_mov_b32 m0, s63
	s_nop 0
	global_load_lds_dwordx4 v202, s[64:65]
	s_mov_b32 m0, s68
	s_waitcnt vmcnt(8)
	s_waitcnt lgkmcnt(0)
	s_barrier
	s_setprio 1
	s_waitcnt lgkmcnt(0)
	v_mfma_f32_16x16x32_bf16 v[128:131], v[136:139], v[168:171], v[128:131]
	v_mfma_f32_16x16x32_bf16 v[124:127], v[144:147], v[168:171], v[124:127]
	v_mfma_f32_16x16x32_bf16 v[120:123], v[136:139], v[176:179], v[120:123]
	v_mfma_f32_16x16x32_bf16 v[116:119], v[144:147], v[176:179], v[116:119]
	v_mfma_f32_16x16x32_bf16 v[110:113], v[136:139], v[184:187], v[110:113]
	v_mfma_f32_16x16x32_bf16 v[106:109], v[144:147], v[184:187], v[106:109]
	v_mfma_f32_16x16x32_bf16 v[102:105], v[136:139], v[194:197], v[102:105]
	v_mfma_f32_16x16x32_bf16 v[98:101], v[144:147], v[194:197], v[98:101]
	v_mfma_f32_16x16x32_bf16 v[128:131], v[140:143], v[172:175], v[128:131]
	v_mfma_f32_16x16x32_bf16 v[124:127], v[148:151], v[172:175], v[124:127]
	v_mfma_f32_16x16x32_bf16 v[120:123], v[140:143], v[180:183], v[120:123]
	v_mfma_f32_16x16x32_bf16 v[116:119], v[148:151], v[180:183], v[116:119]
	v_mfma_f32_16x16x32_bf16 v[110:113], v[140:143], v[188:191], v[110:113]
	v_mfma_f32_16x16x32_bf16 v[106:109], v[148:151], v[188:191], v[106:109]
	v_mfma_f32_16x16x32_bf16 v[102:105], v[140:143], v[198:201], v[102:105]
	v_mfma_f32_16x16x32_bf16 v[98:101], v[148:151], v[198:201], v[98:101]
	s_setprio 0
	s_setprio 1
	v_mfma_f32_16x16x32_bf16 v[94:97], v[152:155], v[168:171], v[94:97]
	v_mfma_f32_16x16x32_bf16 v[90:93], v[160:163], v[168:171], v[90:93]
	v_mfma_f32_16x16x32_bf16 v[86:89], v[152:155], v[176:179], v[86:89]
	v_mfma_f32_16x16x32_bf16 v[82:85], v[160:163], v[176:179], v[82:85]
	v_mfma_f32_16x16x32_bf16 v[78:81], v[152:155], v[184:187], v[78:81]
	v_mfma_f32_16x16x32_bf16 v[74:77], v[160:163], v[184:187], v[74:77]
	v_mfma_f32_16x16x32_bf16 v[70:73], v[152:155], v[194:197], v[70:73]
	v_mfma_f32_16x16x32_bf16 v[66:69], v[160:163], v[194:197], v[66:69]
	v_mfma_f32_16x16x32_bf16 v[94:97], v[156:159], v[172:175], v[94:97]
	v_mfma_f32_16x16x32_bf16 v[90:93], v[164:167], v[172:175], v[90:93]
	v_mfma_f32_16x16x32_bf16 v[86:89], v[156:159], v[180:183], v[86:89]
	v_mfma_f32_16x16x32_bf16 v[82:85], v[164:167], v[180:183], v[82:85]
	v_mfma_f32_16x16x32_bf16 v[78:81], v[156:159], v[188:191], v[78:81]
	v_mfma_f32_16x16x32_bf16 v[74:77], v[164:167], v[188:191], v[74:77]
	v_mfma_f32_16x16x32_bf16 v[70:73], v[156:159], v[198:201], v[70:73]
	v_mfma_f32_16x16x32_bf16 v[66:69], v[164:167], v[198:201], v[66:69]
	s_setprio 0
	s_barrier
	ds_read_b128 v[168:171], v205 offset:16384
	ds_read_b128 v[172:175], v205 offset:17408
	ds_read_b128 v[176:179], v205 offset:18432
	ds_read_b128 v[180:183], v205 offset:19456
	ds_read_b128 v[184:187], v205 offset:20480
	ds_read_b128 v[188:191], v205 offset:21504
	ds_read_b128 v[194:197], v205 offset:22528
	ds_read_b128 v[198:201], v205 offset:23552
	s_nop 4
	s_mov_b32 s64, m0
	s_mov_b32 m0, s44
	s_nop 0
	global_load_lds_dwordx4 v114, s[34:35]
	s_mov_b32 m0, s64
	s_nop 0
	s_nop 4
	s_mov_b32 s64, m0
	s_mov_b32 m0, s45
	s_nop 0
	global_load_lds_dwordx4 v203, s[34:35]
	s_mov_b32 m0, s64
	s_add_u32 s34, s17, 0x40100
	s_addc_u32 s35, s33, 0
	s_nop 4
	s_mov_b32 s64, m0
	s_mov_b32 m0, s46
	s_nop 0
	global_load_lds_dwordx4 v114, s[34:35]
	s_mov_b32 m0, s64
	s_nop 0
	s_nop 4
	s_mov_b32 s64, m0
	s_mov_b32 m0, s47
	s_nop 0
	global_load_lds_dwordx4 v203, s[34:35]
	s_mov_b32 m0, s64
	s_nop 4
	s_mov_b32 s34, m0
	s_mov_b32 m0, s43
	s_nop 0
	global_load_lds_dwordx4 v65, s[20:21]
	s_mov_b32 m0, s34
	s_nop 0
	s_nop 4
	s_mov_b32 s34, m0
	s_mov_b32 m0, s48
	s_nop 0
	global_load_lds_dwordx4 v202, s[20:21]
	s_mov_b32 m0, s34
	s_waitcnt vmcnt(8)
	s_waitcnt lgkmcnt(0)
	s_barrier
	s_setprio 1
	s_waitcnt lgkmcnt(7)
	v_mfma_f32_16x16x32_bf16 v[60:63], v[136:139], v[168:171], v[60:63]
	v_mfma_f32_16x16x32_bf16 v[56:59], v[144:147], v[168:171], v[56:59]
	s_waitcnt lgkmcnt(5)
	v_mfma_f32_16x16x32_bf16 v[52:55], v[136:139], v[176:179], v[52:55]
	v_mfma_f32_16x16x32_bf16 v[48:51], v[144:147], v[176:179], v[48:51]
	s_waitcnt lgkmcnt(3)
	v_mfma_f32_16x16x32_bf16 v[44:47], v[136:139], v[184:187], v[44:47]
	v_mfma_f32_16x16x32_bf16 v[40:43], v[144:147], v[184:187], v[40:43]
	s_waitcnt lgkmcnt(1)
	v_mfma_f32_16x16x32_bf16 v[36:39], v[136:139], v[194:197], v[36:39]
	v_mfma_f32_16x16x32_bf16 v[32:35], v[144:147], v[194:197], v[32:35]
	v_mfma_f32_16x16x32_bf16 v[60:63], v[140:143], v[172:175], v[60:63]
	v_mfma_f32_16x16x32_bf16 v[56:59], v[148:151], v[172:175], v[56:59]
	v_mfma_f32_16x16x32_bf16 v[52:55], v[140:143], v[180:183], v[52:55]
	v_mfma_f32_16x16x32_bf16 v[48:51], v[148:151], v[180:183], v[48:51]
	v_mfma_f32_16x16x32_bf16 v[44:47], v[140:143], v[188:191], v[44:47]
	v_mfma_f32_16x16x32_bf16 v[40:43], v[148:151], v[188:191], v[40:43]
	s_waitcnt lgkmcnt(0)
	v_mfma_f32_16x16x32_bf16 v[36:39], v[140:143], v[198:201], v[36:39]
	v_mfma_f32_16x16x32_bf16 v[32:35], v[148:151], v[198:201], v[32:35]
	s_setprio 0
	s_setprio 1
	v_mfma_f32_16x16x32_bf16 v[28:31], v[152:155], v[168:171], v[28:31]
	v_mfma_f32_16x16x32_bf16 v[24:27], v[160:163], v[168:171], v[24:27]
	v_mfma_f32_16x16x32_bf16 v[20:23], v[152:155], v[176:179], v[20:23]
	v_mfma_f32_16x16x32_bf16 v[16:19], v[160:163], v[176:179], v[16:19]
	v_mfma_f32_16x16x32_bf16 v[12:15], v[152:155], v[184:187], v[12:15]
	v_mfma_f32_16x16x32_bf16 v[8:11], v[160:163], v[184:187], v[8:11]
	v_mfma_f32_16x16x32_bf16 v[4:7], v[152:155], v[194:197], v[4:7]
	v_mfma_f32_16x16x32_bf16 v[0:3], v[160:163], v[194:197], v[0:3]
	v_mfma_f32_16x16x32_bf16 v[28:31], v[156:159], v[172:175], v[28:31]
	v_mfma_f32_16x16x32_bf16 v[24:27], v[164:167], v[172:175], v[24:27]
	v_mfma_f32_16x16x32_bf16 v[20:23], v[156:159], v[180:183], v[20:23]
	v_mfma_f32_16x16x32_bf16 v[16:19], v[164:167], v[180:183], v[16:19]
	v_mfma_f32_16x16x32_bf16 v[12:15], v[156:159], v[188:191], v[12:15]
	v_mfma_f32_16x16x32_bf16 v[8:11], v[164:167], v[188:191], v[8:11]
	v_mfma_f32_16x16x32_bf16 v[4:7], v[156:159], v[198:201], v[4:7]
	v_mfma_f32_16x16x32_bf16 v[0:3], v[164:167], v[198:201], v[0:3]
	s_setprio 0
	s_barrier
	v_add_u32_e32 v133, 0x18000, v204
	v_add_u32_e32 v135, 0x1c000, v204
	ds_read_b128 v[136:139], v133
	ds_read_b128 v[140:143], v133 offset:1024
	ds_read_b128 v[144:147], v133 offset:2048
	ds_read_b128 v[148:151], v133 offset:3072
	ds_read_b128 v[152:155], v135
	ds_read_b128 v[156:159], v135 offset:1024
	ds_read_b128 v[160:163], v135 offset:2048
	ds_read_b128 v[164:167], v135 offset:3072
	ds_read_b128 v[168:171], v205 offset:32768
	ds_read_b128 v[172:175], v205 offset:33792
	ds_read_b128 v[176:179], v205 offset:34816
	ds_read_b128 v[180:183], v205 offset:35840
	ds_read_b128 v[184:187], v205 offset:36864
	ds_read_b128 v[188:191], v205 offset:37888
	ds_read_b128 v[194:197], v205 offset:38912
	ds_read_b128 v[198:201], v205 offset:39936
	s_add_u32 s20, s66, 0x40100
	s_addc_u32 s21, s67, 0
	s_nop 4
	s_mov_b32 s34, m0
	s_mov_b32 m0, s49
	s_nop 0
	global_load_lds_dwordx4 v65, s[20:21]
	s_mov_b32 m0, s34
	s_nop 0
	s_nop 4
	s_mov_b32 s34, m0
	s_mov_b32 m0, s50
	s_nop 0
	global_load_lds_dwordx4 v202, s[20:21]
	s_mov_b32 m0, s34
	s_waitcnt vmcnt(8)
	s_waitcnt lgkmcnt(0)
	s_barrier
	s_setprio 1
	s_waitcnt lgkmcnt(7)
	v_mfma_f32_16x16x32_bf16 v[128:131], v[136:139], v[168:171], v[128:131]
	v_mfma_f32_16x16x32_bf16 v[124:127], v[144:147], v[168:171], v[124:127]
	s_waitcnt lgkmcnt(5)
	v_mfma_f32_16x16x32_bf16 v[120:123], v[136:139], v[176:179], v[120:123]
	v_mfma_f32_16x16x32_bf16 v[116:119], v[144:147], v[176:179], v[116:119]
	s_waitcnt lgkmcnt(3)
	v_mfma_f32_16x16x32_bf16 v[110:113], v[136:139], v[184:187], v[110:113]
	v_mfma_f32_16x16x32_bf16 v[106:109], v[144:147], v[184:187], v[106:109]
	s_waitcnt lgkmcnt(1)
	v_mfma_f32_16x16x32_bf16 v[102:105], v[136:139], v[194:197], v[102:105]
	v_mfma_f32_16x16x32_bf16 v[98:101], v[144:147], v[194:197], v[98:101]
	v_mfma_f32_16x16x32_bf16 v[128:131], v[140:143], v[172:175], v[128:131]
	v_mfma_f32_16x16x32_bf16 v[124:127], v[148:151], v[172:175], v[124:127]
	v_mfma_f32_16x16x32_bf16 v[120:123], v[140:143], v[180:183], v[120:123]
	v_mfma_f32_16x16x32_bf16 v[116:119], v[148:151], v[180:183], v[116:119]
	v_mfma_f32_16x16x32_bf16 v[110:113], v[140:143], v[188:191], v[110:113]
	v_mfma_f32_16x16x32_bf16 v[106:109], v[148:151], v[188:191], v[106:109]
	s_waitcnt lgkmcnt(0)
	v_mfma_f32_16x16x32_bf16 v[102:105], v[140:143], v[198:201], v[102:105]
	v_mfma_f32_16x16x32_bf16 v[98:101], v[148:151], v[198:201], v[98:101]
	s_setprio 0
	s_setprio 1
	v_mfma_f32_16x16x32_bf16 v[94:97], v[152:155], v[168:171], v[94:97]
	v_mfma_f32_16x16x32_bf16 v[90:93], v[160:163], v[168:171], v[90:93]
	v_mfma_f32_16x16x32_bf16 v[86:89], v[152:155], v[176:179], v[86:89]
	v_mfma_f32_16x16x32_bf16 v[82:85], v[160:163], v[176:179], v[82:85]
	v_mfma_f32_16x16x32_bf16 v[78:81], v[152:155], v[184:187], v[78:81]
	v_mfma_f32_16x16x32_bf16 v[74:77], v[160:163], v[184:187], v[74:77]
	v_mfma_f32_16x16x32_bf16 v[70:73], v[152:155], v[194:197], v[70:73]
	v_mfma_f32_16x16x32_bf16 v[66:69], v[160:163], v[194:197], v[66:69]
	v_mfma_f32_16x16x32_bf16 v[94:97], v[156:159], v[172:175], v[94:97]
	v_mfma_f32_16x16x32_bf16 v[90:93], v[164:167], v[172:175], v[90:93]
	v_mfma_f32_16x16x32_bf16 v[86:89], v[156:159], v[180:183], v[86:89]
	v_mfma_f32_16x16x32_bf16 v[82:85], v[164:167], v[180:183], v[82:85]
	v_mfma_f32_16x16x32_bf16 v[78:81], v[156:159], v[188:191], v[78:81]
	v_mfma_f32_16x16x32_bf16 v[74:77], v[164:167], v[188:191], v[74:77]
	v_mfma_f32_16x16x32_bf16 v[70:73], v[156:159], v[198:201], v[70:73]
	v_mfma_f32_16x16x32_bf16 v[66:69], v[164:167], v[198:201], v[66:69]
	s_setprio 0
	s_barrier
	ds_read_b128 v[168:171], v205 offset:49152
	ds_read_b128 v[172:175], v205 offset:50176
	ds_read_b128 v[176:179], v205 offset:51200
	ds_read_b128 v[180:183], v205 offset:52224
	ds_read_b128 v[184:187], v205 offset:53248
	ds_read_b128 v[188:191], v205 offset:54272
	ds_read_b128 v[194:197], v205 offset:55296
	ds_read_b128 v[198:201], v205 offset:56320
	s_add_u32 s20, s17, 0x180
	s_addc_u32 s21, s33, 0
	s_nop 4
	s_mov_b32 s34, m0
	s_mov_b32 m0, s56
	s_nop 0
	global_load_lds_dwordx4 v114, s[20:21]
	s_mov_b32 m0, s34
	s_nop 0
	s_nop 4
	s_mov_b32 s34, m0
	s_mov_b32 m0, s57
	s_nop 0
	global_load_lds_dwordx4 v203, s[20:21]
	s_mov_b32 m0, s34
	s_add_u32 s20, s17, 0x40180
	s_addc_u32 s21, s33, 0
	s_nop 4
	s_mov_b32 s17, m0
	s_mov_b32 m0, s60
	s_nop 0
	global_load_lds_dwordx4 v114, s[20:21]
	s_mov_b32 m0, s17
	s_nop 0
	s_nop 4
	s_mov_b32 s17, m0
	s_mov_b32 m0, s61
	s_nop 0
	global_load_lds_dwordx4 v203, s[20:21]
	s_mov_b32 m0, s17
	s_nop 0
	s_nop 4
	s_mov_b32 s17, m0
	s_mov_b32 m0, s58
	s_nop 0
	global_load_lds_dwordx4 v65, s[18:19]
	s_mov_b32 m0, s17
	s_nop 0
	s_nop 4
	s_mov_b32 s17, m0
	s_mov_b32 m0, s59
	s_nop 0
	global_load_lds_dwordx4 v202, s[18:19]
	s_mov_b32 m0, s17
	s_waitcnt vmcnt(8)
	s_waitcnt lgkmcnt(0)
	s_barrier
	s_setprio 1
	s_waitcnt lgkmcnt(7)
	v_mfma_f32_16x16x32_bf16 v[60:63], v[136:139], v[168:171], v[60:63]
	v_mfma_f32_16x16x32_bf16 v[56:59], v[144:147], v[168:171], v[56:59]
	s_waitcnt lgkmcnt(5)
	v_mfma_f32_16x16x32_bf16 v[52:55], v[136:139], v[176:179], v[52:55]
	v_mfma_f32_16x16x32_bf16 v[48:51], v[144:147], v[176:179], v[48:51]
	s_waitcnt lgkmcnt(3)
	v_mfma_f32_16x16x32_bf16 v[44:47], v[136:139], v[184:187], v[44:47]
	v_mfma_f32_16x16x32_bf16 v[40:43], v[144:147], v[184:187], v[40:43]
	s_waitcnt lgkmcnt(1)
	v_mfma_f32_16x16x32_bf16 v[36:39], v[136:139], v[194:197], v[36:39]
	v_mfma_f32_16x16x32_bf16 v[32:35], v[144:147], v[194:197], v[32:35]
	v_mfma_f32_16x16x32_bf16 v[60:63], v[140:143], v[172:175], v[60:63]
	v_mfma_f32_16x16x32_bf16 v[56:59], v[148:151], v[172:175], v[56:59]
	v_mfma_f32_16x16x32_bf16 v[52:55], v[140:143], v[180:183], v[52:55]
	v_mfma_f32_16x16x32_bf16 v[48:51], v[148:151], v[180:183], v[48:51]
	v_mfma_f32_16x16x32_bf16 v[44:47], v[140:143], v[188:191], v[44:47]
	v_mfma_f32_16x16x32_bf16 v[40:43], v[148:151], v[188:191], v[40:43]
	s_waitcnt lgkmcnt(0)
	v_mfma_f32_16x16x32_bf16 v[36:39], v[140:143], v[198:201], v[36:39]
	v_mfma_f32_16x16x32_bf16 v[32:35], v[148:151], v[198:201], v[32:35]
	s_setprio 0
	s_setprio 1
	v_mfma_f32_16x16x32_bf16 v[28:31], v[152:155], v[168:171], v[28:31]
	v_mfma_f32_16x16x32_bf16 v[24:27], v[160:163], v[168:171], v[24:27]
	v_mfma_f32_16x16x32_bf16 v[20:23], v[152:155], v[176:179], v[20:23]
	v_mfma_f32_16x16x32_bf16 v[16:19], v[160:163], v[176:179], v[16:19]
	v_mfma_f32_16x16x32_bf16 v[12:15], v[152:155], v[184:187], v[12:15]
	v_mfma_f32_16x16x32_bf16 v[8:11], v[160:163], v[184:187], v[8:11]
	v_mfma_f32_16x16x32_bf16 v[4:7], v[152:155], v[194:197], v[4:7]
	v_mfma_f32_16x16x32_bf16 v[0:3], v[160:163], v[194:197], v[0:3]
	v_mfma_f32_16x16x32_bf16 v[28:31], v[156:159], v[172:175], v[28:31]
	v_mfma_f32_16x16x32_bf16 v[24:27], v[164:167], v[172:175], v[24:27]
	v_mfma_f32_16x16x32_bf16 v[20:23], v[156:159], v[180:183], v[20:23]
	v_mfma_f32_16x16x32_bf16 v[16:19], v[164:167], v[180:183], v[16:19]
	v_mfma_f32_16x16x32_bf16 v[12:15], v[156:159], v[188:191], v[12:15]
	v_mfma_f32_16x16x32_bf16 v[8:11], v[164:167], v[188:191], v[8:11]
	v_mfma_f32_16x16x32_bf16 v[4:7], v[156:159], v[198:201], v[4:7]
	v_mfma_f32_16x16x32_bf16 v[0:3], v[164:167], v[198:201], v[0:3]
	s_setprio 0
	s_barrier
	s_add_i32 s15, s15, 2
	s_add_u32 s2, s2, 0x100
	s_addc_u32 s3, s3, 0
	s_cmp_lt_u32 s15, 12
	s_cbranch_scc1 .LBB0_1111
	s_ashr_i32 s17, s16, 31
	s_ashr_i32 s15, s14, 31
	ds_read_b128 v[136:139], v132
	ds_read_b128 v[140:143], v132 offset:1024
	ds_read_b128 v[144:147], v132 offset:2048
	ds_read_b128 v[148:151], v132 offset:3072
	ds_read_b128 v[152:155], v134
	ds_read_b128 v[156:159], v134 offset:1024
	ds_read_b128 v[160:163], v134 offset:2048
	ds_read_b128 v[164:167], v134 offset:3072
	s_lshl_b64 s[2:3], s[16:17], 19
	s_lshl_b64 s[20:21], s[14:15], 19
	s_add_u32 s18, s29, s2
	s_addc_u32 s19, s36, s3
	s_add_u32 s20, s37, s20
	s_addc_u32 s21, s38, s21
	s_and_b64 s[2:3], s[0:1], exec
	s_cselect_b32 s34, s18, s26
	s_cselect_b32 s35, s19, s27
	s_add_u32 s2, s34, 0x80
	s_addc_u32 s3, s35, 0
	s_and_b64 s[64:65], s[0:1], exec
	s_cselect_b32 s25, s21, s25
	s_cselect_b32 s24, s20, s24
	ds_read_b128 v[168:171], v205
	ds_read_b128 v[172:175], v205 offset:1024
	ds_read_b128 v[176:179], v205 offset:2048
	ds_read_b128 v[180:183], v205 offset:3072
	ds_read_b128 v[184:187], v205 offset:4096
	ds_read_b128 v[188:191], v205 offset:5120
	ds_read_b128 v[194:197], v205 offset:6144
	ds_read_b128 v[198:201], v205 offset:7168
	s_add_u32 s26, s26, 0x40780
	s_addc_u32 s27, s27, 0
	s_nop 4
	s_mov_b32 s15, m0
	s_mov_b32 m0, s62
	s_nop 0
	global_load_lds_dwordx4 v65, s[26:27]
	s_mov_b32 m0, s15
	s_nop 0
	s_nop 4
	s_mov_b32 s15, m0
	s_mov_b32 m0, s63
	s_nop 0
	global_load_lds_dwordx4 v202, s[26:27]
	s_mov_b32 m0, s15
	s_waitcnt vmcnt(8)
	s_waitcnt lgkmcnt(0)
	s_barrier
	s_setprio 1
	s_waitcnt lgkmcnt(7)
	v_mfma_f32_16x16x32_bf16 v[128:131], v[136:139], v[168:171], v[128:131]
	v_mfma_f32_16x16x32_bf16 v[124:127], v[144:147], v[168:171], v[124:127]
	s_waitcnt lgkmcnt(5)
	v_mfma_f32_16x16x32_bf16 v[120:123], v[136:139], v[176:179], v[120:123]
	v_mfma_f32_16x16x32_bf16 v[116:119], v[144:147], v[176:179], v[116:119]
	s_waitcnt lgkmcnt(3)
	v_mfma_f32_16x16x32_bf16 v[110:113], v[136:139], v[184:187], v[110:113]
	v_mfma_f32_16x16x32_bf16 v[106:109], v[144:147], v[184:187], v[106:109]
	v_mfma_f32_16x16x32_bf16 v[128:131], v[140:143], v[172:175], v[128:131]
	v_mfma_f32_16x16x32_bf16 v[124:127], v[148:151], v[172:175], v[124:127]
	v_mfma_f32_16x16x32_bf16 v[120:123], v[140:143], v[180:183], v[120:123]
	v_mfma_f32_16x16x32_bf16 v[116:119], v[148:151], v[180:183], v[116:119]
	s_waitcnt lgkmcnt(2)
	v_mfma_f32_16x16x32_bf16 v[110:113], v[140:143], v[188:191], v[110:113]
	v_mfma_f32_16x16x32_bf16 v[106:109], v[148:151], v[188:191], v[106:109]
	s_waitcnt lgkmcnt(1)
	v_mfma_f32_16x16x32_bf16 v[102:105], v[136:139], v[194:197], v[102:105]
	v_mfma_f32_16x16x32_bf16 v[98:101], v[144:147], v[194:197], v[98:101]
	s_waitcnt lgkmcnt(0)
	v_mfma_f32_16x16x32_bf16 v[206:209], v[140:143], v[198:201], v[102:105]
	v_mfma_f32_16x16x32_bf16 v[210:213], v[148:151], v[198:201], v[98:101]
	s_setprio 0
	s_setprio 1
	v_mfma_f32_16x16x32_bf16 v[94:97], v[152:155], v[168:171], v[94:97]
	v_mfma_f32_16x16x32_bf16 v[90:93], v[160:163], v[168:171], v[90:93]
	v_mfma_f32_16x16x32_bf16 v[78:81], v[152:155], v[184:187], v[78:81]
	v_mfma_f32_16x16x32_bf16 v[74:77], v[160:163], v[184:187], v[74:77]
	v_mfma_f32_16x16x32_bf16 v[70:73], v[152:155], v[194:197], v[70:73]
	v_mfma_f32_16x16x32_bf16 v[66:69], v[160:163], v[194:197], v[66:69]
	v_mfma_f32_16x16x32_bf16 v[94:97], v[156:159], v[172:175], v[94:97]
	v_mfma_f32_16x16x32_bf16 v[90:93], v[164:167], v[172:175], v[90:93]
	v_mfma_f32_16x16x32_bf16 v[86:89], v[152:155], v[176:179], v[86:89]
	v_mfma_f32_16x16x32_bf16 v[82:85], v[160:163], v[176:179], v[82:85]
	v_mfma_f32_16x16x32_bf16 v[78:81], v[156:159], v[188:191], v[78:81]
	v_mfma_f32_16x16x32_bf16 v[74:77], v[164:167], v[188:191], v[74:77]
	v_mfma_f32_16x16x32_bf16 v[70:73], v[156:159], v[198:201], v[70:73]
	v_mfma_f32_16x16x32_bf16 v[66:69], v[164:167], v[198:201], v[66:69]
	v_mfma_f32_16x16x32_bf16 v[168:171], v[156:159], v[180:183], v[86:89]
	v_mfma_f32_16x16x32_bf16 v[172:175], v[164:167], v[180:183], v[82:85]
	s_setprio 0
	s_barrier
	s_nop 0
	ds_read_b128 v[82:85], v205 offset:16384
	ds_read_b128 v[86:89], v205 offset:17408
	ds_read_b128 v[98:101], v205 offset:18432
	ds_read_b128 v[102:105], v205 offset:19456
	ds_read_b128 v[176:179], v205 offset:20480
	ds_read_b128 v[180:183], v205 offset:21504
	ds_read_b128 v[184:187], v205 offset:22528
	ds_read_b128 v[188:191], v205 offset:23552
	s_nop 4
	s_mov_b32 s15, m0
	s_mov_b32 m0, s44
	s_nop 0
	global_load_lds_dwordx4 v114, s[24:25]
	s_mov_b32 m0, s15
	s_add_u32 s26, s24, 0x40000
	s_nop 4
	s_mov_b32 s15, m0
	s_mov_b32 m0, s45
	s_nop 0
	global_load_lds_dwordx4 v203, s[24:25]
	s_mov_b32 m0, s15
	s_addc_u32 s27, s25, 0
	s_nop 4
	s_mov_b32 s15, m0
	s_mov_b32 m0, s46
	s_nop 0
	global_load_lds_dwordx4 v114, s[26:27]
	s_mov_b32 m0, s15
	s_nop 0
	s_nop 4
	s_mov_b32 s15, m0
	s_mov_b32 m0, s47
	s_nop 0
	global_load_lds_dwordx4 v203, s[26:27]
	s_mov_b32 m0, s15
	s_nop 0
	s_nop 4
	s_mov_b32 s15, m0
	s_mov_b32 m0, s43
	s_nop 0
	global_load_lds_dwordx4 v65, s[34:35]
	s_mov_b32 m0, s15
	s_nop 0
	s_nop 4
	s_mov_b32 s15, m0
	s_mov_b32 m0, s48
	s_nop 0
	global_load_lds_dwordx4 v202, s[34:35]
	s_mov_b32 m0, s15
	s_waitcnt vmcnt(8)
	s_waitcnt lgkmcnt(0)
	s_barrier
	s_setprio 1
	s_waitcnt lgkmcnt(7)
	v_mfma_f32_16x16x32_bf16 v[60:63], v[136:139], v[82:85], v[60:63]
	v_mfma_f32_16x16x32_bf16 v[56:59], v[144:147], v[82:85], v[56:59]
	s_waitcnt lgkmcnt(5)
	v_mfma_f32_16x16x32_bf16 v[52:55], v[136:139], v[98:101], v[52:55]
	v_mfma_f32_16x16x32_bf16 v[48:51], v[144:147], v[98:101], v[48:51]
	v_mfma_f32_16x16x32_bf16 v[60:63], v[140:143], v[86:89], v[60:63]
	v_mfma_f32_16x16x32_bf16 v[56:59], v[148:151], v[86:89], v[56:59]
	s_waitcnt lgkmcnt(4)
	v_mfma_f32_16x16x32_bf16 v[52:55], v[140:143], v[102:105], v[52:55]
	v_mfma_f32_16x16x32_bf16 v[48:51], v[148:151], v[102:105], v[48:51]
	s_waitcnt lgkmcnt(3)
	v_mfma_f32_16x16x32_bf16 v[44:47], v[136:139], v[176:179], v[44:47]
	v_mfma_f32_16x16x32_bf16 v[40:43], v[144:147], v[176:179], v[40:43]
	s_waitcnt lgkmcnt(1)
	v_mfma_f32_16x16x32_bf16 v[36:39], v[136:139], v[184:187], v[36:39]
	v_mfma_f32_16x16x32_bf16 v[32:35], v[144:147], v[184:187], v[32:35]
	v_mfma_f32_16x16x32_bf16 v[44:47], v[140:143], v[180:183], v[44:47]
	v_mfma_f32_16x16x32_bf16 v[40:43], v[148:151], v[180:183], v[40:43]
	s_waitcnt lgkmcnt(0)
	v_mfma_f32_16x16x32_bf16 v[36:39], v[140:143], v[188:191], v[36:39]
	v_mfma_f32_16x16x32_bf16 v[148:151], v[148:151], v[188:191], v[32:35]
	s_setprio 0
	s_setprio 1
	v_mfma_f32_16x16x32_bf16 v[20:23], v[152:155], v[98:101], v[20:23]
	v_mfma_f32_16x16x32_bf16 v[16:19], v[160:163], v[98:101], v[16:19]
	v_mfma_f32_16x16x32_bf16 v[4:7], v[152:155], v[184:187], v[4:7]
	v_mfma_f32_16x16x32_bf16 v[0:3], v[160:163], v[184:187], v[0:3]
	v_mfma_f32_16x16x32_bf16 v[28:31], v[152:155], v[82:85], v[28:31]
	v_mfma_f32_16x16x32_bf16 v[24:27], v[160:163], v[82:85], v[24:27]
	v_mfma_f32_16x16x32_bf16 v[20:23], v[156:159], v[102:105], v[20:23]
	v_mfma_f32_16x16x32_bf16 v[16:19], v[164:167], v[102:105], v[16:19]
	v_mfma_f32_16x16x32_bf16 v[12:15], v[152:155], v[176:179], v[12:15]
	v_mfma_f32_16x16x32_bf16 v[8:11], v[160:163], v[176:179], v[8:11]
	v_mfma_f32_16x16x32_bf16 v[4:7], v[156:159], v[188:191], v[4:7]
	v_mfma_f32_16x16x32_bf16 v[0:3], v[164:167], v[188:191], v[0:3]
	v_mfma_f32_16x16x32_bf16 v[28:31], v[156:159], v[86:89], v[28:31]
	v_mfma_f32_16x16x32_bf16 v[194:197], v[164:167], v[86:89], v[24:27]
	v_mfma_f32_16x16x32_bf16 v[198:201], v[156:159], v[180:183], v[12:15]
	v_mfma_f32_16x16x32_bf16 v[176:179], v[164:167], v[180:183], v[8:11]
	s_setprio 0
	s_barrier
	s_nop 0
	ds_read_b128 v[8:11], v133
	ds_read_b128 v[12:15], v133 offset:1024
	ds_read_b128 v[152:155], v133 offset:2048
	ds_read_b128 v[156:159], v133 offset:3072
	ds_read_b128 v[160:163], v135
	ds_read_b128 v[164:167], v135 offset:1024
	ds_read_b128 v[180:183], v135 offset:2048
	ds_read_b128 v[184:187], v135 offset:3072
	ds_read_b128 v[24:27], v205 offset:32768
	ds_read_b128 v[32:35], v205 offset:33792
	ds_read_b128 v[188:191], v205 offset:34816
	ds_read_b128 v[214:217], v205 offset:35840
	ds_read_b128 v[218:221], v205 offset:36864
	ds_read_b128 v[222:225], v205 offset:37888
	ds_read_b128 v[226:229], v205 offset:38912
	ds_read_b128 v[230:233], v205 offset:39936
	s_add_u32 s26, s34, 0x40000
	s_addc_u32 s27, s35, 0
	s_nop 4
	s_mov_b32 s15, m0
	s_mov_b32 m0, s49
	s_nop 0
	global_load_lds_dwordx4 v65, s[26:27]
	s_mov_b32 m0, s15
	s_nop 0
	s_nop 4
	s_mov_b32 s15, m0
	s_mov_b32 m0, s50
	s_nop 0
	global_load_lds_dwordx4 v202, s[26:27]
	s_mov_b32 m0, s15
	s_waitcnt vmcnt(8)
	s_waitcnt lgkmcnt(0)
	s_barrier
	s_setprio 1
	s_waitcnt lgkmcnt(7)
	v_mfma_f32_16x16x32_bf16 v[82:85], v[8:11], v[24:27], v[128:131]
	s_waitcnt lgkmcnt(6)
	v_mfma_f32_16x16x32_bf16 v[140:143], v[12:15], v[32:35], v[82:85]
	v_mfma_f32_16x16x32_bf16 v[82:85], v[152:155], v[24:27], v[124:127]
	v_mfma_f32_16x16x32_bf16 v[144:147], v[156:159], v[32:35], v[82:85]
	s_waitcnt lgkmcnt(5)
	v_mfma_f32_16x16x32_bf16 v[82:85], v[8:11], v[188:191], v[120:123]
	s_waitcnt lgkmcnt(4)
	v_mfma_f32_16x16x32_bf16 v[124:127], v[12:15], v[214:217], v[82:85]
	v_mfma_f32_16x16x32_bf16 v[82:85], v[152:155], v[188:191], v[116:119]
	v_mfma_f32_16x16x32_bf16 v[128:131], v[156:159], v[214:217], v[82:85]
	s_waitcnt lgkmcnt(3)
	v_mfma_f32_16x16x32_bf16 v[82:85], v[8:11], v[218:221], v[110:113]
	s_waitcnt lgkmcnt(2)
	v_mfma_f32_16x16x32_bf16 v[98:101], v[12:15], v[222:225], v[82:85]
	v_mfma_f32_16x16x32_bf16 v[82:85], v[152:155], v[218:221], v[106:109]
	v_mfma_f32_16x16x32_bf16 v[102:105], v[156:159], v[222:225], v[82:85]
	s_waitcnt lgkmcnt(1)
	v_mfma_f32_16x16x32_bf16 v[82:85], v[8:11], v[226:229], v[206:209]
	v_mfma_f32_16x16x32_bf16 v[86:89], v[152:155], v[226:229], v[210:213]
	s_waitcnt lgkmcnt(0)
	v_mfma_f32_16x16x32_bf16 v[82:85], v[12:15], v[230:233], v[82:85]
	v_mfma_f32_16x16x32_bf16 v[86:89], v[156:159], v[230:233], v[86:89]
	s_setprio 0
	s_setprio 1
	v_mfma_f32_16x16x32_bf16 v[94:97], v[160:163], v[24:27], v[94:97]
	v_mfma_f32_16x16x32_bf16 v[24:27], v[180:183], v[24:27], v[90:93]
	v_mfma_f32_16x16x32_bf16 v[132:135], v[184:187], v[32:35], v[24:27]
	v_mfma_f32_16x16x32_bf16 v[24:27], v[160:163], v[188:191], v[168:171]
	v_mfma_f32_16x16x32_bf16 v[120:123], v[164:167], v[214:217], v[24:27]
	v_mfma_f32_16x16x32_bf16 v[24:27], v[180:183], v[188:191], v[172:175]
	v_mfma_f32_16x16x32_bf16 v[116:119], v[184:187], v[214:217], v[24:27]
	v_mfma_f32_16x16x32_bf16 v[24:27], v[160:163], v[218:221], v[78:81]
	v_mfma_f32_16x16x32_bf16 v[106:109], v[164:167], v[222:225], v[24:27]
	v_mfma_f32_16x16x32_bf16 v[24:27], v[180:183], v[218:221], v[74:77]
	v_mfma_f32_16x16x32_bf16 v[110:113], v[184:187], v[222:225], v[24:27]
	v_mfma_f32_16x16x32_bf16 v[24:27], v[160:163], v[226:229], v[70:73]
	v_mfma_f32_16x16x32_bf16 v[90:93], v[164:167], v[230:233], v[24:27]
	v_mfma_f32_16x16x32_bf16 v[24:27], v[180:183], v[226:229], v[66:69]
	v_mfma_f32_16x16x32_bf16 v[136:139], v[164:167], v[32:35], v[94:97]
	v_mfma_f32_16x16x32_bf16 v[94:97], v[184:187], v[230:233], v[24:27]
	s_setprio 0
	s_barrier
	ds_read_b128 v[66:69], v205 offset:49152
	ds_read_b128 v[168:171], v205 offset:50176
	ds_read_b128 v[172:175], v205 offset:51200
	ds_read_b128 v[188:191], v205 offset:52224
	ds_read_b128 v[206:209], v205 offset:53248
	ds_read_b128 v[210:213], v205 offset:54272
	ds_read_b128 v[214:217], v205 offset:55296
	ds_read_b128 v[218:221], v205 offset:56320
	s_add_u32 s26, s24, 0x80
	s_addc_u32 s27, s25, 0
	s_nop 4
	s_mov_b32 s15, m0
	s_mov_b32 m0, s56
	s_nop 0
	global_load_lds_dwordx4 v114, s[26:27]
	s_mov_b32 m0, s15
	s_add_u32 s24, s24, 0x40080
	s_nop 4
	s_mov_b32 s15, m0
	s_mov_b32 m0, s57
	s_nop 0
	global_load_lds_dwordx4 v203, s[26:27]
	s_mov_b32 m0, s15
	s_addc_u32 s25, s25, 0
	s_nop 4
	s_mov_b32 s15, m0
	s_mov_b32 m0, s60
	s_nop 0
	global_load_lds_dwordx4 v114, s[24:25]
	s_mov_b32 m0, s15
	s_nop 0
	s_nop 4
	s_mov_b32 s15, m0
	s_mov_b32 m0, s61
	s_nop 0
	global_load_lds_dwordx4 v203, s[24:25]
	s_mov_b32 m0, s15
	s_nop 0
	s_nop 4
	s_mov_b32 s15, m0
	s_mov_b32 m0, s58
	s_nop 0
	global_load_lds_dwordx4 v65, s[2:3]
	s_mov_b32 m0, s15
	s_nop 0
	s_nop 4
	s_mov_b32 s15, m0
	s_mov_b32 m0, s59
	s_nop 0
	global_load_lds_dwordx4 v202, s[2:3]
	s_mov_b32 m0, s15
	s_waitcnt vmcnt(8)
	s_waitcnt lgkmcnt(0)
	s_barrier
	s_setprio 1
	s_waitcnt lgkmcnt(7)
	v_mfma_f32_16x16x32_bf16 v[24:27], v[8:11], v[66:69], v[60:63]
	s_waitcnt lgkmcnt(6)
	v_mfma_f32_16x16x32_bf16 v[78:81], v[12:15], v[168:171], v[24:27]
	v_mfma_f32_16x16x32_bf16 v[24:27], v[152:155], v[66:69], v[56:59]
	v_mfma_f32_16x16x32_bf16 v[74:77], v[156:159], v[168:171], v[24:27]
	s_waitcnt lgkmcnt(5)
	v_mfma_f32_16x16x32_bf16 v[24:27], v[8:11], v[172:175], v[52:55]
	s_waitcnt lgkmcnt(4)
	v_mfma_f32_16x16x32_bf16 v[60:63], v[12:15], v[188:191], v[24:27]
	v_mfma_f32_16x16x32_bf16 v[24:27], v[152:155], v[172:175], v[48:51]
	v_mfma_f32_16x16x32_bf16 v[56:59], v[156:159], v[188:191], v[24:27]
	s_waitcnt lgkmcnt(3)
	v_mfma_f32_16x16x32_bf16 v[24:27], v[8:11], v[206:209], v[44:47]
	s_waitcnt lgkmcnt(1)
	v_mfma_f32_16x16x32_bf16 v[8:11], v[8:11], v[214:217], v[36:39]
	v_mfma_f32_16x16x32_bf16 v[32:35], v[12:15], v[210:213], v[24:27]
	v_mfma_f32_16x16x32_bf16 v[24:27], v[152:155], v[206:209], v[40:43]
	s_waitcnt lgkmcnt(0)
	v_mfma_f32_16x16x32_bf16 v[12:15], v[12:15], v[218:221], v[8:11]
	v_mfma_f32_16x16x32_bf16 v[8:11], v[152:155], v[214:217], v[148:151]
	v_mfma_f32_16x16x32_bf16 v[24:27], v[156:159], v[210:213], v[24:27]
	v_mfma_f32_16x16x32_bf16 v[8:11], v[156:159], v[218:221], v[8:11]
	s_setprio 0
	s_setprio 1
	v_mfma_f32_16x16x32_bf16 v[16:19], v[180:183], v[172:175], v[16:19]
	v_mfma_f32_16x16x32_bf16 v[28:31], v[160:163], v[66:69], v[28:31]
	v_mfma_f32_16x16x32_bf16 v[20:23], v[160:163], v[172:175], v[20:23]
	v_mfma_f32_16x16x32_bf16 v[48:51], v[184:187], v[188:191], v[16:19]
	v_mfma_f32_16x16x32_bf16 v[16:19], v[160:163], v[206:209], v[198:201]
	v_mfma_f32_16x16x32_bf16 v[70:73], v[164:167], v[168:171], v[28:31]
	v_mfma_f32_16x16x32_bf16 v[28:31], v[180:183], v[66:69], v[194:197]
	v_mfma_f32_16x16x32_bf16 v[52:55], v[164:167], v[188:191], v[20:23]
	v_mfma_f32_16x16x32_bf16 v[20:23], v[164:167], v[210:213], v[16:19]
	v_mfma_f32_16x16x32_bf16 v[16:19], v[180:183], v[206:209], v[176:179]
	v_mfma_f32_16x16x32_bf16 v[4:7], v[160:163], v[214:217], v[4:7]
	v_mfma_f32_16x16x32_bf16 v[0:3], v[180:183], v[214:217], v[0:3]
	v_mfma_f32_16x16x32_bf16 v[66:69], v[184:187], v[168:171], v[28:31]
	v_mfma_f32_16x16x32_bf16 v[16:19], v[184:187], v[210:213], v[16:19]
	v_mfma_f32_16x16x32_bf16 v[4:7], v[164:167], v[218:221], v[4:7]
	v_mfma_f32_16x16x32_bf16 v[0:3], v[184:187], v[218:221], v[0:3]
	s_setprio 0
	s_barrier
	s_andn2_b64 vcc, exec, s[10:11]
	s_cbranch_vccnz .LBB0_1114
	s_barrier

.LBB0_1422:
	s_and_b64 vcc, exec, s[0:1]
	s_cbranch_vccnz .LBB0_1424
	v_mbcnt_lo_u32_b32 v0, -1, 0
	v_mbcnt_hi_u32_b32 v0, -1, v0
	s_lshl_b32 s2, s60, 8
	v_or_b32_e32 v0, s38, v0
	v_ashrrev_i32_e32 v2, 31, v0
	v_lshrrev_b32_e32 v2, 26, v2
	v_lshlrev_b32_e32 v1, 4, v0
	v_add_u32_e32 v2, v0, v2
	v_bfe_i32 v0, v0, 27, 1
	v_lshrrev_b32_e32 v0, 22, v0
	v_add_u32_e32 v0, v1, v0
	v_and_b32_e32 v0, 0xfffffc00, v0
	v_sub_u32_e32 v0, v1, v0
	v_lshrrev_b32_e32 v3, 4, v0
	v_ashrrev_i32_e32 v4, 31, v0
	v_ashrrev_i32_e32 v2, 6, v2
	v_and_b32_e32 v3, 32, v3
	v_lshrrev_b32_e32 v4, 26, v4
	v_lshlrev_b32_e32 v2, 3, v2
	v_xad_u32 v0, v3, v0, v4
	v_and_b32_e32 v2, -16, v2
	v_ashrrev_i32_e32 v0, 6, v0
	v_add_u32_e32 v1, 0x2000, v1
	v_add_u32_e32 v0, v0, v2
	v_ashrrev_i32_e32 v2, 31, v1
	v_lshrrev_b32_e32 v2, 22, v2
	v_add_u32_e32 v2, v1, v2
	v_ashrrev_i32_e32 v2, 10, v2
	v_mul_i32_i24_e32 v3, 0x400, v2
	v_sub_u32_e32 v1, v1, v3
	v_lshrrev_b32_e32 v3, 4, v1
	v_ashrrev_i32_e32 v4, 31, v1
	v_and_b32_e32 v3, 32, v3
	v_lshrrev_b32_e32 v4, 26, v4
	v_lshlrev_b32_e32 v2, 3, v2
	v_xad_u32 v1, v3, v1, v4
	s_ashr_i32 s3, s2, 31
	v_and_b32_e32 v2, -16, v2
	v_ashrrev_i32_e32 v1, 6, v1
	s_lshl_b64 s[2:3], s[2:3], 2
	v_add_u32_e32 v2, v1, v2
	s_add_u32 s2, s8, s2
	s_addc_u32 s3, s9, s3
	v_ashrrev_i32_e32 v1, 31, v0
	v_ashrrev_i32_e32 v3, 31, v2
	v_lshl_add_u64 v[0:1], v[0:1], 2, s[2:3]
	v_lshl_add_u64 v[2:3], v[2:3], 2, s[2:3]
	global_load_dword v248, v[0:1], off
	global_load_dword v249, v[2:3], off
	global_load_dword v251, v[2:3], off offset:512
	global_load_dword v250, v[0:1], off offset:512
.LBB0_1424:
	v_mov_b32_e32 v0, 0
	v_readlane_b32 s72, v254, 62
	s_mov_b32 s21, -2
	s_mov_b64 s[2:3], 0
	v_mov_b32_e32 v1, v0
	v_mov_b64_e32 v[2:3], v[0:1]
	v_mov_b64_e32 v[4:5], v[0:1]
	v_mov_b64_e32 v[6:7], v[0:1]
	v_mov_b64_e32 v[8:9], v[0:1]
	v_mov_b64_e32 v[10:11], v[0:1]
	v_mov_b64_e32 v[12:13], v[0:1]
	v_mov_b64_e32 v[14:15], v[0:1]
	v_mov_b64_e32 v[16:17], v[0:1]
	v_mov_b64_e32 v[18:19], v[0:1]
	v_mov_b64_e32 v[20:21], v[0:1]
	v_mov_b64_e32 v[22:23], v[0:1]
	v_mov_b64_e32 v[24:25], v[0:1]
	v_mov_b64_e32 v[26:27], v[0:1]
	v_mov_b64_e32 v[28:29], v[0:1]
	v_mov_b64_e32 v[30:31], v[0:1]
	v_mov_b64_e32 v[32:33], v[0:1]
	v_mov_b64_e32 v[34:35], v[0:1]
	v_mov_b64_e32 v[36:37], v[0:1]
	v_mov_b64_e32 v[38:39], v[0:1]
	v_mov_b64_e32 v[40:41], v[0:1]
	v_mov_b64_e32 v[42:43], v[0:1]
	v_mov_b64_e32 v[44:45], v[0:1]
	v_mov_b64_e32 v[46:47], v[0:1]
	v_mov_b64_e32 v[48:49], v[0:1]
	v_mov_b64_e32 v[50:51], v[0:1]
	v_mov_b64_e32 v[52:53], v[0:1]
	v_mov_b64_e32 v[54:55], v[0:1]
	v_mov_b64_e32 v[56:57], v[0:1]
	v_mov_b64_e32 v[58:59], v[0:1]
	v_mov_b64_e32 v[60:61], v[0:1]
	v_mov_b64_e32 v[62:63], v[0:1]
	v_mov_b64_e32 v[66:67], v[0:1]
	v_mov_b64_e32 v[68:69], v[0:1]
	v_mov_b64_e32 v[70:71], v[0:1]
	v_mov_b64_e32 v[72:73], v[0:1]
	v_mov_b64_e32 v[74:75], v[0:1]
	v_mov_b64_e32 v[76:77], v[0:1]
	v_mov_b64_e32 v[78:79], v[0:1]
	v_mov_b64_e32 v[80:81], v[0:1]
	v_mov_b64_e32 v[82:83], v[0:1]
	v_mov_b64_e32 v[84:85], v[0:1]
	v_mov_b64_e32 v[86:87], v[0:1]
	v_mov_b64_e32 v[88:89], v[0:1]
	v_mov_b64_e32 v[90:91], v[0:1]
	v_mov_b64_e32 v[92:93], v[0:1]
	v_mov_b64_e32 v[94:95], v[0:1]
	v_mov_b64_e32 v[96:97], v[0:1]
	v_mov_b64_e32 v[98:99], v[0:1]
	v_mov_b64_e32 v[100:101], v[0:1]
	v_mov_b64_e32 v[102:103], v[0:1]
	v_mov_b64_e32 v[104:105], v[0:1]
	v_mov_b64_e32 v[106:107], v[0:1]
	v_mov_b64_e32 v[108:109], v[0:1]
	v_mov_b64_e32 v[110:111], v[0:1]
	v_mov_b64_e32 v[112:113], v[0:1]
	v_mov_b64_e32 v[116:117], v[0:1]
	v_mov_b64_e32 v[118:119], v[0:1]
	v_mov_b64_e32 v[120:121], v[0:1]
	v_mov_b64_e32 v[122:123], v[0:1]
	v_mov_b64_e32 v[124:125], v[0:1]
	v_mov_b64_e32 v[126:127], v[0:1]
	v_mov_b64_e32 v[128:129], v[0:1]
	v_mov_b64_e32 v[130:131], v[0:1]
	v_readlane_b32 s73, v254, 63
.LBB0_1425:
	s_add_u32 s66, s72, s2
	s_addc_u32 s67, s73, s3
	s_add_u32 s34, s66, 0x2000100
	s_addc_u32 s35, s67, 0
	v_add_u32_e32 v141, 0x10000, v134
	v_add_u32_e32 v142, 0x14000, v134
	s_add_u32 s26, s66, 0x2000180
	ds_read_b128 v[144:147], v141
	ds_read_b128 v[148:151], v141 offset:1024
	ds_read_b128 v[152:155], v141 offset:2048
	ds_read_b128 v[156:159], v141 offset:3072
	ds_read_b128 v[160:163], v142
	ds_read_b128 v[164:167], v142 offset:1024
	ds_read_b128 v[168:171], v142 offset:2048
	ds_read_b128 v[172:175], v142 offset:3072
	s_addc_u32 s27, s67, 0
	s_add_u32 s33, s24, s2
	s_addc_u32 s63, s25, s3
	s_add_u32 s64, s33, 0x100
	s_addc_u32 s65, s63, 0
	s_add_u32 s66, s66, 0x2000080
	s_addc_u32 s67, s67, 0
	ds_read_b128 v[176:179], v135
	ds_read_b128 v[180:183], v135 offset:1024
	ds_read_b128 v[184:187], v135 offset:2048
	ds_read_b128 v[188:191], v135 offset:3072
	ds_read_b128 v[194:197], v135 offset:4096
	ds_read_b128 v[198:201], v135 offset:5120
	ds_read_b128 v[202:205], v135 offset:6144
	ds_read_b128 v[206:209], v135 offset:7168
	s_nop 4
	s_mov_b32 s68, m0
	s_mov_b32 m0, s57
	s_nop 0
	global_load_lds_dwordx4 v133, s[66:67]
	s_mov_b32 m0, s68
	s_nop 0
	s_nop 4
	s_mov_b32 s68, m0
	s_mov_b32 m0, s58
	s_nop 0
	global_load_lds_dwordx4 v132, s[66:67]
	s_mov_b32 m0, s68
	s_waitcnt vmcnt(8)
	s_waitcnt lgkmcnt(0)
	s_barrier
	s_setprio 1
	s_waitcnt lgkmcnt(0)
	v_mfma_f32_16x16x32_bf16 v[128:131], v[144:147], v[176:179], v[128:131]
	v_mfma_f32_16x16x32_bf16 v[124:127], v[152:155], v[176:179], v[124:127]
	s_waitcnt lgkmcnt(5)
	v_mfma_f32_16x16x32_bf16 v[120:123], v[144:147], v[184:187], v[120:123]
	v_mfma_f32_16x16x32_bf16 v[116:119], v[152:155], v[184:187], v[116:119]
	s_waitcnt lgkmcnt(3)
	v_mfma_f32_16x16x32_bf16 v[110:113], v[144:147], v[194:197], v[110:113]
	v_mfma_f32_16x16x32_bf16 v[106:109], v[152:155], v[194:197], v[106:109]
	s_waitcnt lgkmcnt(1)
	v_mfma_f32_16x16x32_bf16 v[102:105], v[144:147], v[202:205], v[102:105]
	v_mfma_f32_16x16x32_bf16 v[98:101], v[152:155], v[202:205], v[98:101]
	v_mfma_f32_16x16x32_bf16 v[128:131], v[148:151], v[180:183], v[128:131]
	v_mfma_f32_16x16x32_bf16 v[124:127], v[156:159], v[180:183], v[124:127]
	v_mfma_f32_16x16x32_bf16 v[120:123], v[148:151], v[188:191], v[120:123]
	v_mfma_f32_16x16x32_bf16 v[116:119], v[156:159], v[188:191], v[116:119]
	v_mfma_f32_16x16x32_bf16 v[110:113], v[148:151], v[198:201], v[110:113]
	v_mfma_f32_16x16x32_bf16 v[106:109], v[156:159], v[198:201], v[106:109]
	s_waitcnt lgkmcnt(0)
	v_mfma_f32_16x16x32_bf16 v[102:105], v[148:151], v[206:209], v[102:105]
	v_mfma_f32_16x16x32_bf16 v[98:101], v[156:159], v[206:209], v[98:101]
	s_setprio 0
	s_setprio 1
	v_mfma_f32_16x16x32_bf16 v[94:97], v[160:163], v[176:179], v[94:97]
	v_mfma_f32_16x16x32_bf16 v[90:93], v[168:171], v[176:179], v[90:93]
	v_mfma_f32_16x16x32_bf16 v[86:89], v[160:163], v[184:187], v[86:89]
	v_mfma_f32_16x16x32_bf16 v[82:85], v[168:171], v[184:187], v[82:85]
	v_mfma_f32_16x16x32_bf16 v[78:81], v[160:163], v[194:197], v[78:81]
	v_mfma_f32_16x16x32_bf16 v[74:77], v[168:171], v[194:197], v[74:77]
	v_mfma_f32_16x16x32_bf16 v[70:73], v[160:163], v[202:205], v[70:73]
	v_mfma_f32_16x16x32_bf16 v[66:69], v[168:171], v[202:205], v[66:69]
	v_mfma_f32_16x16x32_bf16 v[94:97], v[164:167], v[180:183], v[94:97]
	v_mfma_f32_16x16x32_bf16 v[90:93], v[172:175], v[180:183], v[90:93]
	v_mfma_f32_16x16x32_bf16 v[86:89], v[164:167], v[188:191], v[86:89]
	v_mfma_f32_16x16x32_bf16 v[82:85], v[172:175], v[188:191], v[82:85]
	v_mfma_f32_16x16x32_bf16 v[78:81], v[164:167], v[198:201], v[78:81]
	v_mfma_f32_16x16x32_bf16 v[74:77], v[172:175], v[198:201], v[74:77]
	v_mfma_f32_16x16x32_bf16 v[70:73], v[164:167], v[206:209], v[70:73]
	v_mfma_f32_16x16x32_bf16 v[66:69], v[172:175], v[206:209], v[66:69]
	s_setprio 0
	s_barrier
	ds_read_b128 v[176:179], v135 offset:16384
	ds_read_b128 v[180:183], v135 offset:17408
	ds_read_b128 v[184:187], v135 offset:18432
	ds_read_b128 v[188:191], v135 offset:19456
	ds_read_b128 v[194:197], v135 offset:20480
	ds_read_b128 v[198:201], v135 offset:21504
	ds_read_b128 v[202:205], v135 offset:22528
	ds_read_b128 v[206:209], v135 offset:23552
	s_nop 4
	s_mov_b32 s66, m0
	s_mov_b32 m0, s41
	s_nop 0
	global_load_lds_dwordx4 v65, s[64:65]
	s_mov_b32 m0, s66
	s_nop 0
	s_nop 4
	s_mov_b32 s66, m0
	s_mov_b32 m0, s42
	s_nop 0
	global_load_lds_dwordx4 v114, s[64:65]
	s_mov_b32 m0, s66
	s_add_u32 s64, s33, 0x40100
	s_addc_u32 s65, s63, 0
	s_nop 4
	s_mov_b32 s66, m0
	s_mov_b32 m0, s43
	s_nop 0
	global_load_lds_dwordx4 v65, s[64:65]
	s_mov_b32 m0, s66
	s_nop 0
	s_nop 4
	s_mov_b32 s66, m0
	s_mov_b32 m0, s44
	s_nop 0
	global_load_lds_dwordx4 v114, s[64:65]
	s_mov_b32 m0, s66
	s_nop 4
	s_mov_b32 s64, m0
	s_mov_b32 m0, s40
	s_nop 0
	global_load_lds_dwordx4 v139, s[34:35]
	s_mov_b32 m0, s64
	s_nop 0
	s_nop 4
	s_mov_b32 s64, m0
	s_mov_b32 m0, s45
	s_nop 0
	global_load_lds_dwordx4 v138, s[34:35]
	s_mov_b32 m0, s64
	s_waitcnt vmcnt(8)
	s_waitcnt lgkmcnt(0)
	s_barrier
	s_setprio 1
	s_waitcnt lgkmcnt(0)
	v_mfma_f32_16x16x32_bf16 v[60:63], v[144:147], v[176:179], v[60:63]
	v_mfma_f32_16x16x32_bf16 v[56:59], v[152:155], v[176:179], v[56:59]
	s_waitcnt lgkmcnt(5)
	v_mfma_f32_16x16x32_bf16 v[52:55], v[144:147], v[184:187], v[52:55]
	v_mfma_f32_16x16x32_bf16 v[48:51], v[152:155], v[184:187], v[48:51]
	s_waitcnt lgkmcnt(3)
	v_mfma_f32_16x16x32_bf16 v[44:47], v[144:147], v[194:197], v[44:47]
	v_mfma_f32_16x16x32_bf16 v[40:43], v[152:155], v[194:197], v[40:43]
	s_waitcnt lgkmcnt(1)
	v_mfma_f32_16x16x32_bf16 v[36:39], v[144:147], v[202:205], v[36:39]
	v_mfma_f32_16x16x32_bf16 v[32:35], v[152:155], v[202:205], v[32:35]
	v_mfma_f32_16x16x32_bf16 v[60:63], v[148:151], v[180:183], v[60:63]
	v_mfma_f32_16x16x32_bf16 v[56:59], v[156:159], v[180:183], v[56:59]
	v_mfma_f32_16x16x32_bf16 v[52:55], v[148:151], v[188:191], v[52:55]
	v_mfma_f32_16x16x32_bf16 v[48:51], v[156:159], v[188:191], v[48:51]
	v_mfma_f32_16x16x32_bf16 v[44:47], v[148:151], v[198:201], v[44:47]
	v_mfma_f32_16x16x32_bf16 v[40:43], v[156:159], v[198:201], v[40:43]
	s_waitcnt lgkmcnt(0)
	v_mfma_f32_16x16x32_bf16 v[36:39], v[148:151], v[206:209], v[36:39]
	v_mfma_f32_16x16x32_bf16 v[32:35], v[156:159], v[206:209], v[32:35]
	s_setprio 0
	s_setprio 1
	v_mfma_f32_16x16x32_bf16 v[28:31], v[160:163], v[176:179], v[28:31]
	v_mfma_f32_16x16x32_bf16 v[24:27], v[168:171], v[176:179], v[24:27]
	v_mfma_f32_16x16x32_bf16 v[20:23], v[160:163], v[184:187], v[20:23]
	v_mfma_f32_16x16x32_bf16 v[16:19], v[168:171], v[184:187], v[16:19]
	v_mfma_f32_16x16x32_bf16 v[12:15], v[160:163], v[194:197], v[12:15]
	v_mfma_f32_16x16x32_bf16 v[8:11], v[168:171], v[194:197], v[8:11]
	v_mfma_f32_16x16x32_bf16 v[4:7], v[160:163], v[202:205], v[4:7]
	v_mfma_f32_16x16x32_bf16 v[0:3], v[168:171], v[202:205], v[0:3]
	v_mfma_f32_16x16x32_bf16 v[28:31], v[164:167], v[180:183], v[28:31]
	v_mfma_f32_16x16x32_bf16 v[24:27], v[172:175], v[180:183], v[24:27]
	v_mfma_f32_16x16x32_bf16 v[20:23], v[164:167], v[188:191], v[20:23]
	v_mfma_f32_16x16x32_bf16 v[16:19], v[172:175], v[188:191], v[16:19]
	v_mfma_f32_16x16x32_bf16 v[12:15], v[164:167], v[198:201], v[12:15]
	v_mfma_f32_16x16x32_bf16 v[8:11], v[172:175], v[198:201], v[8:11]
	v_mfma_f32_16x16x32_bf16 v[4:7], v[164:167], v[206:209], v[4:7]
	v_mfma_f32_16x16x32_bf16 v[0:3], v[172:175], v[206:209], v[0:3]
	s_setprio 0
	s_barrier
	v_add_u32_e32 v143, 0x18000, v134
	v_add_u32_e32 v144, 0x1c000, v134
	ds_read_b128 v[146:149], v143
	ds_read_b128 v[150:153], v143 offset:1024
	ds_read_b128 v[154:157], v143 offset:2048
	ds_read_b128 v[158:161], v143 offset:3072
	ds_read_b128 v[162:165], v144
	ds_read_b128 v[166:169], v144 offset:1024
	ds_read_b128 v[170:173], v144 offset:2048
	ds_read_b128 v[174:177], v144 offset:3072
	ds_read_b128 v[178:181], v135 offset:32768
	ds_read_b128 v[182:185], v135 offset:33792
	ds_read_b128 v[186:189], v135 offset:34816
	ds_read_b128 v[194:197], v135 offset:35840
	ds_read_b128 v[198:201], v135 offset:36864
	ds_read_b128 v[202:205], v135 offset:37888
	ds_read_b128 v[206:209], v135 offset:38912
	ds_read_b128 v[210:213], v135 offset:39936
	s_nop 4
	s_mov_b32 s64, m0
	s_mov_b32 m0, s46
	s_nop 0
	global_load_lds_dwordx4 v133, s[34:35]
	s_mov_b32 m0, s64
	s_nop 0
	s_nop 4
	s_mov_b32 s64, m0
	s_mov_b32 m0, s47
	s_nop 0
	global_load_lds_dwordx4 v132, s[34:35]
	s_mov_b32 m0, s64
	s_waitcnt vmcnt(8)
	s_waitcnt lgkmcnt(0)
	s_barrier
	s_setprio 1
	s_waitcnt lgkmcnt(0)
	v_mfma_f32_16x16x32_bf16 v[128:131], v[146:149], v[178:181], v[128:131]
	v_mfma_f32_16x16x32_bf16 v[124:127], v[154:157], v[178:181], v[124:127]
	s_waitcnt lgkmcnt(5)
	v_mfma_f32_16x16x32_bf16 v[120:123], v[146:149], v[186:189], v[120:123]
	v_mfma_f32_16x16x32_bf16 v[116:119], v[154:157], v[186:189], v[116:119]
	s_waitcnt lgkmcnt(3)
	v_mfma_f32_16x16x32_bf16 v[110:113], v[146:149], v[198:201], v[110:113]
	v_mfma_f32_16x16x32_bf16 v[106:109], v[154:157], v[198:201], v[106:109]
	s_waitcnt lgkmcnt(1)
	v_mfma_f32_16x16x32_bf16 v[102:105], v[146:149], v[206:209], v[102:105]
	v_mfma_f32_16x16x32_bf16 v[98:101], v[154:157], v[206:209], v[98:101]
	v_mfma_f32_16x16x32_bf16 v[128:131], v[150:153], v[182:185], v[128:131]
	v_mfma_f32_16x16x32_bf16 v[124:127], v[158:161], v[182:185], v[124:127]
	v_mfma_f32_16x16x32_bf16 v[120:123], v[150:153], v[194:197], v[120:123]
	v_mfma_f32_16x16x32_bf16 v[116:119], v[158:161], v[194:197], v[116:119]
	v_mfma_f32_16x16x32_bf16 v[110:113], v[150:153], v[202:205], v[110:113]
	v_mfma_f32_16x16x32_bf16 v[106:109], v[158:161], v[202:205], v[106:109]
	s_waitcnt lgkmcnt(0)
	v_mfma_f32_16x16x32_bf16 v[102:105], v[150:153], v[210:213], v[102:105]
	v_mfma_f32_16x16x32_bf16 v[98:101], v[158:161], v[210:213], v[98:101]
	s_setprio 0
	s_setprio 1
	v_mfma_f32_16x16x32_bf16 v[94:97], v[162:165], v[178:181], v[94:97]
	v_mfma_f32_16x16x32_bf16 v[90:93], v[170:173], v[178:181], v[90:93]
	v_mfma_f32_16x16x32_bf16 v[86:89], v[162:165], v[186:189], v[86:89]
	v_mfma_f32_16x16x32_bf16 v[82:85], v[170:173], v[186:189], v[82:85]
	v_mfma_f32_16x16x32_bf16 v[78:81], v[162:165], v[198:201], v[78:81]
	v_mfma_f32_16x16x32_bf16 v[74:77], v[170:173], v[198:201], v[74:77]
	v_mfma_f32_16x16x32_bf16 v[70:73], v[162:165], v[206:209], v[70:73]
	v_mfma_f32_16x16x32_bf16 v[66:69], v[170:173], v[206:209], v[66:69]
	v_mfma_f32_16x16x32_bf16 v[94:97], v[166:169], v[182:185], v[94:97]
	v_mfma_f32_16x16x32_bf16 v[90:93], v[174:177], v[182:185], v[90:93]
	v_mfma_f32_16x16x32_bf16 v[86:89], v[166:169], v[194:197], v[86:89]
	v_mfma_f32_16x16x32_bf16 v[82:85], v[174:177], v[194:197], v[82:85]
	v_mfma_f32_16x16x32_bf16 v[78:81], v[166:169], v[202:205], v[78:81]
	v_mfma_f32_16x16x32_bf16 v[74:77], v[174:177], v[202:205], v[74:77]
	v_mfma_f32_16x16x32_bf16 v[70:73], v[166:169], v[210:213], v[70:73]
	v_mfma_f32_16x16x32_bf16 v[66:69], v[174:177], v[210:213], v[66:69]
	s_setprio 0
	s_barrier
	ds_read_b128 v[178:181], v135 offset:49152
	ds_read_b128 v[182:185], v135 offset:50176
	ds_read_b128 v[186:189], v135 offset:51200
	ds_read_b128 v[194:197], v135 offset:52224
	ds_read_b128 v[198:201], v135 offset:53248
	ds_read_b128 v[202:205], v135 offset:54272
	ds_read_b128 v[206:209], v135 offset:55296
	ds_read_b128 v[210:213], v135 offset:56320
	s_add_u32 s34, s33, 0x180
	s_addc_u32 s35, s63, 0
	s_nop 4
	s_mov_b32 s64, m0
	s_mov_b32 m0, s51
	s_nop 0
	global_load_lds_dwordx4 v65, s[34:35]
	s_mov_b32 m0, s64
	s_nop 0
	s_nop 4
	s_mov_b32 s64, m0
	s_mov_b32 m0, s52
	s_nop 0
	global_load_lds_dwordx4 v114, s[34:35]
	s_mov_b32 m0, s64
	s_add_u32 s34, s33, 0x40180
	s_addc_u32 s35, s63, 0
	s_nop 4
	s_mov_b32 s33, m0
	s_mov_b32 m0, s55
	s_nop 0
	global_load_lds_dwordx4 v65, s[34:35]
	s_mov_b32 m0, s33
	s_nop 0
	s_nop 4
	s_mov_b32 s33, m0
	s_mov_b32 m0, s56
	s_nop 0
	global_load_lds_dwordx4 v114, s[34:35]
	s_mov_b32 m0, s33
	s_nop 0
	s_nop 4
	s_mov_b32 s33, m0
	s_mov_b32 m0, s53
	s_nop 0
	global_load_lds_dwordx4 v139, s[26:27]
	s_mov_b32 m0, s33
	s_nop 0
	s_nop 4
	s_mov_b32 s33, m0
	s_mov_b32 m0, s54
	s_nop 0
	global_load_lds_dwordx4 v138, s[26:27]
	s_mov_b32 m0, s33
	s_waitcnt vmcnt(8)
	s_waitcnt lgkmcnt(0)
	s_barrier
	s_setprio 1
	s_waitcnt lgkmcnt(0)
	v_mfma_f32_16x16x32_bf16 v[60:63], v[146:149], v[178:181], v[60:63]
	v_mfma_f32_16x16x32_bf16 v[56:59], v[154:157], v[178:181], v[56:59]
	s_waitcnt lgkmcnt(5)
	v_mfma_f32_16x16x32_bf16 v[52:55], v[146:149], v[186:189], v[52:55]
	v_mfma_f32_16x16x32_bf16 v[48:51], v[154:157], v[186:189], v[48:51]
	s_waitcnt lgkmcnt(3)
	v_mfma_f32_16x16x32_bf16 v[44:47], v[146:149], v[198:201], v[44:47]
	v_mfma_f32_16x16x32_bf16 v[40:43], v[154:157], v[198:201], v[40:43]
	s_waitcnt lgkmcnt(1)
	v_mfma_f32_16x16x32_bf16 v[36:39], v[146:149], v[206:209], v[36:39]
	v_mfma_f32_16x16x32_bf16 v[32:35], v[154:157], v[206:209], v[32:35]
	v_mfma_f32_16x16x32_bf16 v[60:63], v[150:153], v[182:185], v[60:63]
	v_mfma_f32_16x16x32_bf16 v[56:59], v[158:161], v[182:185], v[56:59]
	v_mfma_f32_16x16x32_bf16 v[52:55], v[150:153], v[194:197], v[52:55]
	v_mfma_f32_16x16x32_bf16 v[48:51], v[158:161], v[194:197], v[48:51]
	v_mfma_f32_16x16x32_bf16 v[44:47], v[150:153], v[202:205], v[44:47]
	v_mfma_f32_16x16x32_bf16 v[40:43], v[158:161], v[202:205], v[40:43]
	s_waitcnt lgkmcnt(0)
	v_mfma_f32_16x16x32_bf16 v[36:39], v[150:153], v[210:213], v[36:39]
	v_mfma_f32_16x16x32_bf16 v[32:35], v[158:161], v[210:213], v[32:35]
	s_setprio 0
	s_setprio 1
	v_mfma_f32_16x16x32_bf16 v[28:31], v[162:165], v[178:181], v[28:31]
	v_mfma_f32_16x16x32_bf16 v[24:27], v[170:173], v[178:181], v[24:27]
	v_mfma_f32_16x16x32_bf16 v[20:23], v[162:165], v[186:189], v[20:23]
	v_mfma_f32_16x16x32_bf16 v[16:19], v[170:173], v[186:189], v[16:19]
	v_mfma_f32_16x16x32_bf16 v[12:15], v[162:165], v[198:201], v[12:15]
	v_mfma_f32_16x16x32_bf16 v[8:11], v[170:173], v[198:201], v[8:11]
	v_mfma_f32_16x16x32_bf16 v[4:7], v[162:165], v[206:209], v[4:7]
	v_mfma_f32_16x16x32_bf16 v[0:3], v[170:173], v[206:209], v[0:3]
	v_mfma_f32_16x16x32_bf16 v[28:31], v[166:169], v[182:185], v[28:31]
	v_mfma_f32_16x16x32_bf16 v[24:27], v[174:177], v[182:185], v[24:27]
	v_mfma_f32_16x16x32_bf16 v[20:23], v[166:169], v[194:197], v[20:23]
	v_mfma_f32_16x16x32_bf16 v[16:19], v[174:177], v[194:197], v[16:19]
	v_mfma_f32_16x16x32_bf16 v[12:15], v[166:169], v[202:205], v[12:15]
	v_mfma_f32_16x16x32_bf16 v[8:11], v[174:177], v[202:205], v[8:11]
	v_mfma_f32_16x16x32_bf16 v[4:7], v[166:169], v[210:213], v[4:7]
	v_mfma_f32_16x16x32_bf16 v[0:3], v[174:177], v[210:213], v[0:3]
	s_setprio 0
	s_barrier
	s_add_i32 s21, s21, 2
	s_add_u32 s2, s2, 0x100
	s_addc_u32 s3, s3, 0
	s_cmp_lt_u32 s21, 12
	s_cbranch_scc1 .LBB0_1425
	ds_read_b128 v[146:149], v141
	ds_read_b128 v[150:153], v141 offset:1024
	ds_read_b128 v[154:157], v141 offset:2048
	ds_read_b128 v[158:161], v141 offset:3072
	ds_read_b128 v[162:165], v142
	ds_read_b128 v[166:169], v142 offset:1024
	ds_read_b128 v[170:173], v142 offset:2048
	ds_read_b128 v[174:177], v142 offset:3072
	s_mov_b32 s2, 0x87ff
	v_min_u32_sdwa v140, v248, s2 dst_sel:DWORD dst_unused:UNUSED_PAD src0_sel:WORD_0 src1_sel:DWORD
	v_and_b32_e32 v145, 0x7ff, v139
	v_lshl_or_b32 v140, v140, 11, v145
	v_cndmask_b32_e64 v190, v139, v140, s[4:5]
	v_min_u32_sdwa v139, v249, s2 dst_sel:DWORD dst_unused:UNUSED_PAD src0_sel:WORD_0 src1_sel:DWORD
	v_and_b32_e32 v145, 0x7ff, v138
	v_lshl_or_b32 v139, v139, 11, v145
	v_cndmask_b32_e64 v191, v138, v139, s[4:5]
	v_min_u32_sdwa v138, v250, s2 dst_sel:DWORD dst_unused:UNUSED_PAD src0_sel:WORD_0 src1_sel:DWORD
	v_and_b32_e32 v145, 0x7ff, v133
	v_min_u32_sdwa v141, v251, s2 dst_sel:DWORD dst_unused:UNUSED_PAD src0_sel:WORD_0 src1_sel:DWORD
	v_and_b32_e32 v142, 0x7ff, v132
	v_lshl_or_b32 v138, v138, 11, v145
	v_lshl_or_b32 v141, v141, 11, v142
	v_cndmask_b32_e64 v234, v133, v138, s[4:5]
	v_cndmask_b32_e64 v235, v132, v141, s[4:5]
	ds_read_b128 v[178:181], v135
	ds_read_b128 v[182:185], v135 offset:1024
	ds_read_b128 v[186:189], v135 offset:2048
	ds_read_b128 v[194:197], v135 offset:3072
	ds_read_b128 v[198:201], v135 offset:4096
	ds_read_b128 v[202:205], v135 offset:5120
	ds_read_b128 v[206:209], v135 offset:6144
	ds_read_b128 v[210:213], v135 offset:7168
	s_nop 4
	s_mov_b32 s2, m0
	s_mov_b32 m0, s57
	s_nop 0
	global_load_lds_dwordx4 v133, s[18:19]
	s_mov_b32 m0, s2
	s_nop 0
	s_nop 4
	s_mov_b32 s2, m0
	s_mov_b32 m0, s58
	s_nop 0
	global_load_lds_dwordx4 v132, s[18:19]
	s_mov_b32 m0, s2
	s_waitcnt vmcnt(8)
	s_waitcnt lgkmcnt(0)
	s_barrier
	s_setprio 1
	s_waitcnt lgkmcnt(0)
	v_mfma_f32_16x16x32_bf16 v[128:131], v[146:149], v[178:181], v[128:131]
	v_mfma_f32_16x16x32_bf16 v[124:127], v[154:157], v[178:181], v[124:127]
	s_waitcnt lgkmcnt(5)
	v_mfma_f32_16x16x32_bf16 v[120:123], v[146:149], v[186:189], v[120:123]
	s_waitcnt lgkmcnt(3)
	v_mfma_f32_16x16x32_bf16 v[106:109], v[154:157], v[198:201], v[106:109]
	s_waitcnt lgkmcnt(1)
	v_mfma_f32_16x16x32_bf16 v[102:105], v[146:149], v[206:209], v[102:105]
	v_mfma_f32_16x16x32_bf16 v[128:131], v[150:153], v[182:185], v[128:131]
	v_mfma_f32_16x16x32_bf16 v[124:127], v[158:161], v[182:185], v[124:127]
	v_mfma_f32_16x16x32_bf16 v[120:123], v[150:153], v[194:197], v[120:123]
	v_mfma_f32_16x16x32_bf16 v[116:119], v[154:157], v[186:189], v[116:119]
	v_mfma_f32_16x16x32_bf16 v[110:113], v[146:149], v[198:201], v[110:113]
	v_mfma_f32_16x16x32_bf16 v[106:109], v[158:161], v[202:205], v[106:109]
	s_waitcnt lgkmcnt(0)
	v_mfma_f32_16x16x32_bf16 v[102:105], v[150:153], v[210:213], v[102:105]
	v_mfma_f32_16x16x32_bf16 v[98:101], v[154:157], v[206:209], v[98:101]
	v_mfma_f32_16x16x32_bf16 v[214:217], v[158:161], v[194:197], v[116:119]
	v_mfma_f32_16x16x32_bf16 v[218:221], v[150:153], v[202:205], v[110:113]
	v_mfma_f32_16x16x32_bf16 v[222:225], v[158:161], v[210:213], v[98:101]
	s_setprio 0
	s_setprio 1
	v_mfma_f32_16x16x32_bf16 v[90:93], v[170:173], v[178:181], v[90:93]
	v_mfma_f32_16x16x32_bf16 v[86:89], v[162:165], v[186:189], v[86:89]
	v_mfma_f32_16x16x32_bf16 v[74:77], v[170:173], v[198:201], v[74:77]
	v_mfma_f32_16x16x32_bf16 v[70:73], v[162:165], v[206:209], v[70:73]
	v_mfma_f32_16x16x32_bf16 v[66:69], v[170:173], v[206:209], v[66:69]
	v_mfma_f32_16x16x32_bf16 v[94:97], v[162:165], v[178:181], v[94:97]
	v_mfma_f32_16x16x32_bf16 v[90:93], v[174:177], v[182:185], v[90:93]
	v_mfma_f32_16x16x32_bf16 v[86:89], v[166:169], v[194:197], v[86:89]
	v_mfma_f32_16x16x32_bf16 v[82:85], v[170:173], v[186:189], v[82:85]
	v_mfma_f32_16x16x32_bf16 v[78:81], v[162:165], v[198:201], v[78:81]
	v_mfma_f32_16x16x32_bf16 v[74:77], v[174:177], v[202:205], v[74:77]
	v_mfma_f32_16x16x32_bf16 v[70:73], v[166:169], v[210:213], v[70:73]
	v_mfma_f32_16x16x32_bf16 v[66:69], v[174:177], v[210:213], v[66:69]
	v_mfma_f32_16x16x32_bf16 v[226:229], v[166:169], v[182:185], v[94:97]
	v_mfma_f32_16x16x32_bf16 v[178:181], v[174:177], v[194:197], v[82:85]
	v_mfma_f32_16x16x32_bf16 v[182:185], v[166:169], v[202:205], v[78:81]
	s_setprio 0
	s_barrier
	s_nop 0
	ds_read_b128 v[78:81], v135 offset:16384
	ds_read_b128 v[82:85], v135 offset:17408
	ds_read_b128 v[94:97], v135 offset:18432
	ds_read_b128 v[98:101], v135 offset:19456
	ds_read_b128 v[110:113], v135 offset:20480
	ds_read_b128 v[116:119], v135 offset:21504
	ds_read_b128 v[186:189], v135 offset:22528
	ds_read_b128 v[194:197], v135 offset:23552
	s_nop 4
	s_mov_b32 s2, m0
	s_mov_b32 m0, s41
	s_nop 0
	global_load_lds_dwordx4 v65, s[22:23]
	s_mov_b32 m0, s2
	s_nop 0
	s_nop 4
	s_mov_b32 s2, m0
	s_mov_b32 m0, s42
	s_nop 0
	global_load_lds_dwordx4 v114, s[22:23]
	s_mov_b32 m0, s2
	s_add_u32 s2, s22, 0x40000
	s_addc_u32 s3, s23, 0
	s_nop 4
	s_mov_b32 s4, m0
	s_mov_b32 m0, s43
	s_nop 0
	global_load_lds_dwordx4 v65, s[2:3]
	s_mov_b32 m0, s4
	s_nop 0
	s_nop 4
	s_mov_b32 s4, m0
	s_mov_b32 m0, s44
	s_nop 0
	global_load_lds_dwordx4 v114, s[2:3]
	s_mov_b32 m0, s4
	s_nop 4
	s_mov_b32 s2, m0
	s_mov_b32 m0, s40
	s_nop 0
	global_load_lds_dwordx4 v190, s[6:7]
	s_mov_b32 m0, s2
	s_nop 0
	s_nop 4
	s_mov_b32 s2, m0
	s_mov_b32 m0, s45
	s_nop 0
	global_load_lds_dwordx4 v191, s[6:7]
	s_mov_b32 m0, s2
	s_waitcnt vmcnt(8)
	s_waitcnt lgkmcnt(0)
	s_barrier
	s_setprio 1
	s_waitcnt lgkmcnt(0)
	v_mfma_f32_16x16x32_bf16 v[60:63], v[146:149], v[78:81], v[60:63]
	s_waitcnt lgkmcnt(5)
	v_mfma_f32_16x16x32_bf16 v[52:55], v[146:149], v[94:97], v[52:55]
	s_waitcnt lgkmcnt(3)
	v_mfma_f32_16x16x32_bf16 v[40:43], v[154:157], v[110:113], v[40:43]
	s_waitcnt lgkmcnt(1)
	v_mfma_f32_16x16x32_bf16 v[36:39], v[146:149], v[186:189], v[36:39]
	v_mfma_f32_16x16x32_bf16 v[60:63], v[150:153], v[82:85], v[60:63]
	v_mfma_f32_16x16x32_bf16 v[56:59], v[154:157], v[78:81], v[56:59]
	v_mfma_f32_16x16x32_bf16 v[52:55], v[150:153], v[98:101], v[52:55]
	v_mfma_f32_16x16x32_bf16 v[48:51], v[154:157], v[94:97], v[48:51]
	v_mfma_f32_16x16x32_bf16 v[44:47], v[146:149], v[110:113], v[44:47]
	v_mfma_f32_16x16x32_bf16 v[40:43], v[158:161], v[116:119], v[40:43]
	s_waitcnt lgkmcnt(0)
	v_mfma_f32_16x16x32_bf16 v[36:39], v[150:153], v[194:197], v[36:39]
	v_mfma_f32_16x16x32_bf16 v[32:35], v[154:157], v[186:189], v[32:35]
	v_mfma_f32_16x16x32_bf16 v[198:201], v[158:161], v[82:85], v[56:59]
	v_mfma_f32_16x16x32_bf16 v[202:205], v[158:161], v[98:101], v[48:51]
	v_mfma_f32_16x16x32_bf16 v[206:209], v[150:153], v[116:119], v[44:47]
	v_mfma_f32_16x16x32_bf16 v[146:149], v[158:161], v[194:197], v[32:35]
	s_setprio 0
	s_setprio 1
	v_mfma_f32_16x16x32_bf16 v[24:27], v[170:173], v[78:81], v[24:27]
	v_mfma_f32_16x16x32_bf16 v[20:23], v[162:165], v[94:97], v[20:23]
	v_mfma_f32_16x16x32_bf16 v[8:11], v[170:173], v[110:113], v[8:11]
	v_mfma_f32_16x16x32_bf16 v[4:7], v[162:165], v[186:189], v[4:7]
	v_mfma_f32_16x16x32_bf16 v[28:31], v[162:165], v[78:81], v[28:31]
	v_mfma_f32_16x16x32_bf16 v[24:27], v[174:177], v[82:85], v[24:27]
	v_mfma_f32_16x16x32_bf16 v[20:23], v[166:169], v[98:101], v[20:23]
	v_mfma_f32_16x16x32_bf16 v[16:19], v[170:173], v[94:97], v[16:19]
	v_mfma_f32_16x16x32_bf16 v[12:15], v[162:165], v[110:113], v[12:15]
	v_mfma_f32_16x16x32_bf16 v[8:11], v[174:177], v[116:119], v[8:11]
	v_mfma_f32_16x16x32_bf16 v[4:7], v[166:169], v[194:197], v[4:7]
	v_mfma_f32_16x16x32_bf16 v[0:3], v[170:173], v[186:189], v[0:3]
	v_mfma_f32_16x16x32_bf16 v[150:153], v[166:169], v[82:85], v[28:31]
	v_mfma_f32_16x16x32_bf16 v[154:157], v[174:177], v[98:101], v[16:19]
	v_mfma_f32_16x16x32_bf16 v[158:161], v[166:169], v[116:119], v[12:15]
	v_mfma_f32_16x16x32_bf16 v[162:165], v[174:177], v[194:197], v[0:3]
	s_setprio 0
	s_barrier
	s_nop 1
	ds_read_b128 v[0:3], v143
	ds_read_b128 v[12:15], v143 offset:1024
	ds_read_b128 v[166:169], v143 offset:2048
	ds_read_b128 v[170:173], v143 offset:3072
	ds_read_b128 v[174:177], v144
	ds_read_b128 v[186:189], v144 offset:1024
	ds_read_b128 v[194:197], v144 offset:2048
	ds_read_b128 v[142:145], v144 offset:3072
	ds_read_b128 v[16:19], v135 offset:32768
	ds_read_b128 v[28:31], v135 offset:33792
	ds_read_b128 v[32:35], v135 offset:34816
	ds_read_b128 v[44:47], v135 offset:35840
	ds_read_b128 v[48:51], v135 offset:36864
	ds_read_b128 v[210:213], v135 offset:37888
	ds_read_b128 v[230:233], v135 offset:38912
	ds_read_b128 v[244:247], v135 offset:39936
	s_nop 4
	s_mov_b32 s2, m0
	s_mov_b32 m0, s46
	s_nop 0
	global_load_lds_dwordx4 v234, s[6:7]
	s_mov_b32 m0, s2
	s_nop 0
	s_nop 4
	s_mov_b32 s2, m0
	s_mov_b32 m0, s47
	s_nop 0
	global_load_lds_dwordx4 v235, s[6:7]
	s_mov_b32 m0, s2
	s_waitcnt vmcnt(8)
	s_waitcnt lgkmcnt(0)
	s_barrier
	s_setprio 1
	s_waitcnt lgkmcnt(0)
	v_mfma_f32_16x16x32_bf16 v[56:59], v[0:3], v[16:19], v[128:131]
	s_waitcnt lgkmcnt(6)
	v_mfma_f32_16x16x32_bf16 v[128:131], v[12:15], v[28:31], v[56:59]
	v_mfma_f32_16x16x32_bf16 v[56:59], v[166:169], v[16:19], v[124:127]
	v_mfma_f32_16x16x32_bf16 v[116:119], v[170:173], v[28:31], v[56:59]
	s_waitcnt lgkmcnt(5)
	v_mfma_f32_16x16x32_bf16 v[56:59], v[0:3], v[32:35], v[120:123]
	s_waitcnt lgkmcnt(4)
	v_mfma_f32_16x16x32_bf16 v[110:113], v[12:15], v[44:47], v[56:59]
	v_mfma_f32_16x16x32_bf16 v[56:59], v[166:169], v[32:35], v[214:217]
	v_mfma_f32_16x16x32_bf16 v[98:101], v[170:173], v[44:47], v[56:59]
	s_waitcnt lgkmcnt(3)
	v_mfma_f32_16x16x32_bf16 v[56:59], v[0:3], v[48:51], v[218:221]
	s_waitcnt lgkmcnt(2)
	v_mfma_f32_16x16x32_bf16 v[94:97], v[12:15], v[210:213], v[56:59]
	v_mfma_f32_16x16x32_bf16 v[56:59], v[166:169], v[48:51], v[106:109]
	v_mfma_f32_16x16x32_bf16 v[82:85], v[170:173], v[210:213], v[56:59]
	s_waitcnt lgkmcnt(1)
	v_mfma_f32_16x16x32_bf16 v[56:59], v[0:3], v[230:233], v[102:105]
	s_waitcnt lgkmcnt(0)
	v_mfma_f32_16x16x32_bf16 v[78:81], v[12:15], v[244:247], v[56:59]
	v_mfma_f32_16x16x32_bf16 v[56:59], v[166:169], v[230:233], v[222:225]
	v_mfma_f32_16x16x32_bf16 v[56:59], v[170:173], v[244:247], v[56:59]
	s_setprio 0
	s_setprio 1
	v_mfma_f32_16x16x32_bf16 v[102:105], v[174:177], v[16:19], v[226:229]
	v_mfma_f32_16x16x32_bf16 v[16:19], v[194:197], v[16:19], v[90:93]
	v_mfma_f32_16x16x32_bf16 v[120:123], v[142:145], v[28:31], v[16:19]
	v_mfma_f32_16x16x32_bf16 v[16:19], v[174:177], v[32:35], v[86:89]
	v_mfma_f32_16x16x32_bf16 v[106:109], v[186:189], v[44:47], v[16:19]
	v_mfma_f32_16x16x32_bf16 v[16:19], v[194:197], v[32:35], v[178:181]
	v_mfma_f32_16x16x32_bf16 v[124:127], v[186:189], v[28:31], v[102:105]
	v_mfma_f32_16x16x32_bf16 v[102:105], v[142:145], v[44:47], v[16:19]
	v_mfma_f32_16x16x32_bf16 v[16:19], v[174:177], v[48:51], v[182:185]
	v_mfma_f32_16x16x32_bf16 v[90:93], v[186:189], v[210:213], v[16:19]
	v_mfma_f32_16x16x32_bf16 v[16:19], v[194:197], v[48:51], v[74:77]
	v_mfma_f32_16x16x32_bf16 v[86:89], v[142:145], v[210:213], v[16:19]
	v_mfma_f32_16x16x32_bf16 v[16:19], v[174:177], v[230:233], v[70:73]
	v_mfma_f32_16x16x32_bf16 v[74:77], v[186:189], v[244:247], v[16:19]
	v_mfma_f32_16x16x32_bf16 v[16:19], v[194:197], v[230:233], v[66:69]
	v_mfma_f32_16x16x32_bf16 v[70:73], v[142:145], v[244:247], v[16:19]
	s_setprio 0
	s_barrier
	ds_read_b128 v[178:181], v135 offset:49152
	ds_read_b128 v[182:185], v135 offset:50176
	ds_read_b128 v[210:213], v135 offset:51200
	ds_read_b128 v[214:217], v135 offset:52224
	ds_read_b128 v[218:221], v135 offset:53248
	ds_read_b128 v[222:225], v135 offset:54272
	ds_read_b128 v[226:229], v135 offset:55296
	ds_read_b128 v[230:233], v135 offset:56320
	s_add_u32 s2, s22, 0x80
	s_addc_u32 s3, s23, 0
	s_nop 4
	s_mov_b32 s4, m0
	s_mov_b32 m0, s51
	s_nop 0
	global_load_lds_dwordx4 v65, s[2:3]
	s_mov_b32 m0, s4
	s_nop 0
	s_nop 4
	s_mov_b32 s4, m0
	s_mov_b32 m0, s52
	s_nop 0
	global_load_lds_dwordx4 v114, s[2:3]
	s_mov_b32 m0, s4
	s_add_u32 s2, s22, 0x40080
	s_addc_u32 s3, s23, 0
	s_nop 4
	s_mov_b32 s4, m0
	s_mov_b32 m0, s55
	s_nop 0
	global_load_lds_dwordx4 v65, s[2:3]
	s_mov_b32 m0, s4
	s_nop 0
	s_nop 4
	s_mov_b32 s4, m0
	s_mov_b32 m0, s56
	s_nop 0
	global_load_lds_dwordx4 v114, s[2:3]
	s_mov_b32 m0, s4
	s_nop 4
	s_mov_b32 s2, m0
	s_mov_b32 m0, s53
	s_nop 0
	global_load_lds_dwordx4 v190, s[14:15]
	s_mov_b32 m0, s2
	s_nop 0
	s_nop 4
	s_mov_b32 s2, m0
	s_mov_b32 m0, s54
	s_nop 0
	global_load_lds_dwordx4 v191, s[14:15]
	s_mov_b32 m0, s2
	s_waitcnt vmcnt(8)
	s_waitcnt lgkmcnt(0)
	s_barrier
	s_setprio 1
	s_waitcnt lgkmcnt(0)
	v_mfma_f32_16x16x32_bf16 v[16:19], v[0:3], v[178:181], v[60:63]
	s_waitcnt lgkmcnt(6)
	v_mfma_f32_16x16x32_bf16 v[66:69], v[12:15], v[182:185], v[16:19]
	v_mfma_f32_16x16x32_bf16 v[16:19], v[166:169], v[178:181], v[198:201]
	v_mfma_f32_16x16x32_bf16 v[48:51], v[170:173], v[182:185], v[16:19]
	s_waitcnt lgkmcnt(5)
	v_mfma_f32_16x16x32_bf16 v[16:19], v[0:3], v[210:213], v[52:55]
	s_waitcnt lgkmcnt(4)
	v_mfma_f32_16x16x32_bf16 v[44:47], v[12:15], v[214:217], v[16:19]
	v_mfma_f32_16x16x32_bf16 v[16:19], v[166:169], v[210:213], v[202:205]
	v_mfma_f32_16x16x32_bf16 v[32:35], v[170:173], v[214:217], v[16:19]
	s_waitcnt lgkmcnt(3)
	v_mfma_f32_16x16x32_bf16 v[16:19], v[0:3], v[218:221], v[206:209]
	s_waitcnt lgkmcnt(1)
	v_mfma_f32_16x16x32_bf16 v[0:3], v[0:3], v[226:229], v[36:39]
	v_mfma_f32_16x16x32_bf16 v[28:31], v[12:15], v[222:225], v[16:19]
	v_mfma_f32_16x16x32_bf16 v[16:19], v[166:169], v[218:221], v[40:43]
	s_waitcnt lgkmcnt(0)
	v_mfma_f32_16x16x32_bf16 v[12:15], v[12:15], v[230:233], v[0:3]
	v_mfma_f32_16x16x32_bf16 v[0:3], v[166:169], v[226:229], v[146:149]
	v_mfma_f32_16x16x32_bf16 v[16:19], v[170:173], v[222:225], v[16:19]
	v_mfma_f32_16x16x32_bf16 v[0:3], v[170:173], v[230:233], v[0:3]
	s_setprio 0
	s_setprio 1
	v_mfma_f32_16x16x32_bf16 v[20:23], v[174:177], v[210:213], v[20:23]
	v_mfma_f32_16x16x32_bf16 v[36:39], v[174:177], v[178:181], v[150:153]
	v_mfma_f32_16x16x32_bf16 v[40:43], v[186:189], v[214:217], v[20:23]
	v_mfma_f32_16x16x32_bf16 v[20:23], v[194:197], v[210:213], v[154:157]
	v_mfma_f32_16x16x32_bf16 v[60:63], v[186:189], v[182:185], v[36:39]
	v_mfma_f32_16x16x32_bf16 v[24:27], v[194:197], v[178:181], v[24:27]
	v_mfma_f32_16x16x32_bf16 v[36:39], v[142:145], v[214:217], v[20:23]
	v_mfma_f32_16x16x32_bf16 v[20:23], v[174:177], v[218:221], v[158:161]
	v_mfma_f32_16x16x32_bf16 v[8:11], v[194:197], v[218:221], v[8:11]
	v_mfma_f32_16x16x32_bf16 v[4:7], v[174:177], v[226:229], v[4:7]
	v_mfma_f32_16x16x32_bf16 v[52:55], v[142:145], v[182:185], v[24:27]
	v_mfma_f32_16x16x32_bf16 v[24:27], v[186:189], v[222:225], v[20:23]
	v_mfma_f32_16x16x32_bf16 v[20:23], v[142:145], v[222:225], v[8:11]
	v_mfma_f32_16x16x32_bf16 v[8:11], v[186:189], v[230:233], v[4:7]
	v_mfma_f32_16x16x32_bf16 v[4:7], v[194:197], v[226:229], v[162:165]
	v_mfma_f32_16x16x32_bf16 v[4:7], v[142:145], v[230:233], v[4:7]
	s_setprio 0
	s_barrier
	s_andn2_b64 vcc, exec, s[16:17]
	s_cbranch_vccnz .LBB0_1428
	s_barrier

.LBB0_1505:
	v_mov_b32_e32 v0, 0
	s_mov_b32 s13, -2
	s_mov_b64 s[18:19], 0
	v_mov_b32_e32 v1, v0
	v_mov_b64_e32 v[2:3], v[0:1]
	v_mov_b64_e32 v[4:5], v[0:1]
	v_mov_b64_e32 v[6:7], v[0:1]
	v_mov_b64_e32 v[8:9], v[0:1]
	v_mov_b64_e32 v[10:11], v[0:1]
	v_mov_b64_e32 v[12:13], v[0:1]
	v_mov_b64_e32 v[14:15], v[0:1]
	v_mov_b64_e32 v[16:17], v[0:1]
	v_mov_b64_e32 v[18:19], v[0:1]
	v_mov_b64_e32 v[20:21], v[0:1]
	v_mov_b64_e32 v[22:23], v[0:1]
	v_mov_b64_e32 v[24:25], v[0:1]
	v_mov_b64_e32 v[26:27], v[0:1]
	s_waitcnt lgkmcnt(0)
	v_mov_b64_e32 v[28:29], v[0:1]
	v_mov_b64_e32 v[30:31], v[0:1]
	v_mov_b64_e32 v[32:33], v[0:1]
	v_mov_b64_e32 v[34:35], v[0:1]
	v_mov_b64_e32 v[36:37], v[0:1]
	v_mov_b64_e32 v[38:39], v[0:1]
	v_mov_b64_e32 v[40:41], v[0:1]
	v_mov_b64_e32 v[42:43], v[0:1]
	v_mov_b64_e32 v[44:45], v[0:1]
	v_mov_b64_e32 v[46:47], v[0:1]
	v_mov_b64_e32 v[48:49], v[0:1]
	v_mov_b64_e32 v[50:51], v[0:1]
	v_mov_b64_e32 v[52:53], v[0:1]
	v_mov_b64_e32 v[54:55], v[0:1]
	v_mov_b64_e32 v[56:57], v[0:1]
	v_mov_b64_e32 v[58:59], v[0:1]
	v_mov_b64_e32 v[60:61], v[0:1]
	v_mov_b64_e32 v[62:63], v[0:1]
	v_mov_b64_e32 v[66:67], v[0:1]
	v_mov_b64_e32 v[68:69], v[0:1]
	v_mov_b64_e32 v[70:71], v[0:1]
	v_mov_b64_e32 v[72:73], v[0:1]
	v_mov_b64_e32 v[74:75], v[0:1]
	v_mov_b64_e32 v[76:77], v[0:1]
	v_mov_b64_e32 v[78:79], v[0:1]
	v_mov_b64_e32 v[80:81], v[0:1]
	v_mov_b64_e32 v[82:83], v[0:1]
	v_mov_b64_e32 v[84:85], v[0:1]
	v_mov_b64_e32 v[86:87], v[0:1]
	v_mov_b64_e32 v[88:89], v[0:1]
	v_mov_b64_e32 v[90:91], v[0:1]
	v_mov_b64_e32 v[92:93], v[0:1]
	v_mov_b64_e32 v[94:95], v[0:1]
	v_mov_b64_e32 v[96:97], v[0:1]
	v_mov_b64_e32 v[98:99], v[0:1]
	v_mov_b64_e32 v[100:101], v[0:1]
	v_mov_b64_e32 v[102:103], v[0:1]
	v_mov_b64_e32 v[104:105], v[0:1]
	v_mov_b64_e32 v[106:107], v[0:1]
	v_mov_b64_e32 v[108:109], v[0:1]
	v_mov_b64_e32 v[110:111], v[0:1]
	v_mov_b64_e32 v[112:113], v[0:1]
	v_mov_b64_e32 v[116:117], v[0:1]
	v_mov_b64_e32 v[118:119], v[0:1]
	v_mov_b64_e32 v[120:121], v[0:1]
	v_mov_b64_e32 v[122:123], v[0:1]
	v_mov_b64_e32 v[124:125], v[0:1]
	v_mov_b64_e32 v[126:127], v[0:1]
	v_mov_b64_e32 v[128:129], v[0:1]
	v_mov_b64_e32 v[130:131], v[0:1]
